# v31 + bf16 GEMM K-loops read next B0 fragment one phase early into spare VGPRs (LDS reads 8/4/8/4 per phase instead of 12/4/8/0)
# speedup vs baseline: 1.0025x; 1.0025x over previous
.LBB0_483:
	v_mov_b64_e32 v[0:1], 0xd8
	v_cmp_lt_i64_e32 vcc, s[6:7], v[0:1]
	s_mul_i32 s38, s37, 0x300000
	s_and_b64 s[6:7], vcc, exec
	s_cselect_b32 s6, s38, s11
	s_lshl_b32 s39, s36, 18
	s_and_b64 s[42:43], vcc, exec
	v_mov_b32_e32 v0, 0
	s_cselect_b32 s7, s39, s10
	s_add_i32 s42, s11, 0x180080
	s_add_i32 s43, s10, 0x100
	s_mov_b32 s44, -2
	v_mov_b32_e32 v1, v0
	v_mov_b32_e32 v2, v0
	v_mov_b32_e32 v3, v0
	v_mov_b32_e32 v4, v0
	v_mov_b32_e32 v5, v0
	v_mov_b32_e32 v6, v0
	v_mov_b32_e32 v7, v0
	v_mov_b32_e32 v8, v0
	v_mov_b32_e32 v9, v0
	v_mov_b32_e32 v10, v0
	v_mov_b32_e32 v11, v0
	v_mov_b32_e32 v12, v0
	v_mov_b32_e32 v13, v0
	v_mov_b32_e32 v14, v0
	v_mov_b32_e32 v15, v0
	v_mov_b32_e32 v24, v0
	v_mov_b32_e32 v25, v0
	v_mov_b32_e32 v26, v0
	v_mov_b32_e32 v27, v0
	v_mov_b32_e32 v28, v0
	v_mov_b32_e32 v29, v0
	v_mov_b32_e32 v30, v0
	v_mov_b32_e32 v31, v0
	v_mov_b32_e32 v40, v0
	v_mov_b32_e32 v41, v0
	v_mov_b32_e32 v42, v0
	v_mov_b32_e32 v43, v0
	v_mov_b32_e32 v44, v0
	v_mov_b32_e32 v45, v0
	v_mov_b32_e32 v46, v0
	v_mov_b32_e32 v47, v0
	v_mov_b32_e32 v16, v0
	v_mov_b32_e32 v17, v0
	v_mov_b32_e32 v18, v0
	v_mov_b32_e32 v19, v0
	v_mov_b32_e32 v20, v0
	v_mov_b32_e32 v21, v0
	v_mov_b32_e32 v22, v0
	v_mov_b32_e32 v23, v0
	v_mov_b32_e32 v32, v0
	v_mov_b32_e32 v33, v0
	v_mov_b32_e32 v34, v0
	v_mov_b32_e32 v35, v0
	v_mov_b32_e32 v36, v0
	v_mov_b32_e32 v37, v0
	v_mov_b32_e32 v38, v0
	v_mov_b32_e32 v39, v0
	v_mov_b32_e32 v48, v0
	v_mov_b32_e32 v49, v0
	v_mov_b32_e32 v50, v0
	v_mov_b32_e32 v51, v0
	v_mov_b32_e32 v52, v0
	v_mov_b32_e32 v53, v0
	v_mov_b32_e32 v54, v0
	v_mov_b32_e32 v55, v0
	v_mov_b32_e32 v56, v0
	v_mov_b32_e32 v57, v0
	v_mov_b32_e32 v58, v0
	v_mov_b32_e32 v59, v0
	v_mov_b32_e32 v60, v0
	v_mov_b32_e32 v61, v0
	v_mov_b32_e32 v62, v0
	v_mov_b32_e32 v63, v0
	v_mov_b32_e32 v64, v0
	v_mov_b32_e32 v65, v0
	v_mov_b32_e32 v66, v0
	v_mov_b32_e32 v67, v0
	v_mov_b32_e32 v68, v0
	v_mov_b32_e32 v69, v0
	v_mov_b32_e32 v70, v0
	v_mov_b32_e32 v71, v0
	v_mov_b32_e32 v72, v0
	v_mov_b32_e32 v73, v0
	v_mov_b32_e32 v74, v0
	v_mov_b32_e32 v75, v0
	v_mov_b32_e32 v76, v0
	v_mov_b32_e32 v77, v0
	v_mov_b32_e32 v78, v0
	v_mov_b32_e32 v79, v0
	v_mov_b32_e32 v88, v0
	v_mov_b32_e32 v89, v0
	v_mov_b32_e32 v90, v0
	v_mov_b32_e32 v91, v0
	v_mov_b32_e32 v92, v0
	v_mov_b32_e32 v93, v0
	v_mov_b32_e32 v94, v0
	v_mov_b32_e32 v95, v0
	v_mov_b32_e32 v106, v0
	v_mov_b32_e32 v107, v0
	v_mov_b32_e32 v108, v0
	v_mov_b32_e32 v109, v0
	v_mov_b32_e32 v110, v0
	v_mov_b32_e32 v111, v0
	v_mov_b32_e32 v112, v0
	v_mov_b32_e32 v113, v0
	v_mov_b32_e32 v80, v0
	v_mov_b32_e32 v81, v0
	v_mov_b32_e32 v82, v0
	v_mov_b32_e32 v83, v0
	v_mov_b32_e32 v84, v0
	v_mov_b32_e32 v85, v0
	v_mov_b32_e32 v86, v0
	v_mov_b32_e32 v87, v0
	v_mov_b32_e32 v98, v0
	v_mov_b32_e32 v99, v0
	v_mov_b32_e32 v100, v0
	v_mov_b32_e32 v101, v0
	v_mov_b32_e32 v102, v0
	v_mov_b32_e32 v103, v0
	v_mov_b32_e32 v104, v0
	v_mov_b32_e32 v105, v0
	v_mov_b32_e32 v114, v0
	v_mov_b32_e32 v115, v0
	v_mov_b32_e32 v116, v0
	v_mov_b32_e32 v117, v0
	v_mov_b32_e32 v118, v0
	v_mov_b32_e32 v119, v0
	v_mov_b32_e32 v120, v0
	v_mov_b32_e32 v121, v0
	v_mov_b32_e32 v122, v0
	v_mov_b32_e32 v123, v0
	v_mov_b32_e32 v124, v0
	v_mov_b32_e32 v125, v0
	v_mov_b32_e32 v126, v0
	v_mov_b32_e32 v127, v0
	v_mov_b32_e32 v128, v0
	v_mov_b32_e32 v129, v0
	ds_read_b128 v[220:223], v133
	ds_read_b128 v[224:227], v133 offset:1024
	ds_read_b128 v[228:231], v133 offset:2048
	ds_read_b128 v[232:235], v133 offset:3072
.LBB0_484:
	s_add_i32 s10, s42, 0xffe80080
	s_cmp_eq_u32 s44, 4
	s_cselect_b32 s47, s6, s10
	s_cselect_b32 s45, s7, s43
	s_or_b32 s46, s47, 0x80
	s_mov_b32 m0, s31
	ds_read_b128 v[152:155], v134
	ds_read_b128 v[156:159], v134 offset:1024
	ds_read_b128 v[160:163], v134 offset:2048
	ds_read_b128 v[164:167], v134 offset:3072
	ds_read_b128 v[168:171], v134 offset:4096
	ds_read_b128 v[172:175], v134 offset:5120
	ds_read_b128 v[176:179], v134 offset:6144
	ds_read_b128 v[180:183], v134 offset:7168
	buffer_load_dwordx4 v96, s[72:75], s42 offen lds
	s_mov_b32 m0, s34
	s_nop 0
	buffer_load_dwordx4 v131, s[72:75], s42 offen lds
	s_waitcnt lgkmcnt(8)
	s_waitcnt vmcnt(10)
	s_barrier
	s_waitcnt lgkmcnt(0)
	s_setprio 1
	s_waitcnt lgkmcnt(7)
	v_mfma_f32_16x16x32_bf16 v[126:129], v[220:223], v[152:155], v[126:129]
	v_mfma_f32_16x16x32_bf16 v[122:125], v[228:231], v[152:155], v[122:125]
	s_waitcnt lgkmcnt(5)
	v_mfma_f32_16x16x32_bf16 v[118:121], v[220:223], v[160:163], v[118:121]
	v_mfma_f32_16x16x32_bf16 v[114:117], v[228:231], v[160:163], v[114:117]
	s_waitcnt lgkmcnt(3)
	v_mfma_f32_16x16x32_bf16 v[102:105], v[220:223], v[168:171], v[102:105]
	v_mfma_f32_16x16x32_bf16 v[98:101], v[228:231], v[168:171], v[98:101]
	s_waitcnt lgkmcnt(1)
	v_mfma_f32_16x16x32_bf16 v[84:87], v[220:223], v[176:179], v[84:87]
	v_mfma_f32_16x16x32_bf16 v[80:83], v[228:231], v[176:179], v[80:83]
	v_mfma_f32_16x16x32_bf16 v[126:129], v[224:227], v[156:159], v[126:129]
	v_mfma_f32_16x16x32_bf16 v[122:125], v[232:235], v[156:159], v[122:125]
	v_mfma_f32_16x16x32_bf16 v[118:121], v[224:227], v[164:167], v[118:121]
	v_mfma_f32_16x16x32_bf16 v[114:117], v[232:235], v[164:167], v[114:117]
	v_mfma_f32_16x16x32_bf16 v[102:105], v[224:227], v[172:175], v[102:105]
	v_mfma_f32_16x16x32_bf16 v[98:101], v[232:235], v[172:175], v[98:101]
	s_waitcnt lgkmcnt(0)
	v_mfma_f32_16x16x32_bf16 v[84:87], v[224:227], v[180:183], v[84:87]
	v_mfma_f32_16x16x32_bf16 v[80:83], v[232:235], v[180:183], v[80:83]
	s_setprio 0
	s_barrier
	s_mov_b32 s10, s74
	s_mov_b32 s11, s75
	s_mov_b32 m0, s16
	ds_read_b128 v[184:187], v133 offset:16384
	ds_read_b128 v[188:191], v133 offset:17408
	ds_read_b128 v[192:195], v133 offset:18432
	ds_read_b128 v[196:199], v133 offset:19456
	buffer_load_dwordx4 v130, s[8:11], s45 offen lds
	s_mov_b32 m0, s17
	s_nop 0
	buffer_load_dwordx4 v132, s[8:11], s45 offen lds
	s_waitcnt vmcnt(10)
	s_barrier
	s_waitcnt lgkmcnt(0)
	s_setprio 1
	s_waitcnt lgkmcnt(3)
	v_mfma_f32_16x16x32_bf16 v[110:113], v[184:187], v[152:155], v[110:113]
	s_waitcnt lgkmcnt(1)
	v_mfma_f32_16x16x32_bf16 v[106:109], v[192:195], v[152:155], v[106:109]
	v_mfma_f32_16x16x32_bf16 v[92:95], v[184:187], v[160:163], v[92:95]
	v_mfma_f32_16x16x32_bf16 v[88:91], v[192:195], v[160:163], v[88:91]
	v_mfma_f32_16x16x32_bf16 v[76:79], v[184:187], v[168:171], v[76:79]
	v_mfma_f32_16x16x32_bf16 v[72:75], v[192:195], v[168:171], v[72:75]
	v_mfma_f32_16x16x32_bf16 v[68:71], v[184:187], v[176:179], v[68:71]
	v_mfma_f32_16x16x32_bf16 v[64:67], v[192:195], v[176:179], v[64:67]
	v_mfma_f32_16x16x32_bf16 v[110:113], v[188:191], v[156:159], v[110:113]
	s_waitcnt lgkmcnt(0)
	v_mfma_f32_16x16x32_bf16 v[106:109], v[196:199], v[156:159], v[106:109]
	v_mfma_f32_16x16x32_bf16 v[92:95], v[188:191], v[164:167], v[92:95]
	v_mfma_f32_16x16x32_bf16 v[88:91], v[196:199], v[164:167], v[88:91]
	v_mfma_f32_16x16x32_bf16 v[76:79], v[188:191], v[172:175], v[76:79]
	v_mfma_f32_16x16x32_bf16 v[72:75], v[196:199], v[172:175], v[72:75]
	v_mfma_f32_16x16x32_bf16 v[68:71], v[188:191], v[180:183], v[68:71]
	v_mfma_f32_16x16x32_bf16 v[64:67], v[196:199], v[180:183], v[64:67]
	s_setprio 0
	s_mov_b32 m0, s15
	s_barrier
	ds_read_b128 v[152:155], v134 offset:16384
	ds_read_b128 v[156:159], v134 offset:17408
	ds_read_b128 v[160:163], v134 offset:18432
	ds_read_b128 v[164:167], v134 offset:19456
	ds_read_b128 v[168:171], v134 offset:20480
	ds_read_b128 v[172:175], v134 offset:21504
	ds_read_b128 v[176:179], v134 offset:22528
	ds_read_b128 v[180:183], v134 offset:23552
	buffer_load_dwordx4 v96, s[72:75], s47 offen lds
	s_mov_b32 m0, s18
	s_nop 0
	buffer_load_dwordx4 v131, s[72:75], s47 offen lds
	s_waitcnt vmcnt(10)
	s_barrier
	s_waitcnt lgkmcnt(0)
	s_setprio 1
	s_waitcnt lgkmcnt(7)
	v_mfma_f32_16x16x32_bf16 v[60:63], v[220:223], v[152:155], v[60:63]
	v_mfma_f32_16x16x32_bf16 v[56:59], v[228:231], v[152:155], v[56:59]
	s_waitcnt lgkmcnt(5)
	v_mfma_f32_16x16x32_bf16 v[52:55], v[220:223], v[160:163], v[52:55]
	v_mfma_f32_16x16x32_bf16 v[48:51], v[228:231], v[160:163], v[48:51]
	s_waitcnt lgkmcnt(3)
	v_mfma_f32_16x16x32_bf16 v[36:39], v[220:223], v[168:171], v[36:39]
	v_mfma_f32_16x16x32_bf16 v[32:35], v[228:231], v[168:171], v[32:35]
	s_waitcnt lgkmcnt(1)
	v_mfma_f32_16x16x32_bf16 v[20:23], v[220:223], v[176:179], v[20:23]
	v_mfma_f32_16x16x32_bf16 v[16:19], v[228:231], v[176:179], v[16:19]
	v_mfma_f32_16x16x32_bf16 v[60:63], v[224:227], v[156:159], v[60:63]
	v_mfma_f32_16x16x32_bf16 v[56:59], v[232:235], v[156:159], v[56:59]
	v_mfma_f32_16x16x32_bf16 v[52:55], v[224:227], v[164:167], v[52:55]
	v_mfma_f32_16x16x32_bf16 v[48:51], v[232:235], v[164:167], v[48:51]
	v_mfma_f32_16x16x32_bf16 v[36:39], v[224:227], v[172:175], v[36:39]
	v_mfma_f32_16x16x32_bf16 v[32:35], v[232:235], v[172:175], v[32:35]
	s_waitcnt lgkmcnt(0)
	v_mfma_f32_16x16x32_bf16 v[20:23], v[224:227], v[180:183], v[20:23]
	v_mfma_f32_16x16x32_bf16 v[16:19], v[232:235], v[180:183], v[16:19]
	s_setprio 0
	s_barrier
	ds_read_b128 v[220:223], v133 offset:32768
	ds_read_b128 v[224:227], v133 offset:33792
	ds_read_b128 v[228:231], v133 offset:34816
	ds_read_b128 v[232:235], v133 offset:35840
	s_add_i32 s48, s45, 0x20000
	s_mov_b32 m0, s19
	s_nop 0
	buffer_load_dwordx4 v130, s[8:11], s48 offen lds
	s_mov_b32 m0, s20
	s_nop 0
	buffer_load_dwordx4 v132, s[8:11], s48 offen lds
	s_waitcnt vmcnt(10)
	s_barrier
	s_setprio 1
	v_mfma_f32_16x16x32_bf16 v[44:47], v[184:187], v[152:155], v[44:47]
	v_mfma_f32_16x16x32_bf16 v[40:43], v[192:195], v[152:155], v[40:43]
	v_mfma_f32_16x16x32_bf16 v[28:31], v[184:187], v[160:163], v[28:31]
	v_mfma_f32_16x16x32_bf16 v[24:27], v[192:195], v[160:163], v[24:27]
	v_mfma_f32_16x16x32_bf16 v[12:15], v[184:187], v[168:171], v[12:15]
	v_mfma_f32_16x16x32_bf16 v[8:11], v[192:195], v[168:171], v[8:11]
	v_mfma_f32_16x16x32_bf16 v[4:7], v[184:187], v[176:179], v[4:7]
	v_mfma_f32_16x16x32_bf16 v[0:3], v[192:195], v[176:179], v[0:3]
	v_mfma_f32_16x16x32_bf16 v[44:47], v[188:191], v[156:159], v[44:47]
	v_mfma_f32_16x16x32_bf16 v[40:43], v[196:199], v[156:159], v[40:43]
	v_mfma_f32_16x16x32_bf16 v[28:31], v[188:191], v[164:167], v[28:31]
	v_mfma_f32_16x16x32_bf16 v[24:27], v[196:199], v[164:167], v[24:27]
	v_mfma_f32_16x16x32_bf16 v[12:15], v[188:191], v[172:175], v[12:15]
	v_mfma_f32_16x16x32_bf16 v[8:11], v[196:199], v[172:175], v[8:11]
	v_mfma_f32_16x16x32_bf16 v[4:7], v[188:191], v[180:183], v[4:7]
	v_mfma_f32_16x16x32_bf16 v[0:3], v[196:199], v[180:183], v[0:3]
	s_setprio 0
	s_barrier
	s_add_i32 s47, s47, 0x180000
	s_mov_b32 m0, s21
	ds_read_b128 v[152:155], v134 offset:32768
	ds_read_b128 v[156:159], v134 offset:33792
	ds_read_b128 v[160:163], v134 offset:34816
	ds_read_b128 v[164:167], v134 offset:35840
	ds_read_b128 v[168:171], v134 offset:36864
	ds_read_b128 v[172:175], v134 offset:37888
	ds_read_b128 v[176:179], v134 offset:38912
	ds_read_b128 v[180:183], v134 offset:39936
	buffer_load_dwordx4 v96, s[72:75], s47 offen lds
	s_mov_b32 m0, s22
	s_nop 0
	buffer_load_dwordx4 v131, s[72:75], s47 offen lds
	s_waitcnt lgkmcnt(8)
	s_waitcnt vmcnt(10)
	s_barrier
	s_waitcnt lgkmcnt(0)
	s_setprio 1
	s_waitcnt lgkmcnt(7)
	v_mfma_f32_16x16x32_bf16 v[126:129], v[220:223], v[152:155], v[126:129]
	v_mfma_f32_16x16x32_bf16 v[122:125], v[228:231], v[152:155], v[122:125]
	s_waitcnt lgkmcnt(5)
	v_mfma_f32_16x16x32_bf16 v[118:121], v[220:223], v[160:163], v[118:121]
	v_mfma_f32_16x16x32_bf16 v[114:117], v[228:231], v[160:163], v[114:117]
	s_waitcnt lgkmcnt(3)
	v_mfma_f32_16x16x32_bf16 v[102:105], v[220:223], v[168:171], v[102:105]
	v_mfma_f32_16x16x32_bf16 v[98:101], v[228:231], v[168:171], v[98:101]
	s_waitcnt lgkmcnt(1)
	v_mfma_f32_16x16x32_bf16 v[84:87], v[220:223], v[176:179], v[84:87]
	v_mfma_f32_16x16x32_bf16 v[80:83], v[228:231], v[176:179], v[80:83]
	v_mfma_f32_16x16x32_bf16 v[126:129], v[224:227], v[156:159], v[126:129]
	v_mfma_f32_16x16x32_bf16 v[122:125], v[232:235], v[156:159], v[122:125]
	v_mfma_f32_16x16x32_bf16 v[118:121], v[224:227], v[164:167], v[118:121]
	v_mfma_f32_16x16x32_bf16 v[114:117], v[232:235], v[164:167], v[114:117]
	v_mfma_f32_16x16x32_bf16 v[102:105], v[224:227], v[172:175], v[102:105]
	v_mfma_f32_16x16x32_bf16 v[98:101], v[232:235], v[172:175], v[98:101]
	s_waitcnt lgkmcnt(0)
	v_mfma_f32_16x16x32_bf16 v[84:87], v[224:227], v[180:183], v[84:87]
	v_mfma_f32_16x16x32_bf16 v[80:83], v[232:235], v[180:183], v[80:83]
	s_setprio 0
	s_barrier
	s_or_b32 s47, s45, 0x80
	s_mov_b32 m0, s25
	ds_read_b128 v[184:187], v133 offset:49152
	ds_read_b128 v[188:191], v133 offset:50176
	ds_read_b128 v[192:195], v133 offset:51200
	ds_read_b128 v[196:199], v133 offset:52224
	buffer_load_dwordx4 v130, s[8:11], s47 offen lds
	s_mov_b32 m0, s26
	s_nop 0
	buffer_load_dwordx4 v132, s[8:11], s47 offen lds
	s_waitcnt vmcnt(10)
	s_barrier
	s_waitcnt lgkmcnt(0)
	s_setprio 1
	s_waitcnt lgkmcnt(3)
	v_mfma_f32_16x16x32_bf16 v[110:113], v[184:187], v[152:155], v[110:113]
	s_waitcnt lgkmcnt(1)
	v_mfma_f32_16x16x32_bf16 v[106:109], v[192:195], v[152:155], v[106:109]
	v_mfma_f32_16x16x32_bf16 v[92:95], v[184:187], v[160:163], v[92:95]
	v_mfma_f32_16x16x32_bf16 v[88:91], v[192:195], v[160:163], v[88:91]
	v_mfma_f32_16x16x32_bf16 v[76:79], v[184:187], v[168:171], v[76:79]
	v_mfma_f32_16x16x32_bf16 v[72:75], v[192:195], v[168:171], v[72:75]
	v_mfma_f32_16x16x32_bf16 v[68:71], v[184:187], v[176:179], v[68:71]
	v_mfma_f32_16x16x32_bf16 v[64:67], v[192:195], v[176:179], v[64:67]
	v_mfma_f32_16x16x32_bf16 v[110:113], v[188:191], v[156:159], v[110:113]
	s_waitcnt lgkmcnt(0)
	v_mfma_f32_16x16x32_bf16 v[106:109], v[196:199], v[156:159], v[106:109]
	v_mfma_f32_16x16x32_bf16 v[92:95], v[188:191], v[164:167], v[92:95]
	v_mfma_f32_16x16x32_bf16 v[88:91], v[196:199], v[164:167], v[88:91]
	v_mfma_f32_16x16x32_bf16 v[76:79], v[188:191], v[172:175], v[76:79]
	v_mfma_f32_16x16x32_bf16 v[72:75], v[196:199], v[172:175], v[72:75]
	v_mfma_f32_16x16x32_bf16 v[68:71], v[188:191], v[180:183], v[68:71]
	v_mfma_f32_16x16x32_bf16 v[64:67], v[196:199], v[180:183], v[64:67]
	s_setprio 0
	s_mov_b32 m0, s27
	s_barrier
	ds_read_b128 v[152:155], v134 offset:49152
	ds_read_b128 v[156:159], v134 offset:50176
	ds_read_b128 v[160:163], v134 offset:51200
	ds_read_b128 v[164:167], v134 offset:52224
	ds_read_b128 v[168:171], v134 offset:53248
	ds_read_b128 v[172:175], v134 offset:54272
	ds_read_b128 v[176:179], v134 offset:55296
	ds_read_b128 v[180:183], v134 offset:56320
	buffer_load_dwordx4 v96, s[72:75], s46 offen lds
	s_mov_b32 m0, s28
	s_nop 0
	buffer_load_dwordx4 v131, s[72:75], s46 offen lds
	s_waitcnt vmcnt(10)
	s_barrier
	s_waitcnt lgkmcnt(0)
	s_setprio 1
	s_waitcnt lgkmcnt(7)
	v_mfma_f32_16x16x32_bf16 v[60:63], v[220:223], v[152:155], v[60:63]
	v_mfma_f32_16x16x32_bf16 v[56:59], v[228:231], v[152:155], v[56:59]
	s_waitcnt lgkmcnt(5)
	v_mfma_f32_16x16x32_bf16 v[52:55], v[220:223], v[160:163], v[52:55]
	v_mfma_f32_16x16x32_bf16 v[48:51], v[228:231], v[160:163], v[48:51]
	s_waitcnt lgkmcnt(3)
	v_mfma_f32_16x16x32_bf16 v[36:39], v[220:223], v[168:171], v[36:39]
	v_mfma_f32_16x16x32_bf16 v[32:35], v[228:231], v[168:171], v[32:35]
	s_waitcnt lgkmcnt(1)
	v_mfma_f32_16x16x32_bf16 v[20:23], v[220:223], v[176:179], v[20:23]
	v_mfma_f32_16x16x32_bf16 v[16:19], v[228:231], v[176:179], v[16:19]
	v_mfma_f32_16x16x32_bf16 v[60:63], v[224:227], v[156:159], v[60:63]
	v_mfma_f32_16x16x32_bf16 v[56:59], v[232:235], v[156:159], v[56:59]
	v_mfma_f32_16x16x32_bf16 v[52:55], v[224:227], v[164:167], v[52:55]
	v_mfma_f32_16x16x32_bf16 v[48:51], v[232:235], v[164:167], v[48:51]
	v_mfma_f32_16x16x32_bf16 v[36:39], v[224:227], v[172:175], v[36:39]
	v_mfma_f32_16x16x32_bf16 v[32:35], v[232:235], v[172:175], v[32:35]
	s_waitcnt lgkmcnt(0)
	v_mfma_f32_16x16x32_bf16 v[20:23], v[224:227], v[180:183], v[20:23]
	v_mfma_f32_16x16x32_bf16 v[16:19], v[232:235], v[180:183], v[16:19]
	s_setprio 0
	s_barrier
	ds_read_b128 v[220:223], v133
	ds_read_b128 v[224:227], v133 offset:1024
	ds_read_b128 v[228:231], v133 offset:2048
	ds_read_b128 v[232:235], v133 offset:3072
	s_add_i32 s45, s45, 0x20080
	s_mov_b32 m0, s29
	s_nop 0
	buffer_load_dwordx4 v130, s[8:11], s45 offen lds
	s_mov_b32 m0, s30
	s_nop 0
	buffer_load_dwordx4 v132, s[8:11], s45 offen lds
	s_waitcnt vmcnt(10)
	s_barrier
	s_setprio 1
	v_mfma_f32_16x16x32_bf16 v[44:47], v[184:187], v[152:155], v[44:47]
	v_mfma_f32_16x16x32_bf16 v[40:43], v[192:195], v[152:155], v[40:43]
	v_mfma_f32_16x16x32_bf16 v[28:31], v[184:187], v[160:163], v[28:31]
	v_mfma_f32_16x16x32_bf16 v[24:27], v[192:195], v[160:163], v[24:27]
	v_mfma_f32_16x16x32_bf16 v[12:15], v[184:187], v[168:171], v[12:15]
	v_mfma_f32_16x16x32_bf16 v[8:11], v[192:195], v[168:171], v[8:11]
	v_mfma_f32_16x16x32_bf16 v[4:7], v[184:187], v[176:179], v[4:7]
	v_mfma_f32_16x16x32_bf16 v[0:3], v[192:195], v[176:179], v[0:3]
	v_mfma_f32_16x16x32_bf16 v[44:47], v[188:191], v[156:159], v[44:47]
	v_mfma_f32_16x16x32_bf16 v[40:43], v[196:199], v[156:159], v[40:43]
	v_mfma_f32_16x16x32_bf16 v[28:31], v[188:191], v[164:167], v[28:31]
	v_mfma_f32_16x16x32_bf16 v[24:27], v[196:199], v[164:167], v[24:27]
	v_mfma_f32_16x16x32_bf16 v[12:15], v[188:191], v[172:175], v[12:15]
	v_mfma_f32_16x16x32_bf16 v[8:11], v[196:199], v[172:175], v[8:11]
	v_mfma_f32_16x16x32_bf16 v[4:7], v[188:191], v[180:183], v[4:7]
	v_mfma_f32_16x16x32_bf16 v[0:3], v[196:199], v[180:183], v[0:3]
	s_setprio 0
	s_add_i32 s44, s44, 2
	s_addk_i32 s42, 0x100
	s_addk_i32 s43, 0x100
	s_cmp_gt_u32 s44, 5
	s_barrier
	s_cbranch_scc0 .LBB0_484
	s_waitcnt lgkmcnt(0)
	s_getreg_b32 s6, hwreg(HW_REG_HW_ID, 0, 6)
	s_and_b32 s6, s6, 63
	s_lshl_b32 s6, s6, 2
	s_add_i32 s6, s6, 0
	s_add_i32 s6, s6, 0x20010
	v_mov_b32_e32 v135, s6
	ds_read_b32 v135, v135
	s_lshl_b32 s6, s41, 8
	s_mul_i32 s7, s41, 0x60000
	v_mbcnt_lo_u32_b32 v136, -1, 0
	v_mbcnt_hi_u32_b32 v136, -1, v136
	s_mul_hi_i32 s6, s6, 0x600
	s_waitcnt lgkmcnt(0)
	v_readfirstlane_b32 s10, v135
	v_and_b32_e32 v137, 15, v136
	v_cvt_pk_bf16_f32 v126, v126, v127
	v_lshl_or_b32 v135, s10, 6, v136
	s_add_u32 s10, s23, s7
	s_addc_u32 s11, s24, s6
	s_lshl_b32 s6, s40, 8
	s_ashr_i32 s7, s6, 31
	s_lshl_b64 s[6:7], s[6:7], 1
	s_add_u32 s6, s10, s6
	v_lshrrev_b32_e32 v136, 2, v135
	s_mov_b32 s10, 0x7fffc0
	v_and_or_b32 v136, v136, s10, v137
	v_cvt_pk_bf16_f32 v127, v128, v129
	v_cvt_pk_bf16_f32 v128, v122, v123
	v_mul_u32_u24_e32 v122, 0x600, v136
	s_movk_i32 s10, 0xf0
	s_addc_u32 s7, s11, s7
	v_and_or_b32 v122, v135, s10, v122
	v_cvt_pk_bf16_f32 v110, v110, v111
	v_cvt_pk_bf16_f32 v111, v112, v113
	v_cvt_pk_bf16_f32 v112, v106, v107
	v_cvt_pk_bf16_f32 v113, v108, v109
	v_cvt_pk_bf16_f32 v129, v124, v125
	global_store_dwordx4 v122, v[110:113], s[6:7] offset:256
	v_cvt_pk_bf16_f32 v106, v118, v119
	v_cvt_pk_bf16_f32 v107, v120, v121
	v_cvt_pk_bf16_f32 v108, v114, v115
	v_cvt_pk_bf16_f32 v109, v116, v117
	v_add_u32_e32 v110, 0x6000, v122
	v_cvt_pk_bf16_f32 v92, v92, v93
	v_cvt_pk_bf16_f32 v93, v94, v95
	v_cvt_pk_bf16_f32 v94, v88, v89
	v_cvt_pk_bf16_f32 v95, v90, v91
	v_add_u32_e32 v88, 0x6100, v122
	global_store_dwordx4 v122, v[126:129], s[6:7]
	global_store_dwordx4 v110, v[106:109], s[6:7]
	global_store_dwordx4 v88, v[92:95], s[6:7]
	v_cvt_pk_bf16_f32 v88, v102, v103
	v_cvt_pk_bf16_f32 v89, v104, v105
	v_cvt_pk_bf16_f32 v90, v98, v99
	v_cvt_pk_bf16_f32 v91, v100, v101
	v_add_u32_e32 v92, 0xc000, v122
	v_cvt_pk_bf16_f32 v76, v76, v77
	v_cvt_pk_bf16_f32 v77, v78, v79
	v_cvt_pk_bf16_f32 v78, v72, v73
	v_cvt_pk_bf16_f32 v79, v74, v75
	v_add_u32_e32 v72, 0xc100, v122
	global_store_dwordx4 v92, v[88:91], s[6:7]
	global_store_dwordx4 v72, v[76:79], s[6:7]
	v_cvt_pk_bf16_f32 v72, v84, v85
	v_cvt_pk_bf16_f32 v73, v86, v87
	v_cvt_pk_bf16_f32 v74, v80, v81
	v_cvt_pk_bf16_f32 v75, v82, v83
	v_add_u32_e32 v76, 0x12000, v122
	v_cvt_pk_bf16_f32 v68, v68, v69
	v_cvt_pk_bf16_f32 v69, v70, v71
	v_cvt_pk_bf16_f32 v70, v64, v65
	v_cvt_pk_bf16_f32 v71, v66, v67
	v_cvt_pk_bf16_f32 v60, v60, v61
	v_cvt_pk_bf16_f32 v61, v62, v63
	v_cvt_pk_bf16_f32 v62, v56, v57
	v_cvt_pk_bf16_f32 v63, v58, v59
	v_add_u32_e32 v56, 0x30000, v122
	v_cvt_pk_bf16_f32 v44, v44, v45
	v_cvt_pk_bf16_f32 v45, v46, v47
	v_cvt_pk_bf16_f32 v46, v40, v41
	v_cvt_pk_bf16_f32 v47, v42, v43
	v_add_u32_e32 v40, 0x30100, v122
	global_store_dwordx4 v76, v[72:75], s[6:7]
	global_store_dwordx4 v76, v[68:71], s[6:7] offset:256
	global_store_dwordx4 v56, v[60:63], s[6:7]
	global_store_dwordx4 v40, v[44:47], s[6:7]
	v_cvt_pk_bf16_f32 v28, v28, v29
	v_cvt_pk_bf16_f32 v29, v30, v31
	v_add_u32_e32 v44, 0x36000, v122
	v_cvt_pk_bf16_f32 v30, v24, v25
	v_cvt_pk_bf16_f32 v31, v26, v27
	v_cvt_pk_bf16_f32 v40, v52, v53
	v_cvt_pk_bf16_f32 v41, v54, v55
	v_cvt_pk_bf16_f32 v42, v48, v49
	v_cvt_pk_bf16_f32 v43, v50, v51
	global_store_dwordx4 v44, v[28:31], s[6:7] offset:256
	v_cvt_pk_bf16_f32 v12, v12, v13
	v_cvt_pk_bf16_f32 v13, v14, v15
	v_add_u32_e32 v28, 0x3c000, v122
	v_cvt_pk_bf16_f32 v14, v8, v9
	v_cvt_pk_bf16_f32 v15, v10, v11
	global_store_dwordx4 v44, v[40:43], s[6:7]
	v_cvt_pk_bf16_f32 v24, v36, v37
	v_cvt_pk_bf16_f32 v25, v38, v39
	v_cvt_pk_bf16_f32 v26, v32, v33
	v_cvt_pk_bf16_f32 v27, v34, v35
	global_store_dwordx4 v28, v[12:15], s[6:7] offset:256
	v_cvt_pk_bf16_f32 v8, v20, v21
	v_cvt_pk_bf16_f32 v9, v22, v23
	v_cvt_pk_bf16_f32 v10, v16, v17
	v_cvt_pk_bf16_f32 v11, v18, v19
	v_add_u32_e32 v12, 0x42000, v122
	v_cvt_pk_bf16_f32 v4, v4, v5
	v_cvt_pk_bf16_f32 v5, v6, v7
	v_cvt_pk_bf16_f32 v6, v0, v1
	v_cvt_pk_bf16_f32 v7, v2, v3
	s_and_b64 vcc, exec, s[4:5]
	s_mov_b32 s40, s36
	s_mov_b32 s41, s37
	s_mov_b32 s10, s39
	s_mov_b32 s11, s38
	global_store_dwordx4 v28, v[24:27], s[6:7]
	global_store_dwordx4 v12, v[8:11], s[6:7]
	global_store_dwordx4 v12, v[4:7], s[6:7] offset:256
	s_cbranch_vccz .LBB0_481
	s_waitcnt vmcnt(0)
	s_cmpk_gt_u32 s14, 0xff
	s_cbranch_scc1 .LBB0_488
	s_barrier

.LBB0_1357:
	v_mov_b64_e32 v[0:1], s[12:13]
	v_cmp_lt_i64_e32 vcc, s[10:11], v[0:1]
	s_lshl_b32 s19, s18, 20
	s_lshl_b32 s10, s16, 10
	s_add_i32 s19, s19, s10
	s_and_b64 s[10:11], vcc, exec
	s_cselect_b32 s15, s19, s45
	s_lshl_b32 s43, s17, 18
	s_lshl_b32 s10, s16, 21
	s_add_i32 s43, s43, s10
	s_and_b64 s[10:11], vcc, exec
	v_mov_b32_e32 v0, 0
	s_cselect_b32 s44, s43, s46
	s_add_i32 s45, s45, 0x80080
	s_addk_i32 s46, 0x100
	s_mov_b32 s47, -2
	v_mov_b32_e32 v1, v0
	v_mov_b32_e32 v2, v0
	v_mov_b32_e32 v3, v0
	v_mov_b32_e32 v4, v0
	v_mov_b32_e32 v5, v0
	v_mov_b32_e32 v6, v0
	v_mov_b32_e32 v7, v0
	v_mov_b32_e32 v8, v0
	v_mov_b32_e32 v9, v0
	v_mov_b32_e32 v10, v0
	v_mov_b32_e32 v11, v0
	v_mov_b32_e32 v12, v0
	v_mov_b32_e32 v13, v0
	v_mov_b32_e32 v14, v0
	v_mov_b32_e32 v15, v0
	v_mov_b32_e32 v24, v0
	v_mov_b32_e32 v25, v0
	v_mov_b32_e32 v26, v0
	v_mov_b32_e32 v27, v0
	v_mov_b32_e32 v28, v0
	v_mov_b32_e32 v29, v0
	v_mov_b32_e32 v30, v0
	v_mov_b32_e32 v31, v0
	v_mov_b32_e32 v40, v0
	v_mov_b32_e32 v41, v0
	v_mov_b32_e32 v42, v0
	v_mov_b32_e32 v43, v0
	v_mov_b32_e32 v44, v0
	v_mov_b32_e32 v45, v0
	v_mov_b32_e32 v46, v0
	v_mov_b32_e32 v47, v0
	v_mov_b32_e32 v16, v0
	v_mov_b32_e32 v17, v0
	v_mov_b32_e32 v18, v0
	v_mov_b32_e32 v19, v0
	v_mov_b32_e32 v20, v0
	v_mov_b32_e32 v21, v0
	v_mov_b32_e32 v22, v0
	v_mov_b32_e32 v23, v0
	v_mov_b32_e32 v32, v0
	v_mov_b32_e32 v33, v0
	v_mov_b32_e32 v34, v0
	v_mov_b32_e32 v35, v0
	v_mov_b32_e32 v36, v0
	v_mov_b32_e32 v37, v0
	v_mov_b32_e32 v38, v0
	v_mov_b32_e32 v39, v0
	v_mov_b32_e32 v48, v0
	v_mov_b32_e32 v49, v0
	v_mov_b32_e32 v50, v0
	v_mov_b32_e32 v51, v0
	v_mov_b32_e32 v52, v0
	v_mov_b32_e32 v53, v0
	v_mov_b32_e32 v54, v0
	v_mov_b32_e32 v55, v0
	v_mov_b32_e32 v56, v0
	v_mov_b32_e32 v57, v0
	v_mov_b32_e32 v58, v0
	v_mov_b32_e32 v59, v0
	v_mov_b32_e32 v60, v0
	v_mov_b32_e32 v61, v0
	v_mov_b32_e32 v62, v0
	v_mov_b32_e32 v63, v0
	v_mov_b32_e32 v64, v0
	v_mov_b32_e32 v65, v0
	v_mov_b32_e32 v66, v0
	v_mov_b32_e32 v67, v0
	v_mov_b32_e32 v68, v0
	v_mov_b32_e32 v69, v0
	v_mov_b32_e32 v70, v0
	v_mov_b32_e32 v71, v0
	v_mov_b32_e32 v72, v0
	v_mov_b32_e32 v73, v0
	v_mov_b32_e32 v74, v0
	v_mov_b32_e32 v75, v0
	v_mov_b32_e32 v76, v0
	v_mov_b32_e32 v77, v0
	v_mov_b32_e32 v78, v0
	v_mov_b32_e32 v79, v0
	v_mov_b32_e32 v88, v0
	v_mov_b32_e32 v89, v0
	v_mov_b32_e32 v90, v0
	v_mov_b32_e32 v91, v0
	v_mov_b32_e32 v92, v0
	v_mov_b32_e32 v93, v0
	v_mov_b32_e32 v94, v0
	v_mov_b32_e32 v95, v0
	v_mov_b32_e32 v106, v0
	v_mov_b32_e32 v107, v0
	v_mov_b32_e32 v108, v0
	v_mov_b32_e32 v109, v0
	v_mov_b32_e32 v110, v0
	v_mov_b32_e32 v111, v0
	v_mov_b32_e32 v112, v0
	v_mov_b32_e32 v113, v0
	v_mov_b32_e32 v80, v0
	v_mov_b32_e32 v81, v0
	v_mov_b32_e32 v82, v0
	v_mov_b32_e32 v83, v0
	v_mov_b32_e32 v84, v0
	v_mov_b32_e32 v85, v0
	v_mov_b32_e32 v86, v0
	v_mov_b32_e32 v87, v0
	v_mov_b32_e32 v98, v0
	v_mov_b32_e32 v99, v0
	v_mov_b32_e32 v100, v0
	v_mov_b32_e32 v101, v0
	v_mov_b32_e32 v102, v0
	v_mov_b32_e32 v103, v0
	v_mov_b32_e32 v104, v0
	v_mov_b32_e32 v105, v0
	v_mov_b32_e32 v114, v0
	v_mov_b32_e32 v115, v0
	v_mov_b32_e32 v116, v0
	v_mov_b32_e32 v117, v0
	v_mov_b32_e32 v118, v0
	v_mov_b32_e32 v119, v0
	v_mov_b32_e32 v120, v0
	v_mov_b32_e32 v121, v0
	v_mov_b32_e32 v122, v0
	v_mov_b32_e32 v123, v0
	v_mov_b32_e32 v124, v0
	v_mov_b32_e32 v125, v0
	v_mov_b32_e32 v126, v0
	v_mov_b32_e32 v127, v0
	v_mov_b32_e32 v128, v0
	v_mov_b32_e32 v129, v0
	ds_read_b128 v[220:223], v135
	ds_read_b128 v[224:227], v135 offset:1024
	ds_read_b128 v[228:231], v135 offset:2048
	ds_read_b128 v[232:235], v135 offset:3072
.LBB0_1358:
	s_add_i32 s10, s45, 0xfff80080
	s_cmp_eq_u32 s47, 4
	s_cselect_b32 s50, s15, s10
	s_cselect_b32 s48, s44, s46
	s_add_i32 s49, s50, 0x80
	s_mov_b32 m0, s38
	ds_read_b128 v[154:157], v136
	ds_read_b128 v[158:161], v136 offset:1024
	ds_read_b128 v[162:165], v136 offset:2048
	ds_read_b128 v[166:169], v136 offset:3072
	ds_read_b128 v[170:173], v136 offset:4096
	ds_read_b128 v[174:177], v136 offset:5120
	ds_read_b128 v[178:181], v136 offset:6144
	ds_read_b128 v[182:185], v136 offset:7168
	buffer_load_dwordx4 v131, s[72:75], s45 offen lds
	s_mov_b32 m0, s39
	s_nop 0
	buffer_load_dwordx4 v133, s[72:75], s45 offen lds
	s_waitcnt lgkmcnt(8)
	s_waitcnt vmcnt(10)
	s_barrier
	s_waitcnt lgkmcnt(0)
	s_setprio 1
	s_waitcnt lgkmcnt(7)
	v_mfma_f32_16x16x32_bf16 v[126:129], v[220:223], v[154:157], v[126:129]
	v_mfma_f32_16x16x32_bf16 v[122:125], v[228:231], v[154:157], v[122:125]
	s_waitcnt lgkmcnt(5)
	v_mfma_f32_16x16x32_bf16 v[118:121], v[220:223], v[162:165], v[118:121]
	v_mfma_f32_16x16x32_bf16 v[114:117], v[228:231], v[162:165], v[114:117]
	s_waitcnt lgkmcnt(3)
	v_mfma_f32_16x16x32_bf16 v[102:105], v[220:223], v[170:173], v[102:105]
	v_mfma_f32_16x16x32_bf16 v[98:101], v[228:231], v[170:173], v[98:101]
	s_waitcnt lgkmcnt(1)
	v_mfma_f32_16x16x32_bf16 v[84:87], v[220:223], v[178:181], v[84:87]
	v_mfma_f32_16x16x32_bf16 v[80:83], v[228:231], v[178:181], v[80:83]
	v_mfma_f32_16x16x32_bf16 v[126:129], v[224:227], v[158:161], v[126:129]
	v_mfma_f32_16x16x32_bf16 v[122:125], v[232:235], v[158:161], v[122:125]
	v_mfma_f32_16x16x32_bf16 v[118:121], v[224:227], v[166:169], v[118:121]
	v_mfma_f32_16x16x32_bf16 v[114:117], v[232:235], v[166:169], v[114:117]
	v_mfma_f32_16x16x32_bf16 v[102:105], v[224:227], v[174:177], v[102:105]
	v_mfma_f32_16x16x32_bf16 v[98:101], v[232:235], v[174:177], v[98:101]
	s_waitcnt lgkmcnt(0)
	v_mfma_f32_16x16x32_bf16 v[84:87], v[224:227], v[182:185], v[84:87]
	v_mfma_f32_16x16x32_bf16 v[80:83], v[232:235], v[182:185], v[80:83]
	s_setprio 0
	s_barrier
	s_mov_b32 s10, s74
	s_mov_b32 s11, s75
	s_mov_b32 m0, s21
	ds_read_b128 v[186:189], v135 offset:16384
	ds_read_b128 v[190:193], v135 offset:17408
	ds_read_b128 v[194:197], v135 offset:18432
	ds_read_b128 v[198:201], v135 offset:19456
	buffer_load_dwordx4 v132, s[8:11], s48 offen lds
	s_mov_b32 m0, s22
	s_nop 0
	buffer_load_dwordx4 v134, s[8:11], s48 offen lds
	s_waitcnt vmcnt(10)
	s_barrier
	s_waitcnt lgkmcnt(0)
	s_setprio 1
	s_waitcnt lgkmcnt(3)
	v_mfma_f32_16x16x32_bf16 v[110:113], v[186:189], v[154:157], v[110:113]
	s_waitcnt lgkmcnt(1)
	v_mfma_f32_16x16x32_bf16 v[106:109], v[194:197], v[154:157], v[106:109]
	v_mfma_f32_16x16x32_bf16 v[92:95], v[186:189], v[162:165], v[92:95]
	v_mfma_f32_16x16x32_bf16 v[88:91], v[194:197], v[162:165], v[88:91]
	v_mfma_f32_16x16x32_bf16 v[76:79], v[186:189], v[170:173], v[76:79]
	v_mfma_f32_16x16x32_bf16 v[72:75], v[194:197], v[170:173], v[72:75]
	v_mfma_f32_16x16x32_bf16 v[68:71], v[186:189], v[178:181], v[68:71]
	v_mfma_f32_16x16x32_bf16 v[64:67], v[194:197], v[178:181], v[64:67]
	v_mfma_f32_16x16x32_bf16 v[110:113], v[190:193], v[158:161], v[110:113]
	s_waitcnt lgkmcnt(0)
	v_mfma_f32_16x16x32_bf16 v[106:109], v[198:201], v[158:161], v[106:109]
	v_mfma_f32_16x16x32_bf16 v[92:95], v[190:193], v[166:169], v[92:95]
	v_mfma_f32_16x16x32_bf16 v[88:91], v[198:201], v[166:169], v[88:91]
	v_mfma_f32_16x16x32_bf16 v[76:79], v[190:193], v[174:177], v[76:79]
	v_mfma_f32_16x16x32_bf16 v[72:75], v[198:201], v[174:177], v[72:75]
	v_mfma_f32_16x16x32_bf16 v[68:71], v[190:193], v[182:185], v[68:71]
	v_mfma_f32_16x16x32_bf16 v[64:67], v[198:201], v[182:185], v[64:67]
	s_setprio 0
	s_mov_b32 m0, s2
	s_barrier
	ds_read_b128 v[154:157], v136 offset:16384
	ds_read_b128 v[158:161], v136 offset:17408
	ds_read_b128 v[162:165], v136 offset:18432
	ds_read_b128 v[166:169], v136 offset:19456
	ds_read_b128 v[170:173], v136 offset:20480
	ds_read_b128 v[174:177], v136 offset:21504
	ds_read_b128 v[178:181], v136 offset:22528
	ds_read_b128 v[182:185], v136 offset:23552
	buffer_load_dwordx4 v131, s[72:75], s50 offen lds
	s_mov_b32 m0, s23
	s_nop 0
	buffer_load_dwordx4 v133, s[72:75], s50 offen lds
	s_waitcnt vmcnt(10)
	s_barrier
	s_waitcnt lgkmcnt(0)
	s_setprio 1
	s_waitcnt lgkmcnt(7)
	v_mfma_f32_16x16x32_bf16 v[60:63], v[220:223], v[154:157], v[60:63]
	v_mfma_f32_16x16x32_bf16 v[56:59], v[228:231], v[154:157], v[56:59]
	s_waitcnt lgkmcnt(5)
	v_mfma_f32_16x16x32_bf16 v[52:55], v[220:223], v[162:165], v[52:55]
	v_mfma_f32_16x16x32_bf16 v[48:51], v[228:231], v[162:165], v[48:51]
	s_waitcnt lgkmcnt(3)
	v_mfma_f32_16x16x32_bf16 v[36:39], v[220:223], v[170:173], v[36:39]
	v_mfma_f32_16x16x32_bf16 v[32:35], v[228:231], v[170:173], v[32:35]
	s_waitcnt lgkmcnt(1)
	v_mfma_f32_16x16x32_bf16 v[20:23], v[220:223], v[178:181], v[20:23]
	v_mfma_f32_16x16x32_bf16 v[16:19], v[228:231], v[178:181], v[16:19]
	v_mfma_f32_16x16x32_bf16 v[60:63], v[224:227], v[158:161], v[60:63]
	v_mfma_f32_16x16x32_bf16 v[56:59], v[232:235], v[158:161], v[56:59]
	v_mfma_f32_16x16x32_bf16 v[52:55], v[224:227], v[166:169], v[52:55]
	v_mfma_f32_16x16x32_bf16 v[48:51], v[232:235], v[166:169], v[48:51]
	v_mfma_f32_16x16x32_bf16 v[36:39], v[224:227], v[174:177], v[36:39]
	v_mfma_f32_16x16x32_bf16 v[32:35], v[232:235], v[174:177], v[32:35]
	s_waitcnt lgkmcnt(0)
	v_mfma_f32_16x16x32_bf16 v[20:23], v[224:227], v[182:185], v[20:23]
	v_mfma_f32_16x16x32_bf16 v[16:19], v[232:235], v[182:185], v[16:19]
	s_setprio 0
	s_barrier
	ds_read_b128 v[220:223], v135 offset:32768
	ds_read_b128 v[224:227], v135 offset:33792
	ds_read_b128 v[228:231], v135 offset:34816
	ds_read_b128 v[232:235], v135 offset:35840
	s_add_i32 s51, s48, 0x20000
	s_mov_b32 m0, s24
	s_nop 0
	buffer_load_dwordx4 v132, s[8:11], s51 offen lds
	s_mov_b32 m0, s25
	s_nop 0
	buffer_load_dwordx4 v134, s[8:11], s51 offen lds
	s_waitcnt vmcnt(10)
	s_barrier
	s_setprio 1
	v_mfma_f32_16x16x32_bf16 v[44:47], v[186:189], v[154:157], v[44:47]
	v_mfma_f32_16x16x32_bf16 v[40:43], v[194:197], v[154:157], v[40:43]
	v_mfma_f32_16x16x32_bf16 v[28:31], v[186:189], v[162:165], v[28:31]
	v_mfma_f32_16x16x32_bf16 v[24:27], v[194:197], v[162:165], v[24:27]
	v_mfma_f32_16x16x32_bf16 v[12:15], v[186:189], v[170:173], v[12:15]
	v_mfma_f32_16x16x32_bf16 v[8:11], v[194:197], v[170:173], v[8:11]
	v_mfma_f32_16x16x32_bf16 v[4:7], v[186:189], v[178:181], v[4:7]
	v_mfma_f32_16x16x32_bf16 v[0:3], v[194:197], v[178:181], v[0:3]
	v_mfma_f32_16x16x32_bf16 v[44:47], v[190:193], v[158:161], v[44:47]
	v_mfma_f32_16x16x32_bf16 v[40:43], v[198:201], v[158:161], v[40:43]
	v_mfma_f32_16x16x32_bf16 v[28:31], v[190:193], v[166:169], v[28:31]
	v_mfma_f32_16x16x32_bf16 v[24:27], v[198:201], v[166:169], v[24:27]
	v_mfma_f32_16x16x32_bf16 v[12:15], v[190:193], v[174:177], v[12:15]
	v_mfma_f32_16x16x32_bf16 v[8:11], v[198:201], v[174:177], v[8:11]
	v_mfma_f32_16x16x32_bf16 v[4:7], v[190:193], v[182:185], v[4:7]
	v_mfma_f32_16x16x32_bf16 v[0:3], v[198:201], v[182:185], v[0:3]
	s_setprio 0
	s_barrier
	s_add_i32 s50, s50, 0x80000
	s_mov_b32 m0, s26
	ds_read_b128 v[154:157], v136 offset:32768
	ds_read_b128 v[158:161], v136 offset:33792
	ds_read_b128 v[162:165], v136 offset:34816
	ds_read_b128 v[166:169], v136 offset:35840
	ds_read_b128 v[170:173], v136 offset:36864
	ds_read_b128 v[174:177], v136 offset:37888
	ds_read_b128 v[178:181], v136 offset:38912
	ds_read_b128 v[182:185], v136 offset:39936
	buffer_load_dwordx4 v131, s[72:75], s50 offen lds
	s_mov_b32 m0, s27
	s_nop 0
	buffer_load_dwordx4 v133, s[72:75], s50 offen lds
	s_waitcnt lgkmcnt(8)
	s_waitcnt vmcnt(10)
	s_barrier
	s_waitcnt lgkmcnt(0)
	s_setprio 1
	s_waitcnt lgkmcnt(7)
	v_mfma_f32_16x16x32_bf16 v[126:129], v[220:223], v[154:157], v[126:129]
	v_mfma_f32_16x16x32_bf16 v[122:125], v[228:231], v[154:157], v[122:125]
	s_waitcnt lgkmcnt(5)
	v_mfma_f32_16x16x32_bf16 v[118:121], v[220:223], v[162:165], v[118:121]
	v_mfma_f32_16x16x32_bf16 v[114:117], v[228:231], v[162:165], v[114:117]
	s_waitcnt lgkmcnt(3)
	v_mfma_f32_16x16x32_bf16 v[102:105], v[220:223], v[170:173], v[102:105]
	v_mfma_f32_16x16x32_bf16 v[98:101], v[228:231], v[170:173], v[98:101]
	s_waitcnt lgkmcnt(1)
	v_mfma_f32_16x16x32_bf16 v[84:87], v[220:223], v[178:181], v[84:87]
	v_mfma_f32_16x16x32_bf16 v[80:83], v[228:231], v[178:181], v[80:83]
	v_mfma_f32_16x16x32_bf16 v[126:129], v[224:227], v[158:161], v[126:129]
	v_mfma_f32_16x16x32_bf16 v[122:125], v[232:235], v[158:161], v[122:125]
	v_mfma_f32_16x16x32_bf16 v[118:121], v[224:227], v[166:169], v[118:121]
	v_mfma_f32_16x16x32_bf16 v[114:117], v[232:235], v[166:169], v[114:117]
	v_mfma_f32_16x16x32_bf16 v[102:105], v[224:227], v[174:177], v[102:105]
	v_mfma_f32_16x16x32_bf16 v[98:101], v[232:235], v[174:177], v[98:101]
	s_waitcnt lgkmcnt(0)
	v_mfma_f32_16x16x32_bf16 v[84:87], v[224:227], v[182:185], v[84:87]
	v_mfma_f32_16x16x32_bf16 v[80:83], v[232:235], v[182:185], v[80:83]
	s_setprio 0
	s_barrier
	s_add_i32 s50, s48, 0x80
	s_mov_b32 m0, s30
	ds_read_b128 v[186:189], v135 offset:49152
	ds_read_b128 v[190:193], v135 offset:50176
	ds_read_b128 v[194:197], v135 offset:51200
	ds_read_b128 v[198:201], v135 offset:52224
	buffer_load_dwordx4 v132, s[8:11], s50 offen lds
	s_mov_b32 m0, s31
	s_nop 0
	buffer_load_dwordx4 v134, s[8:11], s50 offen lds
	s_waitcnt vmcnt(10)
	s_barrier
	s_waitcnt lgkmcnt(0)
	s_setprio 1
	s_waitcnt lgkmcnt(3)
	v_mfma_f32_16x16x32_bf16 v[110:113], v[186:189], v[154:157], v[110:113]
	s_waitcnt lgkmcnt(1)
	v_mfma_f32_16x16x32_bf16 v[106:109], v[194:197], v[154:157], v[106:109]
	v_mfma_f32_16x16x32_bf16 v[92:95], v[186:189], v[162:165], v[92:95]
	v_mfma_f32_16x16x32_bf16 v[88:91], v[194:197], v[162:165], v[88:91]
	v_mfma_f32_16x16x32_bf16 v[76:79], v[186:189], v[170:173], v[76:79]
	v_mfma_f32_16x16x32_bf16 v[72:75], v[194:197], v[170:173], v[72:75]
	v_mfma_f32_16x16x32_bf16 v[68:71], v[186:189], v[178:181], v[68:71]
	v_mfma_f32_16x16x32_bf16 v[64:67], v[194:197], v[178:181], v[64:67]
	v_mfma_f32_16x16x32_bf16 v[110:113], v[190:193], v[158:161], v[110:113]
	s_waitcnt lgkmcnt(0)
	v_mfma_f32_16x16x32_bf16 v[106:109], v[198:201], v[158:161], v[106:109]
	v_mfma_f32_16x16x32_bf16 v[92:95], v[190:193], v[166:169], v[92:95]
	v_mfma_f32_16x16x32_bf16 v[88:91], v[198:201], v[166:169], v[88:91]
	v_mfma_f32_16x16x32_bf16 v[76:79], v[190:193], v[174:177], v[76:79]
	v_mfma_f32_16x16x32_bf16 v[72:75], v[198:201], v[174:177], v[72:75]
	v_mfma_f32_16x16x32_bf16 v[68:71], v[190:193], v[182:185], v[68:71]
	v_mfma_f32_16x16x32_bf16 v[64:67], v[198:201], v[182:185], v[64:67]
	s_setprio 0
	s_mov_b32 m0, s34
	s_barrier
	ds_read_b128 v[154:157], v136 offset:49152
	ds_read_b128 v[158:161], v136 offset:50176
	ds_read_b128 v[162:165], v136 offset:51200
	ds_read_b128 v[166:169], v136 offset:52224
	ds_read_b128 v[170:173], v136 offset:53248
	ds_read_b128 v[174:177], v136 offset:54272
	ds_read_b128 v[178:181], v136 offset:55296
	ds_read_b128 v[182:185], v136 offset:56320
	buffer_load_dwordx4 v131, s[72:75], s49 offen lds
	s_mov_b32 m0, s35
	s_nop 0
	buffer_load_dwordx4 v133, s[72:75], s49 offen lds
	s_waitcnt vmcnt(10)
	s_barrier
	s_waitcnt lgkmcnt(0)
	s_setprio 1
	s_waitcnt lgkmcnt(7)
	v_mfma_f32_16x16x32_bf16 v[60:63], v[220:223], v[154:157], v[60:63]
	v_mfma_f32_16x16x32_bf16 v[56:59], v[228:231], v[154:157], v[56:59]
	s_waitcnt lgkmcnt(5)
	v_mfma_f32_16x16x32_bf16 v[52:55], v[220:223], v[162:165], v[52:55]
	v_mfma_f32_16x16x32_bf16 v[48:51], v[228:231], v[162:165], v[48:51]
	s_waitcnt lgkmcnt(3)
	v_mfma_f32_16x16x32_bf16 v[36:39], v[220:223], v[170:173], v[36:39]
	v_mfma_f32_16x16x32_bf16 v[32:35], v[228:231], v[170:173], v[32:35]
	s_waitcnt lgkmcnt(1)
	v_mfma_f32_16x16x32_bf16 v[20:23], v[220:223], v[178:181], v[20:23]
	v_mfma_f32_16x16x32_bf16 v[16:19], v[228:231], v[178:181], v[16:19]
	v_mfma_f32_16x16x32_bf16 v[60:63], v[224:227], v[158:161], v[60:63]
	v_mfma_f32_16x16x32_bf16 v[56:59], v[232:235], v[158:161], v[56:59]
	v_mfma_f32_16x16x32_bf16 v[52:55], v[224:227], v[166:169], v[52:55]
	v_mfma_f32_16x16x32_bf16 v[48:51], v[232:235], v[166:169], v[48:51]
	v_mfma_f32_16x16x32_bf16 v[36:39], v[224:227], v[174:177], v[36:39]
	v_mfma_f32_16x16x32_bf16 v[32:35], v[232:235], v[174:177], v[32:35]
	s_waitcnt lgkmcnt(0)
	v_mfma_f32_16x16x32_bf16 v[20:23], v[224:227], v[182:185], v[20:23]
	v_mfma_f32_16x16x32_bf16 v[16:19], v[232:235], v[182:185], v[16:19]
	s_setprio 0
	s_barrier
	ds_read_b128 v[220:223], v135
	ds_read_b128 v[224:227], v135 offset:1024
	ds_read_b128 v[228:231], v135 offset:2048
	ds_read_b128 v[232:235], v135 offset:3072
	s_add_i32 s48, s48, 0x20080
	s_mov_b32 m0, s36
	s_nop 0
	buffer_load_dwordx4 v132, s[8:11], s48 offen lds
	s_mov_b32 m0, s37
	s_nop 0
	buffer_load_dwordx4 v134, s[8:11], s48 offen lds
	s_waitcnt vmcnt(10)
	s_barrier
	s_setprio 1
	v_mfma_f32_16x16x32_bf16 v[44:47], v[186:189], v[154:157], v[44:47]
	v_mfma_f32_16x16x32_bf16 v[40:43], v[194:197], v[154:157], v[40:43]
	v_mfma_f32_16x16x32_bf16 v[28:31], v[186:189], v[162:165], v[28:31]
	v_mfma_f32_16x16x32_bf16 v[24:27], v[194:197], v[162:165], v[24:27]
	v_mfma_f32_16x16x32_bf16 v[12:15], v[186:189], v[170:173], v[12:15]
	v_mfma_f32_16x16x32_bf16 v[8:11], v[194:197], v[170:173], v[8:11]
	v_mfma_f32_16x16x32_bf16 v[4:7], v[186:189], v[178:181], v[4:7]
	v_mfma_f32_16x16x32_bf16 v[0:3], v[194:197], v[178:181], v[0:3]
	v_mfma_f32_16x16x32_bf16 v[44:47], v[190:193], v[158:161], v[44:47]
	v_mfma_f32_16x16x32_bf16 v[40:43], v[198:201], v[158:161], v[40:43]
	v_mfma_f32_16x16x32_bf16 v[28:31], v[190:193], v[166:169], v[28:31]
	v_mfma_f32_16x16x32_bf16 v[24:27], v[198:201], v[166:169], v[24:27]
	v_mfma_f32_16x16x32_bf16 v[12:15], v[190:193], v[174:177], v[12:15]
	v_mfma_f32_16x16x32_bf16 v[8:11], v[198:201], v[174:177], v[8:11]
	v_mfma_f32_16x16x32_bf16 v[4:7], v[190:193], v[182:185], v[4:7]
	v_mfma_f32_16x16x32_bf16 v[0:3], v[198:201], v[182:185], v[0:3]
	s_setprio 0
	s_add_i32 s47, s47, 2
	s_addk_i32 s45, 0x100
	s_addk_i32 s46, 0x100
	s_cmp_gt_u32 s47, 5
	s_barrier
	s_cbranch_scc0 .LBB0_1358
	s_waitcnt lgkmcnt(0)
	s_getreg_b32 s10, hwreg(HW_REG_HW_ID, 0, 6)
	s_and_b32 s10, s10, 63
	s_lshl_b32 s10, s10, 2
	s_add_i32 s10, s10, 0
	s_add_i32 s10, s10, 0x20010
	v_mov_b32_e32 v96, s10
	ds_read_b32 v96, v96
	s_ashr_i32 s15, s14, 31
	s_lshl_b64 s[10:11], s[14:15], 12
	v_mbcnt_lo_u32_b32 v137, -1, 0
	v_mbcnt_hi_u32_b32 v137, -1, v137
	v_cvt_pk_bf16_f32 v126, v126, v127
	s_waitcnt lgkmcnt(0)
	v_readfirstlane_b32 s14, v96
	s_lshl_b32 s14, s14, 6
	s_add_u32 s15, s28, s10
	s_addc_u32 s44, s29, s11
	s_lshl_b32 s10, s42, 8
	s_ashr_i32 s11, s10, 31
	s_lshl_b64 s[10:11], s[10:11], 14
	s_add_u32 s15, s15, s10
	s_addc_u32 s42, s44, s11
	s_lshl_b32 s10, s41, 8
	s_ashr_i32 s11, s10, 31
	v_or_b32_e32 v96, s14, v137
	s_lshl_b64 s[10:11], s[10:11], 1
	v_and_b32_e32 v138, 15, v137
	s_add_u32 s10, s15, s10
	v_lshrrev_b32_e32 v96, 2, v96
	s_mov_b32 s15, 0x3ffc0
	v_and_or_b32 v96, v96, s15, v138
	v_lshlrev_b32_e32 v138, 14, v96
	v_mov_b32_e32 v96, 0xf0
	v_bitop3_b32 v137, s14, v96, v137 bitop3:0xc8
	s_addc_u32 s11, s42, s11
	v_or_b32_e32 v96, v138, v137
	v_cvt_pk_bf16_f32 v127, v128, v129
	v_cvt_pk_bf16_f32 v128, v122, v123
	v_lshl_add_u64 v[122:123], s[10:11], 0, v[96:97]
	s_mov_b32 s14, 0x40000
	v_cvt_pk_bf16_f32 v92, v92, v93
	v_cvt_pk_bf16_f32 v93, v94, v95
	v_cvt_pk_bf16_f32 v94, v88, v89
	v_add_co_u32_e32 v88, vcc, s14, v122
	v_cvt_pk_bf16_f32 v110, v110, v111
	v_cvt_pk_bf16_f32 v111, v112, v113
	v_cvt_pk_bf16_f32 v112, v106, v107
	v_cvt_pk_bf16_f32 v113, v108, v109
	v_addc_co_u32_e32 v89, vcc, 0, v123, vcc
	s_mov_b32 s14, 0x80000
	v_cvt_pk_bf16_f32 v129, v124, v125
	global_store_dwordx4 v96, v[110:113], s[10:11] offset:256
	v_cvt_pk_bf16_f32 v106, v118, v119
	v_cvt_pk_bf16_f32 v107, v120, v121
	v_cvt_pk_bf16_f32 v108, v114, v115
	v_cvt_pk_bf16_f32 v109, v116, v117
	v_or_b32_e32 v110, 0x40000, v96
	v_cvt_pk_bf16_f32 v95, v90, v91
	v_cvt_pk_bf16_f32 v76, v76, v77
	v_cvt_pk_bf16_f32 v77, v78, v79
	v_cvt_pk_bf16_f32 v78, v72, v73
	v_add_co_u32_e32 v72, vcc, s14, v122
	global_store_dwordx4 v96, v[126:129], s[10:11]
	v_or_b32_e32 v124, 0x100, v137
	global_store_dwordx4 v110, v[106:109], s[10:11]
	global_store_dwordx4 v[88:89], v[92:95], off offset:256
	v_cvt_pk_bf16_f32 v88, v102, v103
	v_cvt_pk_bf16_f32 v89, v104, v105
	v_cvt_pk_bf16_f32 v90, v98, v99
	v_cvt_pk_bf16_f32 v91, v100, v101
	v_or_b32_e32 v92, 0x80000, v96
	v_cvt_pk_bf16_f32 v79, v74, v75
	v_addc_co_u32_e32 v73, vcc, 0, v123, vcc
	v_or_b32_e32 v125, v138, v124
	global_store_dwordx4 v92, v[88:91], s[10:11]
	global_store_dwordx4 v[72:73], v[76:79], off offset:256
	v_cvt_pk_bf16_f32 v72, v84, v85
	v_cvt_pk_bf16_f32 v73, v86, v87
	v_or_b32_e32 v76, 0xc0000, v138
	v_cvt_pk_bf16_f32 v74, v80, v81
	v_cvt_pk_bf16_f32 v75, v82, v83
	v_or_b32_e32 v77, v76, v137
	v_cvt_pk_bf16_f32 v68, v68, v69
	v_cvt_pk_bf16_f32 v69, v70, v71
	v_cvt_pk_bf16_f32 v70, v64, v65
	v_cvt_pk_bf16_f32 v71, v66, v67
	v_or_b32_e32 v64, v76, v124
	v_cvt_pk_bf16_f32 v60, v60, v61
	v_cvt_pk_bf16_f32 v61, v62, v63
	v_cvt_pk_bf16_f32 v62, v56, v57
	v_cvt_pk_bf16_f32 v63, v58, v59
	v_add_u32_e32 v56, 0x200000, v96
	v_cvt_pk_bf16_f32 v44, v44, v45
	v_cvt_pk_bf16_f32 v45, v46, v47
	v_cvt_pk_bf16_f32 v46, v40, v41
	v_cvt_pk_bf16_f32 v47, v42, v43
	v_add_u32_e32 v40, 0x200000, v125
	global_store_dwordx4 v77, v[72:75], s[10:11]
	global_store_dwordx4 v64, v[68:71], s[10:11]
	global_store_dwordx4 v56, v[60:63], s[10:11]
	global_store_dwordx4 v40, v[44:47], s[10:11]
	v_cvt_pk_bf16_f32 v28, v28, v29
	v_cvt_pk_bf16_f32 v29, v30, v31
	v_add_u32_e32 v44, 0x240000, v96
	v_cvt_pk_bf16_f32 v30, v24, v25
	v_cvt_pk_bf16_f32 v31, v26, v27
	v_cvt_pk_bf16_f32 v40, v52, v53
	v_cvt_pk_bf16_f32 v41, v54, v55
	v_cvt_pk_bf16_f32 v42, v48, v49
	v_cvt_pk_bf16_f32 v43, v50, v51
	global_store_dwordx4 v44, v[28:31], s[10:11] offset:256
	v_cvt_pk_bf16_f32 v12, v12, v13
	v_cvt_pk_bf16_f32 v13, v14, v15
	v_add_u32_e32 v28, 0x280000, v96
	v_cvt_pk_bf16_f32 v14, v8, v9
	v_cvt_pk_bf16_f32 v15, v10, v11
	global_store_dwordx4 v44, v[40:43], s[10:11]
	v_cvt_pk_bf16_f32 v24, v36, v37
	v_cvt_pk_bf16_f32 v25, v38, v39
	v_cvt_pk_bf16_f32 v26, v32, v33
	v_cvt_pk_bf16_f32 v27, v34, v35
	global_store_dwordx4 v28, v[12:15], s[10:11] offset:256
	v_cvt_pk_bf16_f32 v8, v20, v21
	v_cvt_pk_bf16_f32 v9, v22, v23
	v_cvt_pk_bf16_f32 v10, v16, v17
	v_cvt_pk_bf16_f32 v11, v18, v19
	v_add_u32_e32 v12, 0x2c0000, v96
	v_cvt_pk_bf16_f32 v4, v4, v5
	v_cvt_pk_bf16_f32 v5, v6, v7
	v_cvt_pk_bf16_f32 v6, v0, v1
	v_cvt_pk_bf16_f32 v7, v2, v3
	s_and_b64 vcc, exec, s[4:5]
	s_mov_b32 s14, s16
	s_mov_b32 s41, s17
	s_mov_b32 s42, s18
	s_mov_b32 s46, s43
	s_mov_b32 s45, s19
	global_store_dwordx4 v28, v[24:27], s[10:11]
	global_store_dwordx4 v12, v[8:11], s[10:11]
	global_store_dwordx4 v12, v[4:7], s[10:11] offset:256
	s_cbranch_vccz .LBB0_1352
	s_branch .LBB0_1361

.LBB0_1495:
	v_mov_b64_e32 v[0:1], s[18:19]
	v_cmp_lt_i64_e32 vcc, s[10:11], v[0:1]
	s_lshl_b32 s22, s21, 20
	s_and_b64 s[10:11], vcc, exec
	s_cselect_b32 s48, s22, s50
	s_lshl_b32 s23, s20, 20
	s_and_b64 s[10:11], vcc, exec
	v_mov_b32_e32 v0, 0
	s_cselect_b32 s49, s23, s51
	s_add_i32 s50, s50, 0x80080
	s_addk_i32 s51, 0x100
	s_mov_b32 s52, -2
	v_mov_b32_e32 v1, v0
	v_mov_b32_e32 v2, v0
	v_mov_b32_e32 v3, v0
	v_mov_b32_e32 v4, v0
	v_mov_b32_e32 v5, v0
	v_mov_b32_e32 v6, v0
	v_mov_b32_e32 v7, v0
	v_mov_b32_e32 v12, v0
	v_mov_b32_e32 v13, v0
	v_mov_b32_e32 v14, v0
	v_mov_b32_e32 v15, v0
	s_waitcnt vmcnt(15)
	v_mov_b32_e32 v20, v0
	v_mov_b32_e32 v21, v0
	v_mov_b32_e32 v22, v0
	v_mov_b32_e32 v23, v0
	v_mov_b32_e32 v48, v0
	v_mov_b32_e32 v49, v0
	v_mov_b32_e32 v50, v0
	v_mov_b32_e32 v51, v0
	v_mov_b32_e32 v52, v0
	v_mov_b32_e32 v53, v0
	v_mov_b32_e32 v54, v0
	v_mov_b32_e32 v55, v0
	v_mov_b32_e32 v56, v0
	v_mov_b32_e32 v57, v0
	v_mov_b32_e32 v58, v0
	v_mov_b32_e32 v59, v0
	s_waitcnt vmcnt(14)
	v_mov_b32_e32 v60, v0
	v_mov_b32_e32 v61, v0
	v_mov_b32_e32 v62, v0
	v_mov_b32_e32 v63, v0
	v_mov_b32_e32 v8, v0
	v_mov_b32_e32 v9, v0
	v_mov_b32_e32 v10, v0
	v_mov_b32_e32 v11, v0
	v_mov_b32_e32 v16, v0
	v_mov_b32_e32 v17, v0
	v_mov_b32_e32 v18, v0
	v_mov_b32_e32 v19, v0
	v_mov_b32_e32 v24, v0
	v_mov_b32_e32 v25, v0
	v_mov_b32_e32 v26, v0
	v_mov_b32_e32 v27, v0
	v_mov_b32_e32 v28, v0
	v_mov_b32_e32 v29, v0
	v_mov_b32_e32 v30, v0
	v_mov_b32_e32 v31, v0
	v_mov_b32_e32 v64, v0
	v_mov_b32_e32 v65, v0
	v_mov_b32_e32 v66, v0
	v_mov_b32_e32 v67, v0
	v_mov_b32_e32 v68, v0
	v_mov_b32_e32 v69, v0
	v_mov_b32_e32 v70, v0
	v_mov_b32_e32 v71, v0
	v_mov_b32_e32 v72, v0
	v_mov_b32_e32 v73, v0
	v_mov_b32_e32 v74, v0
	v_mov_b32_e32 v75, v0
	v_mov_b32_e32 v76, v0
	v_mov_b32_e32 v77, v0
	v_mov_b32_e32 v78, v0
	v_mov_b32_e32 v79, v0
	v_mov_b32_e32 v80, v0
	v_mov_b32_e32 v81, v0
	v_mov_b32_e32 v82, v0
	v_mov_b32_e32 v83, v0
	v_mov_b32_e32 v84, v0
	v_mov_b32_e32 v85, v0
	v_mov_b32_e32 v86, v0
	v_mov_b32_e32 v87, v0
	v_mov_b32_e32 v88, v0
	v_mov_b32_e32 v89, v0
	v_mov_b32_e32 v90, v0
	v_mov_b32_e32 v91, v0
	v_mov_b32_e32 v92, v0
	v_mov_b32_e32 v93, v0
	v_mov_b32_e32 v94, v0
	v_mov_b32_e32 v95, v0
	v_mov_b32_e32 v114, v0
	v_mov_b32_e32 v115, v0
	v_mov_b32_e32 v116, v0
	v_mov_b32_e32 v117, v0
	v_mov_b32_e32 v118, v0
	v_mov_b32_e32 v119, v0
	v_mov_b32_e32 v120, v0
	v_mov_b32_e32 v121, v0
	v_mov_b32_e32 v122, v0
	v_mov_b32_e32 v123, v0
	v_mov_b32_e32 v124, v0
	v_mov_b32_e32 v125, v0
	v_mov_b32_e32 v126, v0
	v_mov_b32_e32 v127, v0
	v_mov_b32_e32 v128, v0
	v_mov_b32_e32 v129, v0
	v_mov_b32_e32 v98, v0
	v_mov_b32_e32 v99, v0
	v_mov_b32_e32 v100, v0
	v_mov_b32_e32 v101, v0
	v_mov_b32_e32 v102, v0
	v_mov_b32_e32 v103, v0
	v_mov_b32_e32 v104, v0
	v_mov_b32_e32 v105, v0
	v_mov_b32_e32 v106, v0
	v_mov_b32_e32 v107, v0
	v_mov_b32_e32 v108, v0
	v_mov_b32_e32 v109, v0
	v_mov_b32_e32 v110, v0
	v_mov_b32_e32 v111, v0
	v_mov_b32_e32 v112, v0
	v_mov_b32_e32 v113, v0
	v_mov_b32_e32 v130, v0
	v_mov_b32_e32 v131, v0
	v_mov_b32_e32 v132, v0
	v_mov_b32_e32 v133, v0
	v_mov_b32_e32 v134, v0
	v_mov_b32_e32 v135, v0
	v_mov_b32_e32 v136, v0
	v_mov_b32_e32 v137, v0
	v_mov_b32_e32 v138, v0
	v_mov_b32_e32 v139, v0
	v_mov_b32_e32 v140, v0
	v_mov_b32_e32 v141, v0
	v_mov_b32_e32 v142, v0
	v_mov_b32_e32 v143, v0
	v_mov_b32_e32 v144, v0
	v_mov_b32_e32 v145, v0
	ds_read_b128 v[220:223], v153
	ds_read_b128 v[224:227], v153 offset:1024
	ds_read_b128 v[228:231], v153 offset:2048
	ds_read_b128 v[232:235], v153 offset:3072
.LBB0_1496:
	s_add_i32 s10, s50, 0xfff80080
	s_cmp_eq_u32 s52, 28
	s_cselect_b32 s55, s48, s10
	s_cselect_b32 s53, s49, s51
	s_or_b32 s54, s55, 0x80
	s_mov_b32 m0, s44
	ds_read_b128 v[156:159], v154
	ds_read_b128 v[160:163], v154 offset:1024
	ds_read_b128 v[164:167], v154 offset:2048
	ds_read_b128 v[168:171], v154 offset:3072
	ds_read_b128 v[172:175], v154 offset:4096
	ds_read_b128 v[176:179], v154 offset:5120
	ds_read_b128 v[180:183], v154 offset:6144
	ds_read_b128 v[184:187], v154 offset:7168
	buffer_load_dwordx4 v149, s[72:75], s50 offen lds
	s_mov_b32 m0, s45
	s_nop 0
	buffer_load_dwordx4 v151, s[72:75], s50 offen lds
	s_waitcnt lgkmcnt(8)
	s_waitcnt vmcnt(10)
	s_barrier
	s_waitcnt lgkmcnt(0)
	s_setprio 1
	s_waitcnt lgkmcnt(7)
	v_mfma_f32_16x16x32_bf16 v[142:145], v[220:223], v[156:159], v[142:145]
	v_mfma_f32_16x16x32_bf16 v[138:141], v[228:231], v[156:159], v[138:141]
	s_waitcnt lgkmcnt(5)
	v_mfma_f32_16x16x32_bf16 v[134:137], v[220:223], v[164:167], v[134:137]
	v_mfma_f32_16x16x32_bf16 v[130:133], v[228:231], v[164:167], v[130:133]
	s_waitcnt lgkmcnt(3)
	v_mfma_f32_16x16x32_bf16 v[110:113], v[220:223], v[172:175], v[110:113]
	v_mfma_f32_16x16x32_bf16 v[106:109], v[228:231], v[172:175], v[106:109]
	s_waitcnt lgkmcnt(1)
	v_mfma_f32_16x16x32_bf16 v[102:105], v[220:223], v[180:183], v[102:105]
	v_mfma_f32_16x16x32_bf16 v[98:101], v[228:231], v[180:183], v[98:101]
	v_mfma_f32_16x16x32_bf16 v[142:145], v[224:227], v[160:163], v[142:145]
	v_mfma_f32_16x16x32_bf16 v[138:141], v[232:235], v[160:163], v[138:141]
	v_mfma_f32_16x16x32_bf16 v[134:137], v[224:227], v[168:171], v[134:137]
	v_mfma_f32_16x16x32_bf16 v[130:133], v[232:235], v[168:171], v[130:133]
	v_mfma_f32_16x16x32_bf16 v[110:113], v[224:227], v[176:179], v[110:113]
	v_mfma_f32_16x16x32_bf16 v[106:109], v[232:235], v[176:179], v[106:109]
	s_waitcnt lgkmcnt(0)
	v_mfma_f32_16x16x32_bf16 v[102:105], v[224:227], v[184:187], v[102:105]
	v_mfma_f32_16x16x32_bf16 v[98:101], v[232:235], v[184:187], v[98:101]
	s_setprio 0
	s_barrier
	s_mov_b32 s10, s74
	s_mov_b32 s11, s75
	s_mov_b32 m0, s29
	ds_read_b128 v[188:191], v153 offset:16384
	ds_read_b128 v[192:195], v153 offset:17408
	ds_read_b128 v[196:199], v153 offset:18432
	ds_read_b128 v[200:203], v153 offset:19456
	buffer_load_dwordx4 v150, s[8:11], s53 offen lds
	s_mov_b32 m0, s30
	s_nop 0
	buffer_load_dwordx4 v152, s[8:11], s53 offen lds
	s_waitcnt vmcnt(10)
	s_barrier
	s_waitcnt lgkmcnt(0)
	s_setprio 1
	s_waitcnt lgkmcnt(3)
	v_mfma_f32_16x16x32_bf16 v[126:129], v[188:191], v[156:159], v[126:129]
	s_waitcnt lgkmcnt(1)
	v_mfma_f32_16x16x32_bf16 v[122:125], v[196:199], v[156:159], v[122:125]
	v_mfma_f32_16x16x32_bf16 v[118:121], v[188:191], v[164:167], v[118:121]
	v_mfma_f32_16x16x32_bf16 v[114:117], v[196:199], v[164:167], v[114:117]
	v_mfma_f32_16x16x32_bf16 v[92:95], v[188:191], v[172:175], v[92:95]
	v_mfma_f32_16x16x32_bf16 v[88:91], v[196:199], v[172:175], v[88:91]
	v_mfma_f32_16x16x32_bf16 v[84:87], v[188:191], v[180:183], v[84:87]
	v_mfma_f32_16x16x32_bf16 v[80:83], v[196:199], v[180:183], v[80:83]
	v_mfma_f32_16x16x32_bf16 v[126:129], v[192:195], v[160:163], v[126:129]
	s_waitcnt lgkmcnt(0)
	v_mfma_f32_16x16x32_bf16 v[122:125], v[200:203], v[160:163], v[122:125]
	v_mfma_f32_16x16x32_bf16 v[118:121], v[192:195], v[168:171], v[118:121]
	v_mfma_f32_16x16x32_bf16 v[114:117], v[200:203], v[168:171], v[114:117]
	v_mfma_f32_16x16x32_bf16 v[92:95], v[192:195], v[176:179], v[92:95]
	v_mfma_f32_16x16x32_bf16 v[88:91], v[200:203], v[176:179], v[88:91]
	v_mfma_f32_16x16x32_bf16 v[84:87], v[192:195], v[184:187], v[84:87]
	v_mfma_f32_16x16x32_bf16 v[80:83], v[200:203], v[184:187], v[80:83]
	s_setprio 0
	s_mov_b32 m0, s28
	s_barrier
	ds_read_b128 v[156:159], v154 offset:16384
	ds_read_b128 v[160:163], v154 offset:17408
	ds_read_b128 v[164:167], v154 offset:18432
	ds_read_b128 v[168:171], v154 offset:19456
	ds_read_b128 v[172:175], v154 offset:20480
	ds_read_b128 v[176:179], v154 offset:21504
	ds_read_b128 v[180:183], v154 offset:22528
	ds_read_b128 v[184:187], v154 offset:23552
	buffer_load_dwordx4 v149, s[72:75], s55 offen lds
	s_mov_b32 m0, s31
	s_nop 0
	buffer_load_dwordx4 v151, s[72:75], s55 offen lds
	s_waitcnt vmcnt(10)
	s_barrier
	s_waitcnt lgkmcnt(0)
	s_setprio 1
	s_waitcnt lgkmcnt(7)
	v_mfma_f32_16x16x32_bf16 v[76:79], v[220:223], v[156:159], v[76:79]
	v_mfma_f32_16x16x32_bf16 v[72:75], v[228:231], v[156:159], v[72:75]
	s_waitcnt lgkmcnt(5)
	v_mfma_f32_16x16x32_bf16 v[68:71], v[220:223], v[164:167], v[68:71]
	v_mfma_f32_16x16x32_bf16 v[64:67], v[228:231], v[164:167], v[64:67]
	s_waitcnt lgkmcnt(3)
	v_mfma_f32_16x16x32_bf16 v[28:31], v[220:223], v[172:175], v[28:31]
	v_mfma_f32_16x16x32_bf16 v[24:27], v[228:231], v[172:175], v[24:27]
	s_waitcnt lgkmcnt(1)
	v_mfma_f32_16x16x32_bf16 v[16:19], v[220:223], v[180:183], v[16:19]
	v_mfma_f32_16x16x32_bf16 v[8:11], v[228:231], v[180:183], v[8:11]
	v_mfma_f32_16x16x32_bf16 v[76:79], v[224:227], v[160:163], v[76:79]
	v_mfma_f32_16x16x32_bf16 v[72:75], v[232:235], v[160:163], v[72:75]
	v_mfma_f32_16x16x32_bf16 v[68:71], v[224:227], v[168:171], v[68:71]
	v_mfma_f32_16x16x32_bf16 v[64:67], v[232:235], v[168:171], v[64:67]
	v_mfma_f32_16x16x32_bf16 v[28:31], v[224:227], v[176:179], v[28:31]
	v_mfma_f32_16x16x32_bf16 v[24:27], v[232:235], v[176:179], v[24:27]
	s_waitcnt lgkmcnt(0)
	v_mfma_f32_16x16x32_bf16 v[16:19], v[224:227], v[184:187], v[16:19]
	v_mfma_f32_16x16x32_bf16 v[8:11], v[232:235], v[184:187], v[8:11]
	s_setprio 0
	s_barrier
	ds_read_b128 v[220:223], v153 offset:32768
	ds_read_b128 v[224:227], v153 offset:33792
	ds_read_b128 v[228:231], v153 offset:34816
	ds_read_b128 v[232:235], v153 offset:35840
	s_add_i32 s56, s53, 0x80000
	s_mov_b32 m0, s34
	s_nop 0
	buffer_load_dwordx4 v150, s[8:11], s56 offen lds
	s_mov_b32 m0, s35
	s_nop 0
	buffer_load_dwordx4 v152, s[8:11], s56 offen lds
	s_waitcnt vmcnt(10)
	s_barrier
	s_setprio 1
	v_mfma_f32_16x16x32_bf16 v[20:23], v[188:191], v[172:175], v[20:23]
	v_mfma_f32_16x16x32_bf16 v[12:15], v[196:199], v[172:175], v[12:15]
	v_mfma_f32_16x16x32_bf16 v[4:7], v[188:191], v[180:183], v[4:7]
	v_mfma_f32_16x16x32_bf16 v[0:3], v[196:199], v[180:183], v[0:3]
	v_mfma_f32_16x16x32_bf16 v[32:35], v[188:191], v[156:159], v[60:63]
	v_mfma_f32_16x16x32_bf16 v[36:39], v[196:199], v[156:159], v[56:59]
	v_mfma_f32_16x16x32_bf16 v[40:43], v[188:191], v[164:167], v[52:55]
	v_mfma_f32_16x16x32_bf16 v[44:47], v[196:199], v[164:167], v[48:51]
	v_mfma_f32_16x16x32_bf16 v[20:23], v[192:195], v[176:179], v[20:23]
	v_mfma_f32_16x16x32_bf16 v[12:15], v[200:203], v[176:179], v[12:15]
	v_mfma_f32_16x16x32_bf16 v[4:7], v[192:195], v[184:187], v[4:7]
	v_mfma_f32_16x16x32_bf16 v[0:3], v[200:203], v[184:187], v[0:3]
	v_mfma_f32_16x16x32_bf16 v[32:35], v[192:195], v[160:163], v[32:35]
	v_mfma_f32_16x16x32_bf16 v[36:39], v[200:203], v[160:163], v[36:39]
	v_mfma_f32_16x16x32_bf16 v[40:43], v[192:195], v[168:171], v[40:43]
	v_mfma_f32_16x16x32_bf16 v[44:47], v[200:203], v[168:171], v[44:47]
	s_setprio 0
	s_barrier
	s_add_i32 s55, s55, 0x80000
	s_mov_b32 m0, s36
	ds_read_b128 v[156:159], v154 offset:32768
	ds_read_b128 v[160:163], v154 offset:33792
	ds_read_b128 v[164:167], v154 offset:34816
	ds_read_b128 v[168:171], v154 offset:35840
	ds_read_b128 v[172:175], v154 offset:36864
	ds_read_b128 v[176:179], v154 offset:37888
	ds_read_b128 v[180:183], v154 offset:38912
	ds_read_b128 v[184:187], v154 offset:39936
	buffer_load_dwordx4 v149, s[72:75], s55 offen lds
	s_mov_b32 m0, s37
	s_nop 0
	buffer_load_dwordx4 v151, s[72:75], s55 offen lds
	s_waitcnt lgkmcnt(8)
	s_waitcnt vmcnt(10)
	s_barrier
	s_waitcnt lgkmcnt(0)
	s_setprio 1
	s_waitcnt lgkmcnt(7)
	v_mfma_f32_16x16x32_bf16 v[142:145], v[220:223], v[156:159], v[142:145]
	v_mfma_f32_16x16x32_bf16 v[138:141], v[228:231], v[156:159], v[138:141]
	s_waitcnt lgkmcnt(5)
	v_mfma_f32_16x16x32_bf16 v[134:137], v[220:223], v[164:167], v[134:137]
	v_mfma_f32_16x16x32_bf16 v[130:133], v[228:231], v[164:167], v[130:133]
	s_waitcnt lgkmcnt(3)
	v_mfma_f32_16x16x32_bf16 v[110:113], v[220:223], v[172:175], v[110:113]
	v_mfma_f32_16x16x32_bf16 v[106:109], v[228:231], v[172:175], v[106:109]
	s_waitcnt lgkmcnt(1)
	v_mfma_f32_16x16x32_bf16 v[102:105], v[220:223], v[180:183], v[102:105]
	v_mfma_f32_16x16x32_bf16 v[98:101], v[228:231], v[180:183], v[98:101]
	v_mfma_f32_16x16x32_bf16 v[142:145], v[224:227], v[160:163], v[142:145]
	v_mfma_f32_16x16x32_bf16 v[138:141], v[232:235], v[160:163], v[138:141]
	v_mfma_f32_16x16x32_bf16 v[134:137], v[224:227], v[168:171], v[134:137]
	v_mfma_f32_16x16x32_bf16 v[130:133], v[232:235], v[168:171], v[130:133]
	v_mfma_f32_16x16x32_bf16 v[110:113], v[224:227], v[176:179], v[110:113]
	v_mfma_f32_16x16x32_bf16 v[106:109], v[232:235], v[176:179], v[106:109]
	s_waitcnt lgkmcnt(0)
	v_mfma_f32_16x16x32_bf16 v[102:105], v[224:227], v[184:187], v[102:105]
	v_mfma_f32_16x16x32_bf16 v[98:101], v[232:235], v[184:187], v[98:101]
	s_setprio 0
	s_barrier
	s_or_b32 s55, s53, 0x80
	s_mov_b32 m0, s38
	ds_read_b128 v[188:191], v153 offset:49152
	ds_read_b128 v[192:195], v153 offset:50176
	ds_read_b128 v[196:199], v153 offset:51200
	ds_read_b128 v[200:203], v153 offset:52224
	buffer_load_dwordx4 v150, s[8:11], s55 offen lds
	s_mov_b32 m0, s39
	s_nop 0
	buffer_load_dwordx4 v152, s[8:11], s55 offen lds
	s_waitcnt vmcnt(10)
	s_barrier
	s_waitcnt lgkmcnt(0)
	s_setprio 1
	s_waitcnt lgkmcnt(3)
	v_mfma_f32_16x16x32_bf16 v[126:129], v[188:191], v[156:159], v[126:129]
	s_waitcnt lgkmcnt(1)
	v_mfma_f32_16x16x32_bf16 v[122:125], v[196:199], v[156:159], v[122:125]
	v_mfma_f32_16x16x32_bf16 v[118:121], v[188:191], v[164:167], v[118:121]
	v_mfma_f32_16x16x32_bf16 v[114:117], v[196:199], v[164:167], v[114:117]
	v_mfma_f32_16x16x32_bf16 v[92:95], v[188:191], v[172:175], v[92:95]
	v_mfma_f32_16x16x32_bf16 v[88:91], v[196:199], v[172:175], v[88:91]
	v_mfma_f32_16x16x32_bf16 v[84:87], v[188:191], v[180:183], v[84:87]
	v_mfma_f32_16x16x32_bf16 v[80:83], v[196:199], v[180:183], v[80:83]
	v_mfma_f32_16x16x32_bf16 v[126:129], v[192:195], v[160:163], v[126:129]
	s_waitcnt lgkmcnt(0)
	v_mfma_f32_16x16x32_bf16 v[122:125], v[200:203], v[160:163], v[122:125]
	v_mfma_f32_16x16x32_bf16 v[118:121], v[192:195], v[168:171], v[118:121]
	v_mfma_f32_16x16x32_bf16 v[114:117], v[200:203], v[168:171], v[114:117]
	v_mfma_f32_16x16x32_bf16 v[92:95], v[192:195], v[176:179], v[92:95]
	v_mfma_f32_16x16x32_bf16 v[88:91], v[200:203], v[176:179], v[88:91]
	v_mfma_f32_16x16x32_bf16 v[84:87], v[192:195], v[184:187], v[84:87]
	v_mfma_f32_16x16x32_bf16 v[80:83], v[200:203], v[184:187], v[80:83]
	s_setprio 0
	s_mov_b32 m0, s40
	s_barrier
	ds_read_b128 v[156:159], v154 offset:49152
	ds_read_b128 v[160:163], v154 offset:50176
	ds_read_b128 v[164:167], v154 offset:51200
	ds_read_b128 v[168:171], v154 offset:52224
	ds_read_b128 v[172:175], v154 offset:53248
	ds_read_b128 v[176:179], v154 offset:54272
	ds_read_b128 v[180:183], v154 offset:55296
	ds_read_b128 v[184:187], v154 offset:56320
	buffer_load_dwordx4 v149, s[72:75], s54 offen lds
	s_mov_b32 m0, s41
	s_nop 0
	buffer_load_dwordx4 v151, s[72:75], s54 offen lds
	s_waitcnt vmcnt(10)
	s_barrier
	s_waitcnt lgkmcnt(0)
	s_setprio 1
	s_waitcnt lgkmcnt(7)
	v_mfma_f32_16x16x32_bf16 v[76:79], v[220:223], v[156:159], v[76:79]
	v_mfma_f32_16x16x32_bf16 v[72:75], v[228:231], v[156:159], v[72:75]
	s_waitcnt lgkmcnt(5)
	v_mfma_f32_16x16x32_bf16 v[68:71], v[220:223], v[164:167], v[68:71]
	v_mfma_f32_16x16x32_bf16 v[64:67], v[228:231], v[164:167], v[64:67]
	s_waitcnt lgkmcnt(3)
	v_mfma_f32_16x16x32_bf16 v[28:31], v[220:223], v[172:175], v[28:31]
	v_mfma_f32_16x16x32_bf16 v[24:27], v[228:231], v[172:175], v[24:27]
	s_waitcnt lgkmcnt(1)
	v_mfma_f32_16x16x32_bf16 v[16:19], v[220:223], v[180:183], v[16:19]
	v_mfma_f32_16x16x32_bf16 v[8:11], v[228:231], v[180:183], v[8:11]
	v_mfma_f32_16x16x32_bf16 v[76:79], v[224:227], v[160:163], v[76:79]
	v_mfma_f32_16x16x32_bf16 v[72:75], v[232:235], v[160:163], v[72:75]
	v_mfma_f32_16x16x32_bf16 v[68:71], v[224:227], v[168:171], v[68:71]
	v_mfma_f32_16x16x32_bf16 v[64:67], v[232:235], v[168:171], v[64:67]
	v_mfma_f32_16x16x32_bf16 v[28:31], v[224:227], v[176:179], v[28:31]
	v_mfma_f32_16x16x32_bf16 v[24:27], v[232:235], v[176:179], v[24:27]
	s_waitcnt lgkmcnt(0)
	v_mfma_f32_16x16x32_bf16 v[16:19], v[224:227], v[184:187], v[16:19]
	v_mfma_f32_16x16x32_bf16 v[8:11], v[232:235], v[184:187], v[8:11]
	s_setprio 0
	s_barrier
	ds_read_b128 v[220:223], v153
	ds_read_b128 v[224:227], v153 offset:1024
	ds_read_b128 v[228:231], v153 offset:2048
	ds_read_b128 v[232:235], v153 offset:3072
	s_add_i32 s53, s53, 0x80080
	s_mov_b32 m0, s42
	s_nop 0
	buffer_load_dwordx4 v150, s[8:11], s53 offen lds
	s_mov_b32 m0, s43
	s_nop 0
	buffer_load_dwordx4 v152, s[8:11], s53 offen lds
	s_waitcnt vmcnt(10)
	s_barrier
	s_setprio 1
	v_mfma_f32_16x16x32_bf16 v[32:35], v[188:191], v[156:159], v[32:35]
	v_mfma_f32_16x16x32_bf16 v[60:63], v[192:195], v[160:163], v[32:35]
	v_mfma_f32_16x16x32_bf16 v[32:35], v[196:199], v[156:159], v[36:39]
	v_mfma_f32_16x16x32_bf16 v[56:59], v[200:203], v[160:163], v[32:35]
	v_mfma_f32_16x16x32_bf16 v[32:35], v[188:191], v[164:167], v[40:43]
	v_mfma_f32_16x16x32_bf16 v[52:55], v[192:195], v[168:171], v[32:35]
	v_mfma_f32_16x16x32_bf16 v[32:35], v[196:199], v[164:167], v[44:47]
	v_mfma_f32_16x16x32_bf16 v[20:23], v[188:191], v[172:175], v[20:23]
	v_mfma_f32_16x16x32_bf16 v[12:15], v[196:199], v[172:175], v[12:15]
	v_mfma_f32_16x16x32_bf16 v[4:7], v[188:191], v[180:183], v[4:7]
	v_mfma_f32_16x16x32_bf16 v[0:3], v[196:199], v[180:183], v[0:3]
	v_mfma_f32_16x16x32_bf16 v[48:51], v[200:203], v[168:171], v[32:35]
	v_mfma_f32_16x16x32_bf16 v[20:23], v[192:195], v[176:179], v[20:23]
	v_mfma_f32_16x16x32_bf16 v[12:15], v[200:203], v[176:179], v[12:15]
	v_mfma_f32_16x16x32_bf16 v[4:7], v[192:195], v[184:187], v[4:7]
	v_mfma_f32_16x16x32_bf16 v[0:3], v[200:203], v[184:187], v[0:3]
	s_setprio 0
	s_add_i32 s52, s52, 2
	s_addk_i32 s50, 0x100
	s_addk_i32 s51, 0x100
	s_cmp_gt_u32 s52, 29
	s_barrier
	s_cbranch_scc0 .LBB0_1496
	s_waitcnt lgkmcnt(0)
	s_getreg_b32 s10, hwreg(HW_REG_HW_ID, 0, 6)
	s_and_b32 s10, s10, 63
	s_lshl_b32 s10, s10, 2
	s_add_i32 s10, s10, 0
	s_add_i32 s10, s10, 0x20010
	v_mov_b32_e32 v32, s10
	ds_read_b32 v32, v32
	s_min_i32 s11, s2, 64
	s_ashr_i32 s11, s11, 3
	v_mbcnt_lo_u32_b32 v155, -1, 0
	v_mbcnt_hi_u32_b32 v155, -1, v155
	s_mov_b32 s51, s23
	s_waitcnt lgkmcnt(0)
	v_readfirstlane_b32 s10, v32
	v_lshrrev_b32_e32 v34, 1, v155
	v_and_b32_e32 v157, 24, v34
	v_lshl_or_b32 v146, s10, 6, v155
	s_lshl_b32 s10, s47, 8
	s_mul_hi_i32 s47, s11, 0xc000
	s_mul_i32 s11, s11, 0xc000
	s_add_u32 s50, s0, s11
	s_addc_u32 s47, s24, s47
	s_ashr_i32 s11, s10, 31
	s_lshl_b64 s[48:49], s[10:11], 2
	v_lshrrev_b32_e32 v32, 1, v146
	s_add_u32 s48, s50, s48
	v_and_b32_e32 v156, 0x60, v32
	s_addc_u32 s49, s47, s49
	v_lshlrev_b32_e32 v96, 2, v156
	v_lshl_add_u64 v[32:33], s[48:49], 0, v[96:97]
	v_lshlrev_b32_e32 v96, 2, v157
	v_lshl_add_u64 v[36:37], v[32:33], 0, v[96:97]
	v_ashrrev_i32_e32 v96, 2, v146
	s_lshl_b32 s48, s2, 8
	v_and_b32_e32 v146, 0xffffffc0, v96
	s_ashr_i32 s49, s48, 31
	v_ashrrev_i32_e32 v147, 31, v146
	v_lshl_add_u64 v[146:147], v[146:147], 0, s[48:49]
	v_and_or_b32 v146, v155, 15, v146
	v_lshlrev_b64 v[146:147], 12, v[146:147]
	v_lshl_add_u64 v[146:147], s[12:13], 0, v[146:147]
	v_lshl_add_u64 v[146:147], s[10:11], 1, v[146:147]
	v_lshlrev_b32_e32 v96, 1, v156
	v_lshl_add_u64 v[146:147], v[146:147], 0, v[96:97]
	v_lshlrev_b32_e32 v96, 1, v157
	v_lshl_add_u64 v[146:147], v[146:147], 0, v[96:97]
	global_load_dwordx4 v[40:43], v[36:37], off offset:16
	global_load_dwordx4 v[44:47], v[36:37], off
	global_load_dwordx4 v[32:35], v[36:37], off offset:528
	s_nop 0
	global_load_dwordx4 v[36:39], v[36:37], off offset:512
	s_mov_b32 s2, 0x10000
	global_load_dwordx4 v[156:159], v[146:147], off
	v_add_co_u32_e32 v176, vcc, s2, v146
	s_mov_b32 s2, 0x30000
	s_nop 0
	v_addc_co_u32_e32 v177, vcc, 0, v147, vcc
	s_mov_b32 s47, s20
	s_mov_b32 s50, s22
	s_waitcnt vmcnt(0)
	v_lshlrev_b32_e32 v160, 16, v156
	v_and_b32_e32 v161, 0xffff0000, v156
	v_lshlrev_b32_e32 v162, 16, v157
	v_and_b32_e32 v163, 0xffff0000, v157
	v_lshlrev_b32_e32 v164, 16, v158
	v_and_b32_e32 v165, 0xffff0000, v158
	v_lshlrev_b32_e32 v166, 16, v159
	v_and_b32_e32 v167, 0xffff0000, v159
	global_load_dwordx4 v[156:159], v[146:147], off offset:256
	v_pk_fma_f32 v[144:145], v[144:145], v[46:47], v[162:163]
	v_pk_fma_f32 v[142:143], v[142:143], v[44:45], v[160:161]
	v_pk_fma_f32 v[160:161], v[140:141], v[42:43], v[166:167]
	v_pk_fma_f32 v[140:141], v[138:139], v[40:41], v[164:165]
	v_cvt_pk_bf16_f32 v138, v142, v143
	v_cvt_pk_bf16_f32 v139, v144, v145
	v_cvt_pk_bf16_f32 v140, v140, v141
	v_cvt_pk_bf16_f32 v141, v160, v161
	global_store_dwordx4 v[146:147], v[138:141], off
	s_waitcnt vmcnt(1)
	v_lshlrev_b32_e32 v168, 16, v156
	v_and_b32_e32 v169, 0xffff0000, v156
	v_lshlrev_b32_e32 v170, 16, v157
	v_and_b32_e32 v171, 0xffff0000, v157
	v_lshlrev_b32_e32 v172, 16, v158
	v_and_b32_e32 v173, 0xffff0000, v158
	v_lshlrev_b32_e32 v174, 16, v159
	v_and_b32_e32 v175, 0xffff0000, v159
	global_load_dwordx4 v[156:159], v[176:177], off
	v_pk_fma_f32 v[128:129], v[128:129], v[38:39], v[170:171]
	v_pk_fma_f32 v[126:127], v[126:127], v[36:37], v[168:169]
	v_pk_fma_f32 v[138:139], v[124:125], v[34:35], v[174:175]
	v_pk_fma_f32 v[124:125], v[122:123], v[32:33], v[172:173]
	v_cvt_pk_bf16_f32 v122, v126, v127
	v_cvt_pk_bf16_f32 v123, v128, v129
	v_cvt_pk_bf16_f32 v124, v124, v125
	v_cvt_pk_bf16_f32 v125, v138, v139
	global_store_dwordx4 v[146:147], v[122:125], off offset:256
	s_waitcnt vmcnt(1)
	v_lshlrev_b32_e32 v178, 16, v156
	v_and_b32_e32 v179, 0xffff0000, v156
	v_lshlrev_b32_e32 v180, 16, v157
	v_and_b32_e32 v181, 0xffff0000, v157
	v_lshlrev_b32_e32 v182, 16, v158
	v_and_b32_e32 v183, 0xffff0000, v158
	v_lshlrev_b32_e32 v184, 16, v159
	v_and_b32_e32 v185, 0xffff0000, v159
	global_load_dwordx4 v[156:159], v[176:177], off offset:256
	v_pk_fma_f32 v[124:125], v[136:137], v[46:47], v[180:181]
	v_pk_fma_f32 v[122:123], v[134:135], v[44:45], v[178:179]
	v_pk_fma_f32 v[126:127], v[132:133], v[42:43], v[184:185]
	v_pk_fma_f32 v[128:129], v[130:131], v[40:41], v[182:183]
	v_cvt_pk_bf16_f32 v122, v122, v123
	v_cvt_pk_bf16_f32 v123, v124, v125
	v_cvt_pk_bf16_f32 v124, v128, v129
	v_cvt_pk_bf16_f32 v125, v126, v127
	global_store_dwordx4 v[176:177], v[122:125], off
	s_waitcnt vmcnt(1)
	v_lshlrev_b32_e32 v186, 16, v156
	v_and_b32_e32 v187, 0xffff0000, v156
	v_lshlrev_b32_e32 v156, 16, v157
	v_and_b32_e32 v157, 0xffff0000, v157
	v_lshlrev_b32_e32 v188, 16, v158
	v_and_b32_e32 v189, 0xffff0000, v158
	v_lshlrev_b32_e32 v158, 16, v159
	v_and_b32_e32 v159, 0xffff0000, v159
	v_pk_fma_f32 v[118:119], v[118:119], v[36:37], v[186:187]
	v_pk_fma_f32 v[120:121], v[120:121], v[38:39], v[156:157]
	v_pk_fma_f32 v[122:123], v[116:117], v[34:35], v[158:159]
	v_pk_fma_f32 v[116:117], v[114:115], v[32:33], v[188:189]
	v_cvt_pk_bf16_f32 v114, v118, v119
	v_add_co_u32_e32 v118, vcc, s75, v146
	v_cvt_pk_bf16_f32 v115, v120, v121
	v_cvt_pk_bf16_f32 v116, v116, v117
	v_cvt_pk_bf16_f32 v117, v122, v123
	v_addc_co_u32_e32 v119, vcc, 0, v147, vcc
	global_store_dwordx4 v[176:177], v[114:117], off offset:256
	global_load_dwordx4 v[114:117], v[118:119], off
	v_add_co_u32_e32 v136, vcc, s2, v146
	s_mov_b32 s2, 0x80000
	s_nop 0
	v_addc_co_u32_e32 v137, vcc, 0, v147, vcc
	s_waitcnt vmcnt(0)
	v_lshlrev_b32_e32 v120, 16, v114
	v_and_b32_e32 v121, 0xffff0000, v114
	v_lshlrev_b32_e32 v122, 16, v115
	v_and_b32_e32 v123, 0xffff0000, v115
	v_lshlrev_b32_e32 v124, 16, v116
	v_and_b32_e32 v125, 0xffff0000, v116
	v_lshlrev_b32_e32 v126, 16, v117
	v_and_b32_e32 v127, 0xffff0000, v117
	global_load_dwordx4 v[114:117], v[118:119], off offset:256
	v_pk_fma_f32 v[112:113], v[112:113], v[46:47], v[122:123]
	v_pk_fma_f32 v[110:111], v[110:111], v[44:45], v[120:121]
	v_pk_fma_f32 v[120:121], v[108:109], v[42:43], v[126:127]
	v_pk_fma_f32 v[108:109], v[106:107], v[40:41], v[124:125]
	v_cvt_pk_bf16_f32 v106, v110, v111
	v_cvt_pk_bf16_f32 v107, v112, v113
	v_cvt_pk_bf16_f32 v108, v108, v109
	v_cvt_pk_bf16_f32 v109, v120, v121
	global_store_dwordx4 v[118:119], v[106:109], off
	s_waitcnt vmcnt(1)
	v_lshlrev_b32_e32 v128, 16, v114
	v_and_b32_e32 v129, 0xffff0000, v114
	v_lshlrev_b32_e32 v130, 16, v115
	v_and_b32_e32 v131, 0xffff0000, v115
	v_lshlrev_b32_e32 v132, 16, v116
	v_and_b32_e32 v133, 0xffff0000, v116
	v_lshlrev_b32_e32 v134, 16, v117
	v_and_b32_e32 v135, 0xffff0000, v117
	global_load_dwordx4 v[114:117], v[136:137], off
	v_pk_fma_f32 v[94:95], v[94:95], v[38:39], v[130:131]
	v_pk_fma_f32 v[92:93], v[92:93], v[36:37], v[128:129]
	v_pk_fma_f32 v[106:107], v[90:91], v[34:35], v[134:135]
	v_pk_fma_f32 v[90:91], v[88:89], v[32:33], v[132:133]
	v_cvt_pk_bf16_f32 v88, v92, v93
	v_cvt_pk_bf16_f32 v89, v94, v95
	v_cvt_pk_bf16_f32 v90, v90, v91
	v_cvt_pk_bf16_f32 v91, v106, v107
	global_store_dwordx4 v[118:119], v[88:91], off offset:256
	s_waitcnt vmcnt(1)
	v_lshlrev_b32_e32 v138, 16, v114
	v_and_b32_e32 v139, 0xffff0000, v114
	v_lshlrev_b32_e32 v140, 16, v115
	v_and_b32_e32 v141, 0xffff0000, v115
	v_lshlrev_b32_e32 v142, 16, v116
	v_and_b32_e32 v143, 0xffff0000, v116
	v_lshlrev_b32_e32 v144, 16, v117
	v_and_b32_e32 v145, 0xffff0000, v117
	global_load_dwordx4 v[114:117], v[136:137], off offset:256
	v_pk_fma_f32 v[90:91], v[104:105], v[46:47], v[140:141]
	v_pk_fma_f32 v[88:89], v[102:103], v[44:45], v[138:139]
	v_pk_fma_f32 v[92:93], v[100:101], v[42:43], v[144:145]
	v_pk_fma_f32 v[94:95], v[98:99], v[40:41], v[142:143]
	v_cvt_pk_bf16_f32 v88, v88, v89
	v_cvt_pk_bf16_f32 v89, v90, v91
	v_cvt_pk_bf16_f32 v90, v94, v95
	v_cvt_pk_bf16_f32 v91, v92, v93
	global_store_dwordx4 v[136:137], v[88:91], off
	s_waitcnt vmcnt(1)
	v_lshlrev_b32_e32 v156, 16, v114
	v_and_b32_e32 v157, 0xffff0000, v114
	v_lshlrev_b32_e32 v114, 16, v115
	v_and_b32_e32 v115, 0xffff0000, v115
	v_lshlrev_b32_e32 v158, 16, v116
	v_and_b32_e32 v159, 0xffff0000, v116
	v_lshlrev_b32_e32 v116, 16, v117
	v_and_b32_e32 v117, 0xffff0000, v117
	v_pk_fma_f32 v[86:87], v[86:87], v[38:39], v[114:115]
	v_pk_fma_f32 v[84:85], v[84:85], v[36:37], v[156:157]
	v_pk_fma_f32 v[88:89], v[82:83], v[34:35], v[116:117]
	v_pk_fma_f32 v[82:83], v[80:81], v[32:33], v[158:159]
	v_cvt_pk_bf16_f32 v80, v84, v85
	v_cvt_pk_bf16_f32 v81, v86, v87
	v_cvt_pk_bf16_f32 v82, v82, v83
	v_cvt_pk_bf16_f32 v83, v88, v89
	global_store_dwordx4 v[136:137], v[80:83], off offset:256
	s_nop 1
	v_add_co_u32_e32 v80, vcc, s2, v146
	s_mov_b32 s2, 0x90000
	s_nop 0
	v_addc_co_u32_e32 v81, vcc, 0, v147, vcc
	global_load_dwordx4 v[82:85], v[80:81], off
	v_add_co_u32_e32 v104, vcc, s2, v146
	s_mov_b32 s2, 0xa0000
	s_nop 0
	v_addc_co_u32_e32 v105, vcc, 0, v147, vcc
	s_waitcnt vmcnt(0)
	v_lshlrev_b32_e32 v86, 16, v82
	v_and_b32_e32 v87, 0xffff0000, v82
	v_lshlrev_b32_e32 v88, 16, v83
	v_and_b32_e32 v89, 0xffff0000, v83
	v_lshlrev_b32_e32 v90, 16, v84
	v_and_b32_e32 v91, 0xffff0000, v84
	v_lshlrev_b32_e32 v92, 16, v85
	v_and_b32_e32 v93, 0xffff0000, v85
	global_load_dwordx4 v[82:85], v[80:81], off offset:256
	v_pk_fma_f32 v[78:79], v[78:79], v[46:47], v[88:89]
	v_pk_fma_f32 v[76:77], v[76:77], v[44:45], v[86:87]
	v_pk_fma_f32 v[86:87], v[74:75], v[42:43], v[92:93]
	v_pk_fma_f32 v[74:75], v[72:73], v[40:41], v[90:91]
	v_cvt_pk_bf16_f32 v72, v76, v77
	v_cvt_pk_bf16_f32 v73, v78, v79
	v_cvt_pk_bf16_f32 v74, v74, v75
	v_cvt_pk_bf16_f32 v75, v86, v87
	global_store_dwordx4 v[80:81], v[72:75], off
	s_waitcnt vmcnt(1)
	v_lshlrev_b32_e32 v94, 16, v82
	v_and_b32_e32 v95, 0xffff0000, v82
	v_lshlrev_b32_e32 v98, 16, v83
	v_and_b32_e32 v99, 0xffff0000, v83
	v_lshlrev_b32_e32 v100, 16, v84
	v_and_b32_e32 v101, 0xffff0000, v84
	v_lshlrev_b32_e32 v102, 16, v85
	v_and_b32_e32 v103, 0xffff0000, v85
	global_load_dwordx4 v[82:85], v[104:105], off
	v_pk_fma_f32 v[62:63], v[62:63], v[38:39], v[98:99]
	v_pk_fma_f32 v[60:61], v[60:61], v[36:37], v[94:95]
	v_pk_fma_f32 v[72:73], v[58:59], v[34:35], v[102:103]
	v_pk_fma_f32 v[58:59], v[56:57], v[32:33], v[100:101]
	v_cvt_pk_bf16_f32 v56, v60, v61
	v_cvt_pk_bf16_f32 v57, v62, v63
	v_cvt_pk_bf16_f32 v58, v58, v59
	v_cvt_pk_bf16_f32 v59, v72, v73
	global_store_dwordx4 v[80:81], v[56:59], off offset:256
	s_waitcnt vmcnt(1)
	v_lshlrev_b32_e32 v106, 16, v82
	v_and_b32_e32 v107, 0xffff0000, v82
	v_lshlrev_b32_e32 v108, 16, v83
	v_and_b32_e32 v109, 0xffff0000, v83
	v_lshlrev_b32_e32 v110, 16, v84
	v_and_b32_e32 v111, 0xffff0000, v84
	v_lshlrev_b32_e32 v112, 16, v85
	v_and_b32_e32 v113, 0xffff0000, v85
	global_load_dwordx4 v[82:85], v[104:105], off offset:256
	v_pk_fma_f32 v[58:59], v[70:71], v[46:47], v[108:109]
	v_pk_fma_f32 v[56:57], v[68:69], v[44:45], v[106:107]
	v_pk_fma_f32 v[60:61], v[66:67], v[42:43], v[112:113]
	v_pk_fma_f32 v[62:63], v[64:65], v[40:41], v[110:111]
	v_cvt_pk_bf16_f32 v56, v56, v57
	v_cvt_pk_bf16_f32 v57, v58, v59
	v_cvt_pk_bf16_f32 v58, v62, v63
	v_cvt_pk_bf16_f32 v59, v60, v61
	global_store_dwordx4 v[104:105], v[56:59], off
	s_waitcnt vmcnt(1)
	v_lshlrev_b32_e32 v114, 16, v82
	v_and_b32_e32 v115, 0xffff0000, v82
	v_lshlrev_b32_e32 v82, 16, v83
	v_and_b32_e32 v83, 0xffff0000, v83
	v_lshlrev_b32_e32 v116, 16, v84
	v_and_b32_e32 v117, 0xffff0000, v84
	v_lshlrev_b32_e32 v84, 16, v85
	v_and_b32_e32 v85, 0xffff0000, v85
	v_pk_fma_f32 v[52:53], v[52:53], v[36:37], v[114:115]
	v_pk_fma_f32 v[54:55], v[54:55], v[38:39], v[82:83]
	v_pk_fma_f32 v[56:57], v[50:51], v[34:35], v[84:85]
	v_pk_fma_f32 v[50:51], v[48:49], v[32:33], v[116:117]
	v_cvt_pk_bf16_f32 v48, v52, v53
	v_add_co_u32_e32 v52, vcc, s2, v146
	v_cvt_pk_bf16_f32 v49, v54, v55
	v_cvt_pk_bf16_f32 v50, v50, v51
	v_cvt_pk_bf16_f32 v51, v56, v57
	v_addc_co_u32_e32 v53, vcc, 0, v147, vcc
	global_store_dwordx4 v[104:105], v[48:51], off offset:256
	global_load_dwordx4 v[48:51], v[52:53], off
	s_mov_b32 s2, 0xb0000
	v_add_co_u32_e32 v62, vcc, s2, v146
	s_mov_b32 s2, s21
	s_nop 0
	v_addc_co_u32_e32 v63, vcc, 0, v147, vcc
	s_and_b64 vcc, exec, s[4:5]
	s_waitcnt vmcnt(0)
	v_lshlrev_b32_e32 v56, 16, v48
	v_and_b32_e32 v57, 0xffff0000, v48
	v_lshlrev_b32_e32 v60, 16, v49
	v_and_b32_e32 v61, 0xffff0000, v49
	v_lshlrev_b32_e32 v54, 16, v50
	v_and_b32_e32 v55, 0xffff0000, v50
	v_lshlrev_b32_e32 v58, 16, v51
	v_and_b32_e32 v59, 0xffff0000, v51
	global_load_dwordx4 v[48:51], v[52:53], off offset:256
	v_pk_fma_f32 v[30:31], v[30:31], v[46:47], v[60:61]
	v_pk_fma_f32 v[28:29], v[28:29], v[44:45], v[56:57]
	v_pk_fma_f32 v[56:57], v[26:27], v[42:43], v[58:59]
	v_pk_fma_f32 v[26:27], v[24:25], v[40:41], v[54:55]
	v_cvt_pk_bf16_f32 v24, v28, v29
	v_cvt_pk_bf16_f32 v25, v30, v31
	v_cvt_pk_bf16_f32 v26, v26, v27
	v_cvt_pk_bf16_f32 v27, v56, v57
	global_store_dwordx4 v[52:53], v[24:27], off
	s_waitcnt vmcnt(1)
	v_lshlrev_b32_e32 v66, 16, v48
	v_and_b32_e32 v67, 0xffff0000, v48
	v_lshlrev_b32_e32 v70, 16, v49
	v_and_b32_e32 v71, 0xffff0000, v49
	v_lshlrev_b32_e32 v64, 16, v50
	v_and_b32_e32 v65, 0xffff0000, v50
	v_lshlrev_b32_e32 v68, 16, v51
	v_and_b32_e32 v69, 0xffff0000, v51
	global_load_dwordx4 v[48:51], v[62:63], off
	v_pk_fma_f32 v[22:23], v[22:23], v[38:39], v[70:71]
	v_pk_fma_f32 v[20:21], v[20:21], v[36:37], v[66:67]
	v_pk_fma_f32 v[24:25], v[14:15], v[34:35], v[68:69]
	v_pk_fma_f32 v[14:15], v[12:13], v[32:33], v[64:65]
	v_cvt_pk_bf16_f32 v12, v20, v21
	v_cvt_pk_bf16_f32 v13, v22, v23
	v_cvt_pk_bf16_f32 v14, v14, v15
	v_cvt_pk_bf16_f32 v15, v24, v25
	global_store_dwordx4 v[52:53], v[12:15], off offset:256
	s_waitcnt vmcnt(1)
	v_lshlrev_b32_e32 v74, 16, v48
	v_and_b32_e32 v75, 0xffff0000, v48
	v_lshlrev_b32_e32 v78, 16, v49
	v_and_b32_e32 v79, 0xffff0000, v49
	v_lshlrev_b32_e32 v72, 16, v50
	v_and_b32_e32 v73, 0xffff0000, v50
	v_lshlrev_b32_e32 v76, 16, v51
	v_and_b32_e32 v77, 0xffff0000, v51
	global_load_dwordx4 v[48:51], v[62:63], off offset:256
	v_pk_fma_f32 v[12:13], v[18:19], v[46:47], v[78:79]
	v_pk_fma_f32 v[14:15], v[16:17], v[44:45], v[74:75]
	v_pk_fma_f32 v[16:17], v[10:11], v[42:43], v[76:77]
	v_pk_fma_f32 v[10:11], v[8:9], v[40:41], v[72:73]
	v_cvt_pk_bf16_f32 v8, v14, v15
	v_cvt_pk_bf16_f32 v9, v12, v13
	v_cvt_pk_bf16_f32 v10, v10, v11
	v_cvt_pk_bf16_f32 v11, v16, v17
	global_store_dwordx4 v[62:63], v[8:11], off
	s_waitcnt vmcnt(1)
	v_lshlrev_b32_e32 v80, 16, v48
	v_and_b32_e32 v81, 0xffff0000, v48
	v_lshlrev_b32_e32 v48, 16, v49
	v_and_b32_e32 v49, 0xffff0000, v49
	v_lshlrev_b32_e32 v82, 16, v50
	v_and_b32_e32 v83, 0xffff0000, v50
	v_lshlrev_b32_e32 v50, 16, v51
	v_and_b32_e32 v51, 0xffff0000, v51
	v_pk_fma_f32 v[6:7], v[6:7], v[38:39], v[48:49]
	v_pk_fma_f32 v[4:5], v[4:5], v[36:37], v[80:81]
	v_pk_fma_f32 v[8:9], v[2:3], v[34:35], v[50:51]
	v_pk_fma_f32 v[2:3], v[0:1], v[32:33], v[82:83]
	v_cvt_pk_bf16_f32 v0, v4, v5
	v_cvt_pk_bf16_f32 v1, v6, v7
	v_cvt_pk_bf16_f32 v2, v2, v3
	v_cvt_pk_bf16_f32 v3, v8, v9
	global_store_dwordx4 v[62:63], v[0:3], off offset:256
	s_cbranch_vccz .LBB0_1490
	s_branch .LBB0_1499

.LBB0_1513:
	v_mov_b64_e32 v[0:1], s[18:19]
	v_cmp_lt_i64_e32 vcc, s[10:11], v[0:1]
	s_lshl_b32 s16, s15, 20
	s_and_b64 s[10:11], vcc, exec
	s_cselect_b32 s47, s16, s49
	s_lshl_b32 s17, s14, 20
	s_and_b64 s[10:11], vcc, exec
	v_mov_b32_e32 v0, 0
	s_cselect_b32 s48, s17, s50
	s_add_i32 s49, s49, 0x80080
	s_addk_i32 s50, 0x100
	s_mov_b32 s51, -2
	v_mov_b32_e32 v1, v0
	v_mov_b32_e32 v2, v0
	v_mov_b32_e32 v3, v0
	v_mov_b32_e32 v4, v0
	v_mov_b32_e32 v5, v0
	v_mov_b32_e32 v6, v0
	v_mov_b32_e32 v7, v0
	v_mov_b32_e32 v8, v0
	v_mov_b32_e32 v9, v0
	v_mov_b32_e32 v10, v0
	v_mov_b32_e32 v11, v0
	v_mov_b32_e32 v12, v0
	v_mov_b32_e32 v13, v0
	v_mov_b32_e32 v14, v0
	v_mov_b32_e32 v15, v0
	v_mov_b32_e32 v32, v0
	v_mov_b32_e32 v33, v0
	v_mov_b32_e32 v34, v0
	v_mov_b32_e32 v35, v0
	v_mov_b32_e32 v36, v0
	v_mov_b32_e32 v37, v0
	v_mov_b32_e32 v38, v0
	v_mov_b32_e32 v39, v0
	v_mov_b32_e32 v40, v0
	v_mov_b32_e32 v41, v0
	v_mov_b32_e32 v42, v0
	v_mov_b32_e32 v43, v0
	v_mov_b32_e32 v44, v0
	v_mov_b32_e32 v45, v0
	v_mov_b32_e32 v46, v0
	v_mov_b32_e32 v47, v0
	s_waitcnt vmcnt(14)
	v_mov_b32_e32 v16, v0
	v_mov_b32_e32 v17, v0
	v_mov_b32_e32 v18, v0
	v_mov_b32_e32 v19, v0
	v_mov_b32_e32 v20, v0
	v_mov_b32_e32 v21, v0
	v_mov_b32_e32 v22, v0
	v_mov_b32_e32 v23, v0
	v_mov_b32_e32 v24, v0
	v_mov_b32_e32 v25, v0
	v_mov_b32_e32 v26, v0
	v_mov_b32_e32 v27, v0
	v_mov_b32_e32 v28, v0
	v_mov_b32_e32 v29, v0
	v_mov_b32_e32 v30, v0
	v_mov_b32_e32 v31, v0
	v_mov_b32_e32 v48, v0
	v_mov_b32_e32 v49, v0
	v_mov_b32_e32 v50, v0
	v_mov_b32_e32 v51, v0
	v_mov_b32_e32 v52, v0
	v_mov_b32_e32 v53, v0
	v_mov_b32_e32 v54, v0
	v_mov_b32_e32 v55, v0
	v_mov_b32_e32 v56, v0
	v_mov_b32_e32 v57, v0
	v_mov_b32_e32 v58, v0
	v_mov_b32_e32 v59, v0
	v_mov_b32_e32 v60, v0
	v_mov_b32_e32 v61, v0
	v_mov_b32_e32 v62, v0
	v_mov_b32_e32 v63, v0
	v_mov_b32_e32 v80, v0
	v_mov_b32_e32 v81, v0
	v_mov_b32_e32 v82, v0
	v_mov_b32_e32 v83, v0
	v_mov_b32_e32 v84, v0
	v_mov_b32_e32 v85, v0
	v_mov_b32_e32 v86, v0
	v_mov_b32_e32 v87, v0
	v_mov_b32_e32 v88, v0
	v_mov_b32_e32 v89, v0
	v_mov_b32_e32 v90, v0
	v_mov_b32_e32 v91, v0
	v_mov_b32_e32 v92, v0
	v_mov_b32_e32 v93, v0
	v_mov_b32_e32 v94, v0
	v_mov_b32_e32 v95, v0
	v_mov_b32_e32 v114, v0
	v_mov_b32_e32 v115, v0
	v_mov_b32_e32 v116, v0
	v_mov_b32_e32 v117, v0
	v_mov_b32_e32 v118, v0
	v_mov_b32_e32 v119, v0
	v_mov_b32_e32 v120, v0
	v_mov_b32_e32 v121, v0
	v_mov_b32_e32 v122, v0
	v_mov_b32_e32 v123, v0
	v_mov_b32_e32 v124, v0
	v_mov_b32_e32 v125, v0
	v_mov_b32_e32 v126, v0
	v_mov_b32_e32 v127, v0
	v_mov_b32_e32 v128, v0
	v_mov_b32_e32 v129, v0
	v_mov_b32_e32 v98, v0
	v_mov_b32_e32 v99, v0
	v_mov_b32_e32 v100, v0
	v_mov_b32_e32 v101, v0
	v_mov_b32_e32 v102, v0
	v_mov_b32_e32 v103, v0
	v_mov_b32_e32 v104, v0
	v_mov_b32_e32 v105, v0
	v_mov_b32_e32 v106, v0
	v_mov_b32_e32 v107, v0
	v_mov_b32_e32 v108, v0
	v_mov_b32_e32 v109, v0
	v_mov_b32_e32 v110, v0
	v_mov_b32_e32 v111, v0
	v_mov_b32_e32 v112, v0
	v_mov_b32_e32 v113, v0
	v_mov_b32_e32 v130, v0
	v_mov_b32_e32 v131, v0
	v_mov_b32_e32 v132, v0
	v_mov_b32_e32 v133, v0
	v_mov_b32_e32 v134, v0
	v_mov_b32_e32 v135, v0
	v_mov_b32_e32 v136, v0
	v_mov_b32_e32 v137, v0
	v_mov_b32_e32 v138, v0
	v_mov_b32_e32 v139, v0
	v_mov_b32_e32 v140, v0
	v_mov_b32_e32 v141, v0
	v_mov_b32_e32 v142, v0
	v_mov_b32_e32 v143, v0
	v_mov_b32_e32 v144, v0
	v_mov_b32_e32 v145, v0
	ds_read_b128 v[220:223], v154
	ds_read_b128 v[224:227], v154 offset:1024
	ds_read_b128 v[228:231], v154 offset:2048
	ds_read_b128 v[232:235], v154 offset:3072
.LBB0_1514:
	s_add_i32 s10, s49, 0xfff80080
	s_cmp_eq_u32 s51, 28
	s_cselect_b32 s54, s47, s10
	s_cselect_b32 s52, s48, s50
	s_or_b32 s53, s54, 0x80
	s_mov_b32 m0, s41
	ds_read_b128 v[146:149], v155
	ds_read_b128 v[156:159], v155 offset:1024
	ds_read_b128 v[160:163], v155 offset:2048
	ds_read_b128 v[164:167], v155 offset:3072
	ds_read_b128 v[168:171], v155 offset:4096
	ds_read_b128 v[172:175], v155 offset:5120
	ds_read_b128 v[176:179], v155 offset:6144
	ds_read_b128 v[180:183], v155 offset:7168
	buffer_load_dwordx4 v150, s[72:75], s49 offen lds
	s_mov_b32 m0, s42
	s_nop 0
	buffer_load_dwordx4 v152, s[72:75], s49 offen lds
	s_waitcnt lgkmcnt(8)
	s_waitcnt vmcnt(10)
	s_barrier
	s_waitcnt lgkmcnt(0)
	s_setprio 1
	s_waitcnt lgkmcnt(7)
	v_mfma_f32_16x16x32_bf16 v[142:145], v[220:223], v[146:149], v[142:145]
	v_mfma_f32_16x16x32_bf16 v[138:141], v[228:231], v[146:149], v[138:141]
	s_waitcnt lgkmcnt(5)
	v_mfma_f32_16x16x32_bf16 v[134:137], v[220:223], v[160:163], v[134:137]
	v_mfma_f32_16x16x32_bf16 v[130:133], v[228:231], v[160:163], v[130:133]
	s_waitcnt lgkmcnt(3)
	v_mfma_f32_16x16x32_bf16 v[110:113], v[220:223], v[168:171], v[110:113]
	v_mfma_f32_16x16x32_bf16 v[106:109], v[228:231], v[168:171], v[106:109]
	s_waitcnt lgkmcnt(1)
	v_mfma_f32_16x16x32_bf16 v[102:105], v[220:223], v[176:179], v[102:105]
	v_mfma_f32_16x16x32_bf16 v[98:101], v[228:231], v[176:179], v[98:101]
	v_mfma_f32_16x16x32_bf16 v[142:145], v[224:227], v[156:159], v[142:145]
	v_mfma_f32_16x16x32_bf16 v[138:141], v[232:235], v[156:159], v[138:141]
	v_mfma_f32_16x16x32_bf16 v[134:137], v[224:227], v[164:167], v[134:137]
	v_mfma_f32_16x16x32_bf16 v[130:133], v[232:235], v[164:167], v[130:133]
	v_mfma_f32_16x16x32_bf16 v[110:113], v[224:227], v[172:175], v[110:113]
	v_mfma_f32_16x16x32_bf16 v[106:109], v[232:235], v[172:175], v[106:109]
	s_waitcnt lgkmcnt(0)
	v_mfma_f32_16x16x32_bf16 v[102:105], v[224:227], v[180:183], v[102:105]
	v_mfma_f32_16x16x32_bf16 v[98:101], v[232:235], v[180:183], v[98:101]
	s_setprio 0
	s_barrier
	s_mov_b32 s10, s74
	s_mov_b32 s11, s75
	s_mov_b32 m0, s26
	ds_read_b128 v[184:187], v154 offset:16384
	ds_read_b128 v[188:191], v154 offset:17408
	ds_read_b128 v[192:195], v154 offset:18432
	ds_read_b128 v[196:199], v154 offset:19456
	buffer_load_dwordx4 v151, s[8:11], s52 offen lds
	s_mov_b32 m0, s27
	s_nop 0
	buffer_load_dwordx4 v153, s[8:11], s52 offen lds
	s_waitcnt vmcnt(10)
	s_barrier
	s_waitcnt lgkmcnt(0)
	s_setprio 1
	s_waitcnt lgkmcnt(3)
	v_mfma_f32_16x16x32_bf16 v[126:129], v[184:187], v[146:149], v[126:129]
	s_waitcnt lgkmcnt(1)
	v_mfma_f32_16x16x32_bf16 v[122:125], v[192:195], v[146:149], v[122:125]
	v_mfma_f32_16x16x32_bf16 v[118:121], v[184:187], v[160:163], v[118:121]
	v_mfma_f32_16x16x32_bf16 v[114:117], v[192:195], v[160:163], v[114:117]
	v_mfma_f32_16x16x32_bf16 v[92:95], v[184:187], v[168:171], v[92:95]
	v_mfma_f32_16x16x32_bf16 v[88:91], v[192:195], v[168:171], v[88:91]
	v_mfma_f32_16x16x32_bf16 v[84:87], v[184:187], v[176:179], v[84:87]
	v_mfma_f32_16x16x32_bf16 v[80:83], v[192:195], v[176:179], v[80:83]
	v_mfma_f32_16x16x32_bf16 v[126:129], v[188:191], v[156:159], v[126:129]
	s_waitcnt lgkmcnt(0)
	v_mfma_f32_16x16x32_bf16 v[122:125], v[196:199], v[156:159], v[122:125]
	v_mfma_f32_16x16x32_bf16 v[118:121], v[188:191], v[164:167], v[118:121]
	v_mfma_f32_16x16x32_bf16 v[114:117], v[196:199], v[164:167], v[114:117]
	v_mfma_f32_16x16x32_bf16 v[92:95], v[188:191], v[172:175], v[92:95]
	v_mfma_f32_16x16x32_bf16 v[88:91], v[196:199], v[172:175], v[88:91]
	v_mfma_f32_16x16x32_bf16 v[84:87], v[188:191], v[180:183], v[84:87]
	v_mfma_f32_16x16x32_bf16 v[80:83], v[196:199], v[180:183], v[80:83]
	s_setprio 0
	s_mov_b32 m0, s23
	s_barrier
	ds_read_b128 v[146:149], v155 offset:16384
	ds_read_b128 v[156:159], v155 offset:17408
	ds_read_b128 v[160:163], v155 offset:18432
	ds_read_b128 v[164:167], v155 offset:19456
	ds_read_b128 v[168:171], v155 offset:20480
	ds_read_b128 v[172:175], v155 offset:21504
	ds_read_b128 v[176:179], v155 offset:22528
	ds_read_b128 v[180:183], v155 offset:23552
	buffer_load_dwordx4 v150, s[72:75], s54 offen lds
	s_mov_b32 m0, s28
	s_nop 0
	buffer_load_dwordx4 v152, s[72:75], s54 offen lds
	s_waitcnt vmcnt(10)
	s_barrier
	s_waitcnt lgkmcnt(0)
	s_setprio 1
	s_waitcnt lgkmcnt(7)
	v_mfma_f32_16x16x32_bf16 v[60:63], v[220:223], v[146:149], v[60:63]
	v_mfma_f32_16x16x32_bf16 v[56:59], v[228:231], v[146:149], v[56:59]
	s_waitcnt lgkmcnt(5)
	v_mfma_f32_16x16x32_bf16 v[52:55], v[220:223], v[160:163], v[52:55]
	v_mfma_f32_16x16x32_bf16 v[48:51], v[228:231], v[160:163], v[48:51]
	s_waitcnt lgkmcnt(3)
	v_mfma_f32_16x16x32_bf16 v[28:31], v[220:223], v[168:171], v[28:31]
	v_mfma_f32_16x16x32_bf16 v[24:27], v[228:231], v[168:171], v[24:27]
	s_waitcnt lgkmcnt(1)
	v_mfma_f32_16x16x32_bf16 v[20:23], v[220:223], v[176:179], v[20:23]
	v_mfma_f32_16x16x32_bf16 v[16:19], v[228:231], v[176:179], v[16:19]
	v_mfma_f32_16x16x32_bf16 v[60:63], v[224:227], v[156:159], v[60:63]
	v_mfma_f32_16x16x32_bf16 v[56:59], v[232:235], v[156:159], v[56:59]
	v_mfma_f32_16x16x32_bf16 v[52:55], v[224:227], v[164:167], v[52:55]
	v_mfma_f32_16x16x32_bf16 v[48:51], v[232:235], v[164:167], v[48:51]
	v_mfma_f32_16x16x32_bf16 v[28:31], v[224:227], v[172:175], v[28:31]
	v_mfma_f32_16x16x32_bf16 v[24:27], v[232:235], v[172:175], v[24:27]
	s_waitcnt lgkmcnt(0)
	v_mfma_f32_16x16x32_bf16 v[20:23], v[224:227], v[180:183], v[20:23]
	v_mfma_f32_16x16x32_bf16 v[16:19], v[232:235], v[180:183], v[16:19]
	s_setprio 0
	s_barrier
	ds_read_b128 v[220:223], v154 offset:32768
	ds_read_b128 v[224:227], v154 offset:33792
	ds_read_b128 v[228:231], v154 offset:34816
	ds_read_b128 v[232:235], v154 offset:35840
	s_add_i32 s55, s52, 0x80000
	s_mov_b32 m0, s29
	s_nop 0
	buffer_load_dwordx4 v151, s[8:11], s55 offen lds
	s_mov_b32 m0, s30
	s_nop 0
	buffer_load_dwordx4 v153, s[8:11], s55 offen lds
	s_waitcnt vmcnt(10)
	s_barrier
	s_setprio 1
	v_mfma_f32_16x16x32_bf16 v[44:47], v[184:187], v[146:149], v[44:47]
	v_mfma_f32_16x16x32_bf16 v[40:43], v[192:195], v[146:149], v[40:43]
	v_mfma_f32_16x16x32_bf16 v[36:39], v[184:187], v[160:163], v[36:39]
	v_mfma_f32_16x16x32_bf16 v[32:35], v[192:195], v[160:163], v[32:35]
	v_mfma_f32_16x16x32_bf16 v[12:15], v[184:187], v[168:171], v[12:15]
	v_mfma_f32_16x16x32_bf16 v[8:11], v[192:195], v[168:171], v[8:11]
	v_mfma_f32_16x16x32_bf16 v[4:7], v[184:187], v[176:179], v[4:7]
	v_mfma_f32_16x16x32_bf16 v[0:3], v[192:195], v[176:179], v[0:3]
	v_mfma_f32_16x16x32_bf16 v[44:47], v[188:191], v[156:159], v[44:47]
	v_mfma_f32_16x16x32_bf16 v[40:43], v[196:199], v[156:159], v[40:43]
	v_mfma_f32_16x16x32_bf16 v[36:39], v[188:191], v[164:167], v[36:39]
	v_mfma_f32_16x16x32_bf16 v[32:35], v[196:199], v[164:167], v[32:35]
	v_mfma_f32_16x16x32_bf16 v[12:15], v[188:191], v[172:175], v[12:15]
	v_mfma_f32_16x16x32_bf16 v[8:11], v[196:199], v[172:175], v[8:11]
	v_mfma_f32_16x16x32_bf16 v[4:7], v[188:191], v[180:183], v[4:7]
	v_mfma_f32_16x16x32_bf16 v[0:3], v[196:199], v[180:183], v[0:3]
	s_setprio 0
	s_barrier
	s_add_i32 s54, s54, 0x80000
	s_mov_b32 m0, s31
	ds_read_b128 v[146:149], v155 offset:32768
	ds_read_b128 v[156:159], v155 offset:33792
	ds_read_b128 v[160:163], v155 offset:34816
	ds_read_b128 v[164:167], v155 offset:35840
	ds_read_b128 v[168:171], v155 offset:36864
	ds_read_b128 v[172:175], v155 offset:37888
	ds_read_b128 v[176:179], v155 offset:38912
	ds_read_b128 v[180:183], v155 offset:39936
	buffer_load_dwordx4 v150, s[72:75], s54 offen lds
	s_mov_b32 m0, s34
	s_nop 0
	buffer_load_dwordx4 v152, s[72:75], s54 offen lds
	s_waitcnt lgkmcnt(8)
	s_waitcnt vmcnt(10)
	s_barrier
	s_waitcnt lgkmcnt(0)
	s_setprio 1
	s_waitcnt lgkmcnt(7)
	v_mfma_f32_16x16x32_bf16 v[142:145], v[220:223], v[146:149], v[142:145]
	v_mfma_f32_16x16x32_bf16 v[138:141], v[228:231], v[146:149], v[138:141]
	s_waitcnt lgkmcnt(5)
	v_mfma_f32_16x16x32_bf16 v[134:137], v[220:223], v[160:163], v[134:137]
	v_mfma_f32_16x16x32_bf16 v[130:133], v[228:231], v[160:163], v[130:133]
	s_waitcnt lgkmcnt(3)
	v_mfma_f32_16x16x32_bf16 v[110:113], v[220:223], v[168:171], v[110:113]
	v_mfma_f32_16x16x32_bf16 v[106:109], v[228:231], v[168:171], v[106:109]
	s_waitcnt lgkmcnt(1)
	v_mfma_f32_16x16x32_bf16 v[102:105], v[220:223], v[176:179], v[102:105]
	v_mfma_f32_16x16x32_bf16 v[98:101], v[228:231], v[176:179], v[98:101]
	v_mfma_f32_16x16x32_bf16 v[142:145], v[224:227], v[156:159], v[142:145]
	v_mfma_f32_16x16x32_bf16 v[138:141], v[232:235], v[156:159], v[138:141]
	v_mfma_f32_16x16x32_bf16 v[134:137], v[224:227], v[164:167], v[134:137]
	v_mfma_f32_16x16x32_bf16 v[130:133], v[232:235], v[164:167], v[130:133]
	v_mfma_f32_16x16x32_bf16 v[110:113], v[224:227], v[172:175], v[110:113]
	v_mfma_f32_16x16x32_bf16 v[106:109], v[232:235], v[172:175], v[106:109]
	s_waitcnt lgkmcnt(0)
	v_mfma_f32_16x16x32_bf16 v[102:105], v[224:227], v[180:183], v[102:105]
	v_mfma_f32_16x16x32_bf16 v[98:101], v[232:235], v[180:183], v[98:101]
	s_setprio 0
	s_barrier
	s_or_b32 s54, s52, 0x80
	s_mov_b32 m0, s35
	ds_read_b128 v[184:187], v154 offset:49152
	ds_read_b128 v[188:191], v154 offset:50176
	ds_read_b128 v[192:195], v154 offset:51200
	ds_read_b128 v[196:199], v154 offset:52224
	buffer_load_dwordx4 v151, s[8:11], s54 offen lds
	s_mov_b32 m0, s36
	s_nop 0
	buffer_load_dwordx4 v153, s[8:11], s54 offen lds
	s_waitcnt vmcnt(10)
	s_barrier
	s_waitcnt lgkmcnt(0)
	s_setprio 1
	s_waitcnt lgkmcnt(3)
	v_mfma_f32_16x16x32_bf16 v[126:129], v[184:187], v[146:149], v[126:129]
	s_waitcnt lgkmcnt(1)
	v_mfma_f32_16x16x32_bf16 v[122:125], v[192:195], v[146:149], v[122:125]
	v_mfma_f32_16x16x32_bf16 v[118:121], v[184:187], v[160:163], v[118:121]
	v_mfma_f32_16x16x32_bf16 v[114:117], v[192:195], v[160:163], v[114:117]
	v_mfma_f32_16x16x32_bf16 v[92:95], v[184:187], v[168:171], v[92:95]
	v_mfma_f32_16x16x32_bf16 v[88:91], v[192:195], v[168:171], v[88:91]
	v_mfma_f32_16x16x32_bf16 v[84:87], v[184:187], v[176:179], v[84:87]
	v_mfma_f32_16x16x32_bf16 v[80:83], v[192:195], v[176:179], v[80:83]
	v_mfma_f32_16x16x32_bf16 v[126:129], v[188:191], v[156:159], v[126:129]
	s_waitcnt lgkmcnt(0)
	v_mfma_f32_16x16x32_bf16 v[122:125], v[196:199], v[156:159], v[122:125]
	v_mfma_f32_16x16x32_bf16 v[118:121], v[188:191], v[164:167], v[118:121]
	v_mfma_f32_16x16x32_bf16 v[114:117], v[196:199], v[164:167], v[114:117]
	v_mfma_f32_16x16x32_bf16 v[92:95], v[188:191], v[172:175], v[92:95]
	v_mfma_f32_16x16x32_bf16 v[88:91], v[196:199], v[172:175], v[88:91]
	v_mfma_f32_16x16x32_bf16 v[84:87], v[188:191], v[180:183], v[84:87]
	v_mfma_f32_16x16x32_bf16 v[80:83], v[196:199], v[180:183], v[80:83]
	s_setprio 0
	s_mov_b32 m0, s37
	s_barrier
	ds_read_b128 v[146:149], v155 offset:49152
	ds_read_b128 v[156:159], v155 offset:50176
	ds_read_b128 v[160:163], v155 offset:51200
	ds_read_b128 v[164:167], v155 offset:52224
	ds_read_b128 v[168:171], v155 offset:53248
	ds_read_b128 v[172:175], v155 offset:54272
	ds_read_b128 v[176:179], v155 offset:55296
	ds_read_b128 v[180:183], v155 offset:56320
	buffer_load_dwordx4 v150, s[72:75], s53 offen lds
	s_mov_b32 m0, s38
	s_nop 0
	buffer_load_dwordx4 v152, s[72:75], s53 offen lds
	s_waitcnt vmcnt(10)
	s_barrier
	s_waitcnt lgkmcnt(0)
	s_setprio 1
	s_waitcnt lgkmcnt(7)
	v_mfma_f32_16x16x32_bf16 v[60:63], v[220:223], v[146:149], v[60:63]
	v_mfma_f32_16x16x32_bf16 v[56:59], v[228:231], v[146:149], v[56:59]
	s_waitcnt lgkmcnt(5)
	v_mfma_f32_16x16x32_bf16 v[52:55], v[220:223], v[160:163], v[52:55]
	v_mfma_f32_16x16x32_bf16 v[48:51], v[228:231], v[160:163], v[48:51]
	s_waitcnt lgkmcnt(3)
	v_mfma_f32_16x16x32_bf16 v[28:31], v[220:223], v[168:171], v[28:31]
	v_mfma_f32_16x16x32_bf16 v[24:27], v[228:231], v[168:171], v[24:27]
	s_waitcnt lgkmcnt(1)
	v_mfma_f32_16x16x32_bf16 v[20:23], v[220:223], v[176:179], v[20:23]
	v_mfma_f32_16x16x32_bf16 v[16:19], v[228:231], v[176:179], v[16:19]
	v_mfma_f32_16x16x32_bf16 v[60:63], v[224:227], v[156:159], v[60:63]
	v_mfma_f32_16x16x32_bf16 v[56:59], v[232:235], v[156:159], v[56:59]
	v_mfma_f32_16x16x32_bf16 v[52:55], v[224:227], v[164:167], v[52:55]
	v_mfma_f32_16x16x32_bf16 v[48:51], v[232:235], v[164:167], v[48:51]
	v_mfma_f32_16x16x32_bf16 v[28:31], v[224:227], v[172:175], v[28:31]
	v_mfma_f32_16x16x32_bf16 v[24:27], v[232:235], v[172:175], v[24:27]
	s_waitcnt lgkmcnt(0)
	v_mfma_f32_16x16x32_bf16 v[20:23], v[224:227], v[180:183], v[20:23]
	v_mfma_f32_16x16x32_bf16 v[16:19], v[232:235], v[180:183], v[16:19]
	s_setprio 0
	s_barrier
	ds_read_b128 v[220:223], v154
	ds_read_b128 v[224:227], v154 offset:1024
	ds_read_b128 v[228:231], v154 offset:2048
	ds_read_b128 v[232:235], v154 offset:3072
	s_add_i32 s52, s52, 0x80080
	s_mov_b32 m0, s39
	s_nop 0
	buffer_load_dwordx4 v151, s[8:11], s52 offen lds
	s_mov_b32 m0, s40
	s_nop 0
	buffer_load_dwordx4 v153, s[8:11], s52 offen lds
	s_waitcnt vmcnt(10)
	s_barrier
	s_setprio 1
	v_mfma_f32_16x16x32_bf16 v[44:47], v[184:187], v[146:149], v[44:47]
	v_mfma_f32_16x16x32_bf16 v[40:43], v[192:195], v[146:149], v[40:43]
	v_mfma_f32_16x16x32_bf16 v[36:39], v[184:187], v[160:163], v[36:39]
	v_mfma_f32_16x16x32_bf16 v[32:35], v[192:195], v[160:163], v[32:35]
	v_mfma_f32_16x16x32_bf16 v[12:15], v[184:187], v[168:171], v[12:15]
	v_mfma_f32_16x16x32_bf16 v[8:11], v[192:195], v[168:171], v[8:11]
	v_mfma_f32_16x16x32_bf16 v[4:7], v[184:187], v[176:179], v[4:7]
	v_mfma_f32_16x16x32_bf16 v[0:3], v[192:195], v[176:179], v[0:3]
	v_mfma_f32_16x16x32_bf16 v[44:47], v[188:191], v[156:159], v[44:47]
	v_mfma_f32_16x16x32_bf16 v[40:43], v[196:199], v[156:159], v[40:43]
	v_mfma_f32_16x16x32_bf16 v[36:39], v[188:191], v[164:167], v[36:39]
	v_mfma_f32_16x16x32_bf16 v[32:35], v[196:199], v[164:167], v[32:35]
	v_mfma_f32_16x16x32_bf16 v[12:15], v[188:191], v[172:175], v[12:15]
	v_mfma_f32_16x16x32_bf16 v[8:11], v[196:199], v[172:175], v[8:11]
	v_mfma_f32_16x16x32_bf16 v[4:7], v[188:191], v[180:183], v[4:7]
	v_mfma_f32_16x16x32_bf16 v[0:3], v[196:199], v[180:183], v[0:3]
	s_setprio 0
	s_add_i32 s51, s51, 2
	s_addk_i32 s49, 0x100
	s_addk_i32 s50, 0x100
	s_cmp_gt_u32 s51, 29
	s_barrier
	s_cbranch_scc0 .LBB0_1514
	s_waitcnt lgkmcnt(0)
	s_getreg_b32 s10, hwreg(HW_REG_HW_ID, 0, 6)
	s_and_b32 s10, s10, 63
	s_lshl_b32 s10, s10, 2
	s_add_i32 s10, s10, 0
	s_add_i32 s10, s10, 0x20010
	v_mov_b32_e32 v64, s10
	ds_read_b32 v64, v64
	v_mbcnt_lo_u32_b32 v148, -1, 0
	v_mbcnt_hi_u32_b32 v148, -1, v148
	s_mov_b32 s50, s17
	v_lshrrev_b32_e32 v66, 1, v148
	v_and_b32_e32 v156, 24, v66
	s_waitcnt lgkmcnt(0)
	v_readfirstlane_b32 s10, v64
	s_nop 1
	v_lshl_or_b32 v146, s10, 6, v148
	s_lshl_b32 s10, s2, 8
	s_min_i32 s2, s46, 64
	s_ashr_i32 s2, s2, 3
	s_mul_hi_i32 s11, s2, 0xc000
	s_mul_i32 s2, s2, 0xc000
	s_add_u32 s2, s0, s2
	s_addc_u32 s47, s24, s11
	s_ashr_i32 s11, s10, 31
	s_lshl_b64 s[48:49], s[10:11], 2
	v_lshrrev_b32_e32 v64, 1, v146
	s_add_u32 s48, s2, s48
	v_and_b32_e32 v149, 0x60, v64
	s_addc_u32 s49, s47, s49
	v_lshlrev_b32_e32 v96, 2, v149
	v_lshl_add_u64 v[64:65], s[48:49], 0, v[96:97]
	v_lshlrev_b32_e32 v96, 2, v156
	v_lshl_add_u64 v[68:69], v[64:65], 0, v[96:97]
	v_ashrrev_i32_e32 v96, 2, v146
	s_lshl_b32 s48, s46, 8
	v_and_b32_e32 v146, 0xffffffc0, v96
	s_ashr_i32 s49, s48, 31
	v_ashrrev_i32_e32 v147, 31, v146
	v_lshl_add_u64 v[146:147], v[146:147], 0, s[48:49]
	v_and_or_b32 v146, v148, 15, v146
	s_cmp_gt_i32 s46, 63
	v_lshlrev_b64 v[146:147], 11, v[146:147]
	v_lshl_add_u64 v[146:147], v[146:147], 0, s[10:11]
	s_cselect_b32 s2, s44, s21
	s_cselect_b32 s10, s43, s20
	v_or3_b32 v146, v146, v149, v156
	v_mov_b32_e32 v148, s10
	v_mov_b32_e32 v149, s2
	v_lshl_add_u64 v[148:149], v[146:147], 2, v[148:149]
	global_load_dwordx4 v[72:75], v[68:69], off offset:16
	global_load_dwordx4 v[76:79], v[68:69], off
	global_load_dwordx4 v[64:67], v[68:69], off offset:528
	s_nop 0
	global_load_dwordx4 v[68:71], v[68:69], off offset:512
	s_nop 0
	global_load_dwordx4 v[156:159], v[148:149], off offset:16
	global_load_dwordx4 v[160:163], v[148:149], off
	global_load_dwordx4 v[164:167], v[148:149], off offset:528
	global_load_dwordx4 v[168:171], v[148:149], off offset:512
	s_mov_b64 s[10:11], 0x20000
	v_add_co_u32_e32 v180, vcc, s75, v148
	v_lshl_add_u64 v[176:177], v[148:149], 0, s[10:11]
	s_nop 0
	v_addc_co_u32_e32 v181, vcc, 0, v149, vcc
	global_load_dwordx4 v[172:175], v[180:181], off
	s_nop 0
	global_load_dwordx4 v[176:179], v[176:177], off offset:16
	s_mov_b64 s[10:11], 0x20200
	v_lshl_add_u64 v[184:185], v[148:149], 0, s[10:11]
	global_load_dwordx4 v[180:183], v[180:181], off offset:512
	s_nop 0
	global_load_dwordx4 v[184:187], v[184:185], off offset:16
	v_lshl_add_u64 v[146:147], v[146:147], 1, s[12:13]
	s_mov_b32 s2, 0x10000
	s_mov_b64 s[10:11], 0x40000
	s_mov_b32 s46, s15
	s_mov_b32 s49, s16
	s_waitcnt vmcnt(7)
	v_pk_fma_f32 v[158:159], v[140:141], v[74:75], v[158:159]
	s_waitcnt vmcnt(6)
	v_pk_fma_f32 v[144:145], v[144:145], v[78:79], v[162:163]
	v_pk_fma_f32 v[142:143], v[142:143], v[76:77], v[160:161]
	v_pk_fma_f32 v[140:141], v[138:139], v[72:73], v[156:157]
	v_cvt_pk_bf16_f32 v138, v142, v143
	v_cvt_pk_bf16_f32 v139, v144, v145
	v_cvt_pk_bf16_f32 v140, v140, v141
	v_cvt_pk_bf16_f32 v141, v158, v159
	global_store_dwordx4 v[146:147], v[138:141], off
	s_waitcnt vmcnt(5)
	v_pk_fma_f32 v[128:129], v[128:129], v[70:71], v[170:171]
	v_pk_fma_f32 v[126:127], v[126:127], v[68:69], v[168:169]
	v_pk_fma_f32 v[138:139], v[124:125], v[66:67], v[166:167]
	v_pk_fma_f32 v[124:125], v[122:123], v[64:65], v[164:165]
	v_cvt_pk_bf16_f32 v122, v126, v127
	v_cvt_pk_bf16_f32 v123, v128, v129
	v_cvt_pk_bf16_f32 v124, v124, v125
	v_cvt_pk_bf16_f32 v125, v138, v139
	global_store_dwordx4 v[146:147], v[122:125], off offset:256
	s_waitcnt vmcnt(4)
	v_pk_fma_f32 v[126:127], v[132:133], v[74:75], v[178:179]
	v_pk_fma_f32 v[128:129], v[130:131], v[72:73], v[176:177]
	v_pk_fma_f32 v[124:125], v[136:137], v[78:79], v[174:175]
	v_pk_fma_f32 v[122:123], v[134:135], v[76:77], v[172:173]
	s_waitcnt vmcnt(3)
	v_pk_fma_f32 v[120:121], v[120:121], v[70:71], v[182:183]
	v_cvt_pk_bf16_f32 v122, v122, v123
	v_cvt_pk_bf16_f32 v123, v124, v125
	v_cvt_pk_bf16_f32 v125, v126, v127
	v_add_co_u32_e32 v126, vcc, s2, v146
	v_cvt_pk_bf16_f32 v124, v128, v129
	s_nop 0
	v_addc_co_u32_e32 v127, vcc, 0, v147, vcc
	global_store_dwordx4 v[126:127], v[122:125], off
	v_pk_fma_f32 v[118:119], v[118:119], v[68:69], v[180:181]
	s_mov_b32 s2, 0x40000
	s_waitcnt vmcnt(3)
	v_pk_fma_f32 v[122:123], v[116:117], v[66:67], v[186:187]
	v_pk_fma_f32 v[116:117], v[114:115], v[64:65], v[184:185]
	v_cvt_pk_bf16_f32 v114, v118, v119
	v_cvt_pk_bf16_f32 v115, v120, v121
	v_cvt_pk_bf16_f32 v116, v116, v117
	v_cvt_pk_bf16_f32 v117, v122, v123
	v_add_co_u32_e32 v122, vcc, s2, v148
	global_store_dwordx4 v[126:127], v[114:117], off offset:256
	v_lshl_add_u64 v[118:119], v[148:149], 0, s[10:11]
	v_addc_co_u32_e32 v123, vcc, 0, v149, vcc
	global_load_dwordx4 v[114:117], v[122:123], off
	s_nop 0
	global_load_dwordx4 v[118:121], v[118:119], off offset:16
	s_mov_b64 s[10:11], 0x40200
	v_lshl_add_u64 v[126:127], v[148:149], 0, s[10:11]
	s_mov_b32 s2, 0x60000
	global_load_dwordx4 v[122:125], v[122:123], off offset:512
	s_nop 0
	global_load_dwordx4 v[126:129], v[126:127], off offset:16
	s_mov_b64 s[10:11], 0x60000
	v_add_co_u32_e32 v138, vcc, s2, v148
	v_lshl_add_u64 v[134:135], v[148:149], 0, s[10:11]
	s_nop 0
	v_addc_co_u32_e32 v139, vcc, 0, v149, vcc
	global_load_dwordx4 v[130:133], v[138:139], off
	s_nop 0
	global_load_dwordx4 v[134:137], v[134:135], off offset:16
	s_mov_b64 s[10:11], 0x60200
	v_lshl_add_u64 v[142:143], v[148:149], 0, s[10:11]
	global_load_dwordx4 v[138:141], v[138:139], off offset:512
	s_nop 0
	global_load_dwordx4 v[142:145], v[142:143], off offset:16
	s_mov_b32 s2, 0x30000
	s_mov_b64 s[10:11], 0x100000
	s_waitcnt vmcnt(7)
	v_pk_fma_f32 v[110:111], v[110:111], v[76:77], v[114:115]
	v_pk_fma_f32 v[112:113], v[112:113], v[78:79], v[116:117]
	s_waitcnt vmcnt(6)
	v_pk_fma_f32 v[114:115], v[108:109], v[74:75], v[120:121]
	v_pk_fma_f32 v[108:109], v[106:107], v[72:73], v[118:119]
	v_cvt_pk_bf16_f32 v106, v110, v111
	v_add_co_u32_e32 v110, vcc, s75, v146
	v_cvt_pk_bf16_f32 v107, v112, v113
	v_cvt_pk_bf16_f32 v108, v108, v109
	v_cvt_pk_bf16_f32 v109, v114, v115
	v_addc_co_u32_e32 v111, vcc, 0, v147, vcc
	global_store_dwordx4 v[110:111], v[106:109], off
	s_waitcnt vmcnt(6)
	v_pk_fma_f32 v[94:95], v[94:95], v[70:71], v[124:125]
	v_pk_fma_f32 v[92:93], v[92:93], v[68:69], v[122:123]
	s_waitcnt vmcnt(5)
	v_pk_fma_f32 v[106:107], v[90:91], v[66:67], v[128:129]
	v_pk_fma_f32 v[90:91], v[88:89], v[64:65], v[126:127]
	v_cvt_pk_bf16_f32 v88, v92, v93
	v_cvt_pk_bf16_f32 v89, v94, v95
	v_cvt_pk_bf16_f32 v90, v90, v91
	v_cvt_pk_bf16_f32 v91, v106, v107
	global_store_dwordx4 v[110:111], v[88:91], off offset:256
	s_waitcnt vmcnt(4)
	v_pk_fma_f32 v[92:93], v[100:101], v[74:75], v[136:137]
	v_pk_fma_f32 v[94:95], v[98:99], v[72:73], v[134:135]
	v_pk_fma_f32 v[90:91], v[104:105], v[78:79], v[132:133]
	v_pk_fma_f32 v[88:89], v[102:103], v[76:77], v[130:131]
	s_waitcnt vmcnt(3)
	v_pk_fma_f32 v[86:87], v[86:87], v[70:71], v[140:141]
	v_cvt_pk_bf16_f32 v88, v88, v89
	v_cvt_pk_bf16_f32 v89, v90, v91
	v_cvt_pk_bf16_f32 v91, v92, v93
	v_add_co_u32_e32 v92, vcc, s2, v146
	v_cvt_pk_bf16_f32 v90, v94, v95
	s_nop 0
	v_addc_co_u32_e32 v93, vcc, 0, v147, vcc
	global_store_dwordx4 v[92:93], v[88:91], off
	v_pk_fma_f32 v[84:85], v[84:85], v[68:69], v[138:139]
	s_mov_b32 s2, 0x100000
	s_waitcnt vmcnt(3)
	v_pk_fma_f32 v[88:89], v[82:83], v[66:67], v[144:145]
	v_pk_fma_f32 v[82:83], v[80:81], v[64:65], v[142:143]
	v_cvt_pk_bf16_f32 v80, v84, v85
	v_cvt_pk_bf16_f32 v81, v86, v87
	v_cvt_pk_bf16_f32 v82, v82, v83
	v_cvt_pk_bf16_f32 v83, v88, v89
	v_add_co_u32_e32 v88, vcc, s2, v148
	global_store_dwordx4 v[92:93], v[80:83], off offset:256
	s_nop 0
	v_addc_co_u32_e32 v89, vcc, 0, v149, vcc
	v_lshl_add_u64 v[80:81], v[148:149], 0, s[10:11]
	global_load_dwordx4 v[84:87], v[88:89], off
	s_nop 0
	global_load_dwordx4 v[80:83], v[80:81], off offset:16
	s_mov_b64 s[10:11], 0x100200
	v_lshl_add_u64 v[92:93], v[148:149], 0, s[10:11]
	s_mov_b32 s2, 0x120000
	global_load_dwordx4 v[88:91], v[88:89], off offset:512
	s_nop 0
	global_load_dwordx4 v[92:95], v[92:93], off offset:16
	s_mov_b64 s[10:11], 0x120000
	v_add_co_u32_e32 v106, vcc, s2, v148
	v_lshl_add_u64 v[102:103], v[148:149], 0, s[10:11]
	s_nop 0
	v_addc_co_u32_e32 v107, vcc, 0, v149, vcc
	global_load_dwordx4 v[98:101], v[106:107], off
	s_nop 0
	global_load_dwordx4 v[102:105], v[102:103], off offset:16
	s_mov_b64 s[10:11], 0x120200
	v_lshl_add_u64 v[110:111], v[148:149], 0, s[10:11]
	global_load_dwordx4 v[106:109], v[106:107], off offset:512
	s_nop 0
	global_load_dwordx4 v[110:113], v[110:111], off offset:16
	s_mov_b32 s2, 0x80000
	s_mov_b64 s[10:11], 0x140000
	s_waitcnt vmcnt(7)
	v_pk_fma_f32 v[60:61], v[60:61], v[76:77], v[84:85]
	v_pk_fma_f32 v[62:63], v[62:63], v[78:79], v[86:87]
	s_waitcnt vmcnt(6)
	v_pk_fma_f32 v[82:83], v[58:59], v[74:75], v[82:83]
	v_pk_fma_f32 v[58:59], v[56:57], v[72:73], v[80:81]
	v_cvt_pk_bf16_f32 v56, v60, v61
	v_add_co_u32_e32 v60, vcc, s2, v146
	v_cvt_pk_bf16_f32 v57, v62, v63
	v_cvt_pk_bf16_f32 v58, v58, v59
	v_cvt_pk_bf16_f32 v59, v82, v83
	v_addc_co_u32_e32 v61, vcc, 0, v147, vcc
	global_store_dwordx4 v[60:61], v[56:59], off
	s_waitcnt vmcnt(6)
	v_pk_fma_f32 v[46:47], v[46:47], v[70:71], v[90:91]
	v_pk_fma_f32 v[44:45], v[44:45], v[68:69], v[88:89]
	s_waitcnt vmcnt(5)
	v_pk_fma_f32 v[56:57], v[42:43], v[66:67], v[94:95]
	v_pk_fma_f32 v[42:43], v[40:41], v[64:65], v[92:93]
	v_cvt_pk_bf16_f32 v40, v44, v45
	v_cvt_pk_bf16_f32 v41, v46, v47
	v_cvt_pk_bf16_f32 v42, v42, v43
	v_cvt_pk_bf16_f32 v43, v56, v57
	global_store_dwordx4 v[60:61], v[40:43], off offset:256
	s_waitcnt vmcnt(4)
	v_pk_fma_f32 v[44:45], v[50:51], v[74:75], v[104:105]
	s_mov_b32 s2, 0x90000
	v_pk_fma_f32 v[42:43], v[54:55], v[78:79], v[100:101]
	v_pk_fma_f32 v[40:41], v[52:53], v[76:77], v[98:99]
	v_pk_fma_f32 v[46:47], v[48:49], v[72:73], v[102:103]
	v_cvt_pk_bf16_f32 v40, v40, v41
	v_cvt_pk_bf16_f32 v41, v42, v43
	v_cvt_pk_bf16_f32 v43, v44, v45
	v_add_co_u32_e32 v44, vcc, s2, v146
	v_cvt_pk_bf16_f32 v42, v46, v47
	s_nop 0
	v_addc_co_u32_e32 v45, vcc, 0, v147, vcc
	global_store_dwordx4 v[44:45], v[40:43], off
	s_waitcnt vmcnt(4)
	v_pk_fma_f32 v[38:39], v[38:39], v[70:71], v[108:109]
	v_pk_fma_f32 v[36:37], v[36:37], v[68:69], v[106:107]
	s_waitcnt vmcnt(3)
	v_pk_fma_f32 v[40:41], v[34:35], v[66:67], v[112:113]
	v_pk_fma_f32 v[34:35], v[32:33], v[64:65], v[110:111]
	s_mov_b32 s2, 0x140000
	v_cvt_pk_bf16_f32 v32, v36, v37
	v_cvt_pk_bf16_f32 v33, v38, v39
	v_cvt_pk_bf16_f32 v34, v34, v35
	v_cvt_pk_bf16_f32 v35, v40, v41
	v_add_co_u32_e32 v40, vcc, s2, v148
	global_store_dwordx4 v[44:45], v[32:35], off offset:256
	v_lshl_add_u64 v[36:37], v[148:149], 0, s[10:11]
	v_addc_co_u32_e32 v41, vcc, 0, v149, vcc
	global_load_dwordx4 v[32:35], v[40:41], off
	s_nop 0
	global_load_dwordx4 v[36:39], v[36:37], off offset:16
	s_mov_b64 s[10:11], 0x140200
	v_lshl_add_u64 v[44:45], v[148:149], 0, s[10:11]
	s_mov_b32 s2, 0x160000
	global_load_dwordx4 v[40:43], v[40:41], off offset:512
	s_nop 0
	global_load_dwordx4 v[44:47], v[44:45], off offset:16
	s_mov_b64 s[10:11], 0x160000
	v_add_co_u32_e32 v56, vcc, s2, v148
	v_lshl_add_u64 v[52:53], v[148:149], 0, s[10:11]
	s_nop 0
	v_addc_co_u32_e32 v57, vcc, 0, v149, vcc
	global_load_dwordx4 v[48:51], v[56:57], off
	s_nop 0
	global_load_dwordx4 v[52:55], v[52:53], off offset:16
	s_mov_b64 s[10:11], 0x160200
	v_lshl_add_u64 v[60:61], v[148:149], 0, s[10:11]
	global_load_dwordx4 v[56:59], v[56:57], off offset:512
	s_nop 0
	global_load_dwordx4 v[60:63], v[60:61], off offset:16
	s_mov_b32 s2, 0xa0000
	s_waitcnt vmcnt(7)
	v_pk_fma_f32 v[28:29], v[28:29], v[76:77], v[32:33]
	v_pk_fma_f32 v[30:31], v[30:31], v[78:79], v[34:35]
	s_waitcnt vmcnt(6)
	v_pk_fma_f32 v[32:33], v[26:27], v[74:75], v[38:39]
	v_pk_fma_f32 v[26:27], v[24:25], v[72:73], v[36:37]
	v_cvt_pk_bf16_f32 v24, v28, v29
	v_add_co_u32_e32 v28, vcc, s2, v146
	v_cvt_pk_bf16_f32 v25, v30, v31
	v_cvt_pk_bf16_f32 v26, v26, v27
	v_cvt_pk_bf16_f32 v27, v32, v33
	v_addc_co_u32_e32 v29, vcc, 0, v147, vcc
	global_store_dwordx4 v[28:29], v[24:27], off
	s_waitcnt vmcnt(6)
	v_pk_fma_f32 v[14:15], v[14:15], v[70:71], v[42:43]
	v_pk_fma_f32 v[12:13], v[12:13], v[68:69], v[40:41]
	s_waitcnt vmcnt(5)
	v_pk_fma_f32 v[24:25], v[10:11], v[66:67], v[46:47]
	v_pk_fma_f32 v[10:11], v[8:9], v[64:65], v[44:45]
	v_cvt_pk_bf16_f32 v8, v12, v13
	v_cvt_pk_bf16_f32 v9, v14, v15
	v_cvt_pk_bf16_f32 v10, v10, v11
	v_cvt_pk_bf16_f32 v11, v24, v25
	global_store_dwordx4 v[28:29], v[8:11], off offset:256
	s_waitcnt vmcnt(4)
	v_pk_fma_f32 v[12:13], v[18:19], v[74:75], v[54:55]
	s_mov_b32 s2, 0xb0000
	v_pk_fma_f32 v[10:11], v[22:23], v[78:79], v[50:51]
	v_pk_fma_f32 v[8:9], v[20:21], v[76:77], v[48:49]
	v_pk_fma_f32 v[14:15], v[16:17], v[72:73], v[52:53]
	v_cvt_pk_bf16_f32 v8, v8, v9
	v_cvt_pk_bf16_f32 v9, v10, v11
	v_cvt_pk_bf16_f32 v11, v12, v13
	v_add_co_u32_e32 v12, vcc, s2, v146
	v_cvt_pk_bf16_f32 v10, v14, v15
	s_nop 0
	v_addc_co_u32_e32 v13, vcc, 0, v147, vcc
	global_store_dwordx4 v[12:13], v[8:11], off
	s_waitcnt vmcnt(4)
	v_pk_fma_f32 v[6:7], v[6:7], v[70:71], v[58:59]
	v_pk_fma_f32 v[4:5], v[4:5], v[68:69], v[56:57]
	s_waitcnt vmcnt(3)
	v_pk_fma_f32 v[8:9], v[2:3], v[66:67], v[62:63]
	v_pk_fma_f32 v[2:3], v[0:1], v[64:65], v[60:61]
	v_cvt_pk_bf16_f32 v0, v4, v5
	v_cvt_pk_bf16_f32 v1, v6, v7
	v_cvt_pk_bf16_f32 v2, v2, v3
	v_cvt_pk_bf16_f32 v3, v8, v9
	s_and_b64 vcc, exec, s[4:5]
	s_mov_b32 s2, s14
	global_store_dwordx4 v[12:13], v[0:3], off offset:256
	s_cbranch_vccz .LBB0_1508
	s_branch .LBB0_1517

.LBB0_1638:
	v_mov_b64_e32 v[0:1], s[6:7]
	v_cmp_lt_i64_e32 vcc, s[10:11], v[0:1]
	s_lshl_b32 s16, s15, 20
	s_and_b64 s[10:11], vcc, exec
	s_cselect_b32 s39, s16, s41
	s_lshl_b32 s17, s14, 20
	s_and_b64 s[10:11], vcc, exec
	v_mov_b32_e32 v0, 0
	s_cselect_b32 s40, s17, s42
	s_add_i32 s41, s41, 0x80080
	s_addk_i32 s42, 0x100
	s_mov_b32 s43, -2
	v_mov_b32_e32 v1, v0
	v_mov_b32_e32 v2, v0
	v_mov_b32_e32 v3, v0
	v_mov_b32_e32 v12, v0
	v_mov_b32_e32 v13, v0
	v_mov_b32_e32 v14, v0
	v_mov_b32_e32 v15, v0
	v_mov_b32_e32 v4, v0
	v_mov_b32_e32 v5, v0
	v_mov_b32_e32 v6, v0
	v_mov_b32_e32 v7, v0
	v_mov_b32_e32 v20, v0
	v_mov_b32_e32 v21, v0
	v_mov_b32_e32 v22, v0
	v_mov_b32_e32 v23, v0
	v_mov_b32_e32 v8, v0
	v_mov_b32_e32 v9, v0
	v_mov_b32_e32 v10, v0
	v_mov_b32_e32 v11, v0
	v_mov_b32_e32 v24, v0
	v_mov_b32_e32 v25, v0
	v_mov_b32_e32 v26, v0
	v_mov_b32_e32 v27, v0
	v_mov_b32_e32 v16, v0
	v_mov_b32_e32 v17, v0
	v_mov_b32_e32 v18, v0
	v_mov_b32_e32 v19, v0
	v_mov_b32_e32 v28, v0
	v_mov_b32_e32 v29, v0
	v_mov_b32_e32 v30, v0
	v_mov_b32_e32 v31, v0
	v_mov_b32_e32 v36, v0
	v_mov_b32_e32 v37, v0
	v_mov_b32_e32 v38, v0
	v_mov_b32_e32 v39, v0
	v_mov_b32_e32 v52, v0
	v_mov_b32_e32 v53, v0
	v_mov_b32_e32 v54, v0
	v_mov_b32_e32 v55, v0
	v_mov_b32_e32 v44, v0
	v_mov_b32_e32 v45, v0
	v_mov_b32_e32 v46, v0
	v_mov_b32_e32 v47, v0
	v_mov_b32_e32 v68, v0
	v_mov_b32_e32 v69, v0
	v_mov_b32_e32 v70, v0
	v_mov_b32_e32 v71, v0
	v_mov_b32_e32 v56, v0
	v_mov_b32_e32 v57, v0
	v_mov_b32_e32 v58, v0
	v_mov_b32_e32 v59, v0
	v_mov_b32_e32 v80, v0
	v_mov_b32_e32 v81, v0
	v_mov_b32_e32 v82, v0
	v_mov_b32_e32 v83, v0
	v_mov_b32_e32 v72, v0
	v_mov_b32_e32 v73, v0
	v_mov_b32_e32 v74, v0
	v_mov_b32_e32 v75, v0
	v_mov_b32_e32 v88, v0
	v_mov_b32_e32 v89, v0
	v_mov_b32_e32 v90, v0
	v_mov_b32_e32 v91, v0
	v_mov_b32_e32 v32, v0
	v_mov_b32_e32 v33, v0
	v_mov_b32_e32 v34, v0
	v_mov_b32_e32 v35, v0
	v_mov_b32_e32 v60, v0
	v_mov_b32_e32 v61, v0
	v_mov_b32_e32 v62, v0
	v_mov_b32_e32 v63, v0
	v_mov_b32_e32 v40, v0
	v_mov_b32_e32 v41, v0
	v_mov_b32_e32 v42, v0
	v_mov_b32_e32 v43, v0
	v_mov_b32_e32 v76, v0
	v_mov_b32_e32 v77, v0
	v_mov_b32_e32 v78, v0
	v_mov_b32_e32 v79, v0
	v_mov_b32_e32 v48, v0
	v_mov_b32_e32 v49, v0
	v_mov_b32_e32 v50, v0
	v_mov_b32_e32 v51, v0
	v_mov_b32_e32 v84, v0
	v_mov_b32_e32 v85, v0
	v_mov_b32_e32 v86, v0
	v_mov_b32_e32 v87, v0
	v_mov_b32_e32 v64, v0
	v_mov_b32_e32 v65, v0
	v_mov_b32_e32 v66, v0
	v_mov_b32_e32 v67, v0
	v_mov_b32_e32 v92, v0
	v_mov_b32_e32 v93, v0
	v_mov_b32_e32 v94, v0
	v_mov_b32_e32 v95, v0
	v_mov_b32_e32 v98, v0
	v_mov_b32_e32 v99, v0
	v_mov_b32_e32 v100, v0
	v_mov_b32_e32 v101, v0
	v_mov_b32_e32 v110, v0
	v_mov_b32_e32 v111, v0
	v_mov_b32_e32 v112, v0
	v_mov_b32_e32 v113, v0
	v_mov_b32_e32 v102, v0
	v_mov_b32_e32 v103, v0
	v_mov_b32_e32 v104, v0
	v_mov_b32_e32 v105, v0
	v_mov_b32_e32 v118, v0
	v_mov_b32_e32 v119, v0
	v_mov_b32_e32 v120, v0
	v_mov_b32_e32 v121, v0
	v_mov_b32_e32 v106, v0
	v_mov_b32_e32 v107, v0
	v_mov_b32_e32 v108, v0
	v_mov_b32_e32 v109, v0
	v_mov_b32_e32 v122, v0
	v_mov_b32_e32 v123, v0
	v_mov_b32_e32 v124, v0
	v_mov_b32_e32 v125, v0
	v_mov_b32_e32 v114, v0
	v_mov_b32_e32 v115, v0
	v_mov_b32_e32 v116, v0
	v_mov_b32_e32 v117, v0
	v_mov_b32_e32 v126, v0
	v_mov_b32_e32 v127, v0
	v_mov_b32_e32 v128, v0
	v_mov_b32_e32 v129, v0
	ds_read_b128 v[220:223], v132
	ds_read_b128 v[224:227], v132 offset:1024
	ds_read_b128 v[228:231], v132 offset:2048
	ds_read_b128 v[232:235], v132 offset:3072
.LBB0_1639:
	s_add_i32 s10, s41, 0xfff80080
	s_cmp_eq_u32 s43, 28
	s_cselect_b32 s46, s39, s10
	s_cselect_b32 s44, s40, s42
	s_or_b32 s45, s46, 0x80
	s_mov_b32 m0, s35
	ds_read_b128 v[150:153], v133
	ds_read_b128 v[154:157], v133 offset:1024
	ds_read_b128 v[158:161], v133 offset:2048
	ds_read_b128 v[162:165], v133 offset:3072
	ds_read_b128 v[166:169], v133 offset:4096
	ds_read_b128 v[170:173], v133 offset:5120
	ds_read_b128 v[174:177], v133 offset:6144
	ds_read_b128 v[178:181], v133 offset:7168
	buffer_load_dwordx4 v130, s[72:75], s41 offen lds
	s_mov_b32 m0, s36
	s_nop 0
	buffer_load_dwordx4 v131, s[72:75], s41 offen lds
	s_waitcnt lgkmcnt(8)
	s_waitcnt vmcnt(10)
	s_barrier
	s_waitcnt lgkmcnt(0)
	s_setprio 1
	s_waitcnt lgkmcnt(7)
	v_mfma_f32_16x16x32_bf16 v[126:129], v[150:153], v[220:223], v[126:129]
	v_mfma_f32_16x16x32_bf16 v[114:117], v[150:153], v[228:231], v[114:117]
	s_waitcnt lgkmcnt(5)
	v_mfma_f32_16x16x32_bf16 v[122:125], v[158:161], v[220:223], v[122:125]
	v_mfma_f32_16x16x32_bf16 v[106:109], v[158:161], v[228:231], v[106:109]
	s_waitcnt lgkmcnt(3)
	v_mfma_f32_16x16x32_bf16 v[118:121], v[166:169], v[220:223], v[118:121]
	v_mfma_f32_16x16x32_bf16 v[102:105], v[166:169], v[228:231], v[102:105]
	s_waitcnt lgkmcnt(1)
	v_mfma_f32_16x16x32_bf16 v[110:113], v[174:177], v[220:223], v[110:113]
	v_mfma_f32_16x16x32_bf16 v[98:101], v[174:177], v[228:231], v[98:101]
	v_mfma_f32_16x16x32_bf16 v[126:129], v[154:157], v[224:227], v[126:129]
	v_mfma_f32_16x16x32_bf16 v[114:117], v[154:157], v[232:235], v[114:117]
	v_mfma_f32_16x16x32_bf16 v[122:125], v[162:165], v[224:227], v[122:125]
	v_mfma_f32_16x16x32_bf16 v[106:109], v[162:165], v[232:235], v[106:109]
	v_mfma_f32_16x16x32_bf16 v[118:121], v[170:173], v[224:227], v[118:121]
	v_mfma_f32_16x16x32_bf16 v[102:105], v[170:173], v[232:235], v[102:105]
	s_waitcnt lgkmcnt(0)
	v_mfma_f32_16x16x32_bf16 v[110:113], v[178:181], v[224:227], v[110:113]
	v_mfma_f32_16x16x32_bf16 v[98:101], v[178:181], v[232:235], v[98:101]
	s_setprio 0
	s_barrier
	s_mov_b32 s10, s74
	s_mov_b32 s11, s75
	s_mov_b32 m0, s19
	ds_read_b128 v[182:185], v132 offset:16384
	ds_read_b128 v[186:189], v132 offset:17408
	ds_read_b128 v[190:193], v132 offset:18432
	ds_read_b128 v[194:197], v132 offset:19456
	buffer_load_dwordx4 v130, s[8:11], s44 offen lds
	s_mov_b32 m0, s20
	s_nop 0
	buffer_load_dwordx4 v131, s[8:11], s44 offen lds
	s_waitcnt vmcnt(10)
	s_barrier
	s_waitcnt lgkmcnt(0)
	s_setprio 1
	s_waitcnt lgkmcnt(3)
	v_mfma_f32_16x16x32_bf16 v[92:95], v[150:153], v[182:185], v[92:95]
	s_waitcnt lgkmcnt(1)
	v_mfma_f32_16x16x32_bf16 v[64:67], v[150:153], v[190:193], v[64:67]
	v_mfma_f32_16x16x32_bf16 v[84:87], v[158:161], v[182:185], v[84:87]
	v_mfma_f32_16x16x32_bf16 v[48:51], v[158:161], v[190:193], v[48:51]
	v_mfma_f32_16x16x32_bf16 v[76:79], v[166:169], v[182:185], v[76:79]
	v_mfma_f32_16x16x32_bf16 v[40:43], v[166:169], v[190:193], v[40:43]
	v_mfma_f32_16x16x32_bf16 v[60:63], v[174:177], v[182:185], v[60:63]
	v_mfma_f32_16x16x32_bf16 v[32:35], v[174:177], v[190:193], v[32:35]
	v_mfma_f32_16x16x32_bf16 v[92:95], v[154:157], v[186:189], v[92:95]
	s_waitcnt lgkmcnt(0)
	v_mfma_f32_16x16x32_bf16 v[64:67], v[154:157], v[194:197], v[64:67]
	v_mfma_f32_16x16x32_bf16 v[84:87], v[162:165], v[186:189], v[84:87]
	v_mfma_f32_16x16x32_bf16 v[48:51], v[162:165], v[194:197], v[48:51]
	v_mfma_f32_16x16x32_bf16 v[76:79], v[170:173], v[186:189], v[76:79]
	v_mfma_f32_16x16x32_bf16 v[40:43], v[170:173], v[194:197], v[40:43]
	v_mfma_f32_16x16x32_bf16 v[60:63], v[178:181], v[186:189], v[60:63]
	v_mfma_f32_16x16x32_bf16 v[32:35], v[178:181], v[194:197], v[32:35]
	s_setprio 0
	s_mov_b32 m0, s2
	s_barrier
	ds_read_b128 v[150:153], v133 offset:16384
	ds_read_b128 v[154:157], v133 offset:17408
	ds_read_b128 v[158:161], v133 offset:18432
	ds_read_b128 v[162:165], v133 offset:19456
	ds_read_b128 v[166:169], v133 offset:20480
	ds_read_b128 v[170:173], v133 offset:21504
	ds_read_b128 v[174:177], v133 offset:22528
	ds_read_b128 v[178:181], v133 offset:23552
	buffer_load_dwordx4 v130, s[72:75], s46 offen lds
	s_mov_b32 m0, s21
	s_nop 0
	buffer_load_dwordx4 v131, s[72:75], s46 offen lds
	s_waitcnt vmcnt(10)
	s_barrier
	s_waitcnt lgkmcnt(0)
	s_setprio 1
	s_waitcnt lgkmcnt(7)
	v_mfma_f32_16x16x32_bf16 v[88:91], v[150:153], v[220:223], v[88:91]
	v_mfma_f32_16x16x32_bf16 v[72:75], v[150:153], v[228:231], v[72:75]
	s_waitcnt lgkmcnt(5)
	v_mfma_f32_16x16x32_bf16 v[80:83], v[158:161], v[220:223], v[80:83]
	v_mfma_f32_16x16x32_bf16 v[56:59], v[158:161], v[228:231], v[56:59]
	s_waitcnt lgkmcnt(3)
	v_mfma_f32_16x16x32_bf16 v[68:71], v[166:169], v[220:223], v[68:71]
	v_mfma_f32_16x16x32_bf16 v[44:47], v[166:169], v[228:231], v[44:47]
	s_waitcnt lgkmcnt(1)
	v_mfma_f32_16x16x32_bf16 v[52:55], v[174:177], v[220:223], v[52:55]
	v_mfma_f32_16x16x32_bf16 v[36:39], v[174:177], v[228:231], v[36:39]
	v_mfma_f32_16x16x32_bf16 v[88:91], v[154:157], v[224:227], v[88:91]
	v_mfma_f32_16x16x32_bf16 v[72:75], v[154:157], v[232:235], v[72:75]
	v_mfma_f32_16x16x32_bf16 v[80:83], v[162:165], v[224:227], v[80:83]
	v_mfma_f32_16x16x32_bf16 v[56:59], v[162:165], v[232:235], v[56:59]
	v_mfma_f32_16x16x32_bf16 v[68:71], v[170:173], v[224:227], v[68:71]
	v_mfma_f32_16x16x32_bf16 v[44:47], v[170:173], v[232:235], v[44:47]
	s_waitcnt lgkmcnt(0)
	v_mfma_f32_16x16x32_bf16 v[52:55], v[178:181], v[224:227], v[52:55]
	v_mfma_f32_16x16x32_bf16 v[36:39], v[178:181], v[232:235], v[36:39]
	s_setprio 0
	s_barrier
	ds_read_b128 v[220:223], v132 offset:32768
	ds_read_b128 v[224:227], v132 offset:33792
	ds_read_b128 v[228:231], v132 offset:34816
	ds_read_b128 v[232:235], v132 offset:35840
	s_add_i32 s47, s44, 0x80000
	s_mov_b32 m0, s22
	s_nop 0
	buffer_load_dwordx4 v130, s[8:11], s47 offen lds
	s_mov_b32 m0, s23
	s_nop 0
	buffer_load_dwordx4 v131, s[8:11], s47 offen lds
	s_waitcnt vmcnt(10)
	s_barrier
	s_setprio 1
	v_mfma_f32_16x16x32_bf16 v[28:31], v[150:153], v[182:185], v[28:31]
	v_mfma_f32_16x16x32_bf16 v[16:19], v[150:153], v[190:193], v[16:19]
	v_mfma_f32_16x16x32_bf16 v[24:27], v[158:161], v[182:185], v[24:27]
	v_mfma_f32_16x16x32_bf16 v[8:11], v[158:161], v[190:193], v[8:11]
	v_mfma_f32_16x16x32_bf16 v[20:23], v[166:169], v[182:185], v[20:23]
	v_mfma_f32_16x16x32_bf16 v[4:7], v[166:169], v[190:193], v[4:7]
	v_mfma_f32_16x16x32_bf16 v[12:15], v[174:177], v[182:185], v[12:15]
	v_mfma_f32_16x16x32_bf16 v[0:3], v[174:177], v[190:193], v[0:3]
	v_mfma_f32_16x16x32_bf16 v[28:31], v[154:157], v[186:189], v[28:31]
	v_mfma_f32_16x16x32_bf16 v[16:19], v[154:157], v[194:197], v[16:19]
	v_mfma_f32_16x16x32_bf16 v[24:27], v[162:165], v[186:189], v[24:27]
	v_mfma_f32_16x16x32_bf16 v[8:11], v[162:165], v[194:197], v[8:11]
	v_mfma_f32_16x16x32_bf16 v[20:23], v[170:173], v[186:189], v[20:23]
	v_mfma_f32_16x16x32_bf16 v[4:7], v[170:173], v[194:197], v[4:7]
	v_mfma_f32_16x16x32_bf16 v[12:15], v[178:181], v[186:189], v[12:15]
	v_mfma_f32_16x16x32_bf16 v[0:3], v[178:181], v[194:197], v[0:3]
	s_setprio 0
	s_barrier
	s_add_i32 s46, s46, 0x80000
	s_mov_b32 m0, s24
	ds_read_b128 v[150:153], v133 offset:32768
	ds_read_b128 v[154:157], v133 offset:33792
	ds_read_b128 v[158:161], v133 offset:34816
	ds_read_b128 v[162:165], v133 offset:35840
	ds_read_b128 v[166:169], v133 offset:36864
	ds_read_b128 v[170:173], v133 offset:37888
	ds_read_b128 v[174:177], v133 offset:38912
	ds_read_b128 v[178:181], v133 offset:39936
	buffer_load_dwordx4 v130, s[72:75], s46 offen lds
	s_mov_b32 m0, s25
	s_nop 0
	buffer_load_dwordx4 v131, s[72:75], s46 offen lds
	s_waitcnt lgkmcnt(8)
	s_waitcnt vmcnt(10)
	s_barrier
	s_waitcnt lgkmcnt(0)
	s_setprio 1
	s_waitcnt lgkmcnt(7)
	v_mfma_f32_16x16x32_bf16 v[126:129], v[150:153], v[220:223], v[126:129]
	v_mfma_f32_16x16x32_bf16 v[114:117], v[150:153], v[228:231], v[114:117]
	s_waitcnt lgkmcnt(5)
	v_mfma_f32_16x16x32_bf16 v[122:125], v[158:161], v[220:223], v[122:125]
	v_mfma_f32_16x16x32_bf16 v[106:109], v[158:161], v[228:231], v[106:109]
	s_waitcnt lgkmcnt(3)
	v_mfma_f32_16x16x32_bf16 v[118:121], v[166:169], v[220:223], v[118:121]
	v_mfma_f32_16x16x32_bf16 v[102:105], v[166:169], v[228:231], v[102:105]
	s_waitcnt lgkmcnt(1)
	v_mfma_f32_16x16x32_bf16 v[110:113], v[174:177], v[220:223], v[110:113]
	v_mfma_f32_16x16x32_bf16 v[98:101], v[174:177], v[228:231], v[98:101]
	v_mfma_f32_16x16x32_bf16 v[126:129], v[154:157], v[224:227], v[126:129]
	v_mfma_f32_16x16x32_bf16 v[114:117], v[154:157], v[232:235], v[114:117]
	v_mfma_f32_16x16x32_bf16 v[122:125], v[162:165], v[224:227], v[122:125]
	v_mfma_f32_16x16x32_bf16 v[106:109], v[162:165], v[232:235], v[106:109]
	v_mfma_f32_16x16x32_bf16 v[118:121], v[170:173], v[224:227], v[118:121]
	v_mfma_f32_16x16x32_bf16 v[102:105], v[170:173], v[232:235], v[102:105]
	s_waitcnt lgkmcnt(0)
	v_mfma_f32_16x16x32_bf16 v[110:113], v[178:181], v[224:227], v[110:113]
	v_mfma_f32_16x16x32_bf16 v[98:101], v[178:181], v[232:235], v[98:101]
	s_setprio 0
	s_barrier
	s_or_b32 s46, s44, 0x80
	s_mov_b32 m0, s26
	ds_read_b128 v[182:185], v132 offset:49152
	ds_read_b128 v[186:189], v132 offset:50176
	ds_read_b128 v[190:193], v132 offset:51200
	ds_read_b128 v[194:197], v132 offset:52224
	buffer_load_dwordx4 v130, s[8:11], s46 offen lds
	s_mov_b32 m0, s27
	s_nop 0
	buffer_load_dwordx4 v131, s[8:11], s46 offen lds
	s_waitcnt vmcnt(10)
	s_barrier
	s_waitcnt lgkmcnt(0)
	s_setprio 1
	s_waitcnt lgkmcnt(3)
	v_mfma_f32_16x16x32_bf16 v[92:95], v[150:153], v[182:185], v[92:95]
	s_waitcnt lgkmcnt(1)
	v_mfma_f32_16x16x32_bf16 v[64:67], v[150:153], v[190:193], v[64:67]
	v_mfma_f32_16x16x32_bf16 v[84:87], v[158:161], v[182:185], v[84:87]
	v_mfma_f32_16x16x32_bf16 v[48:51], v[158:161], v[190:193], v[48:51]
	v_mfma_f32_16x16x32_bf16 v[76:79], v[166:169], v[182:185], v[76:79]
	v_mfma_f32_16x16x32_bf16 v[40:43], v[166:169], v[190:193], v[40:43]
	v_mfma_f32_16x16x32_bf16 v[60:63], v[174:177], v[182:185], v[60:63]
	v_mfma_f32_16x16x32_bf16 v[32:35], v[174:177], v[190:193], v[32:35]
	v_mfma_f32_16x16x32_bf16 v[92:95], v[154:157], v[186:189], v[92:95]
	s_waitcnt lgkmcnt(0)
	v_mfma_f32_16x16x32_bf16 v[64:67], v[154:157], v[194:197], v[64:67]
	v_mfma_f32_16x16x32_bf16 v[84:87], v[162:165], v[186:189], v[84:87]
	v_mfma_f32_16x16x32_bf16 v[48:51], v[162:165], v[194:197], v[48:51]
	v_mfma_f32_16x16x32_bf16 v[76:79], v[170:173], v[186:189], v[76:79]
	v_mfma_f32_16x16x32_bf16 v[40:43], v[170:173], v[194:197], v[40:43]
	v_mfma_f32_16x16x32_bf16 v[60:63], v[178:181], v[186:189], v[60:63]
	v_mfma_f32_16x16x32_bf16 v[32:35], v[178:181], v[194:197], v[32:35]
	s_setprio 0
	s_mov_b32 m0, s28
	s_barrier
	ds_read_b128 v[150:153], v133 offset:49152
	ds_read_b128 v[154:157], v133 offset:50176
	ds_read_b128 v[158:161], v133 offset:51200
	ds_read_b128 v[162:165], v133 offset:52224
	ds_read_b128 v[166:169], v133 offset:53248
	ds_read_b128 v[170:173], v133 offset:54272
	ds_read_b128 v[174:177], v133 offset:55296
	ds_read_b128 v[178:181], v133 offset:56320
	buffer_load_dwordx4 v130, s[72:75], s45 offen lds
	s_mov_b32 m0, s29
	s_nop 0
	buffer_load_dwordx4 v131, s[72:75], s45 offen lds
	s_waitcnt vmcnt(10)
	s_barrier
	s_waitcnt lgkmcnt(0)
	s_setprio 1
	s_waitcnt lgkmcnt(7)
	v_mfma_f32_16x16x32_bf16 v[88:91], v[150:153], v[220:223], v[88:91]
	v_mfma_f32_16x16x32_bf16 v[72:75], v[150:153], v[228:231], v[72:75]
	s_waitcnt lgkmcnt(5)
	v_mfma_f32_16x16x32_bf16 v[80:83], v[158:161], v[220:223], v[80:83]
	v_mfma_f32_16x16x32_bf16 v[56:59], v[158:161], v[228:231], v[56:59]
	s_waitcnt lgkmcnt(3)
	v_mfma_f32_16x16x32_bf16 v[68:71], v[166:169], v[220:223], v[68:71]
	v_mfma_f32_16x16x32_bf16 v[44:47], v[166:169], v[228:231], v[44:47]
	s_waitcnt lgkmcnt(1)
	v_mfma_f32_16x16x32_bf16 v[52:55], v[174:177], v[220:223], v[52:55]
	v_mfma_f32_16x16x32_bf16 v[36:39], v[174:177], v[228:231], v[36:39]
	v_mfma_f32_16x16x32_bf16 v[88:91], v[154:157], v[224:227], v[88:91]
	v_mfma_f32_16x16x32_bf16 v[72:75], v[154:157], v[232:235], v[72:75]
	v_mfma_f32_16x16x32_bf16 v[80:83], v[162:165], v[224:227], v[80:83]
	v_mfma_f32_16x16x32_bf16 v[56:59], v[162:165], v[232:235], v[56:59]
	v_mfma_f32_16x16x32_bf16 v[68:71], v[170:173], v[224:227], v[68:71]
	v_mfma_f32_16x16x32_bf16 v[44:47], v[170:173], v[232:235], v[44:47]
	s_waitcnt lgkmcnt(0)
	v_mfma_f32_16x16x32_bf16 v[52:55], v[178:181], v[224:227], v[52:55]
	v_mfma_f32_16x16x32_bf16 v[36:39], v[178:181], v[232:235], v[36:39]
	s_setprio 0
	s_barrier
	ds_read_b128 v[220:223], v132
	ds_read_b128 v[224:227], v132 offset:1024
	ds_read_b128 v[228:231], v132 offset:2048
	ds_read_b128 v[232:235], v132 offset:3072
	s_add_i32 s44, s44, 0x80080
	s_mov_b32 m0, s30
	s_nop 0
	buffer_load_dwordx4 v130, s[8:11], s44 offen lds
	s_mov_b32 m0, s31
	s_nop 0
	buffer_load_dwordx4 v131, s[8:11], s44 offen lds
	s_waitcnt vmcnt(10)
	s_barrier
	s_setprio 1
	v_mfma_f32_16x16x32_bf16 v[28:31], v[150:153], v[182:185], v[28:31]
	v_mfma_f32_16x16x32_bf16 v[16:19], v[150:153], v[190:193], v[16:19]
	v_mfma_f32_16x16x32_bf16 v[24:27], v[158:161], v[182:185], v[24:27]
	v_mfma_f32_16x16x32_bf16 v[8:11], v[158:161], v[190:193], v[8:11]
	v_mfma_f32_16x16x32_bf16 v[20:23], v[166:169], v[182:185], v[20:23]
	v_mfma_f32_16x16x32_bf16 v[4:7], v[166:169], v[190:193], v[4:7]
	v_mfma_f32_16x16x32_bf16 v[12:15], v[174:177], v[182:185], v[12:15]
	v_mfma_f32_16x16x32_bf16 v[0:3], v[174:177], v[190:193], v[0:3]
	v_mfma_f32_16x16x32_bf16 v[28:31], v[154:157], v[186:189], v[28:31]
	v_mfma_f32_16x16x32_bf16 v[16:19], v[154:157], v[194:197], v[16:19]
	v_mfma_f32_16x16x32_bf16 v[24:27], v[162:165], v[186:189], v[24:27]
	v_mfma_f32_16x16x32_bf16 v[8:11], v[162:165], v[194:197], v[8:11]
	v_mfma_f32_16x16x32_bf16 v[20:23], v[170:173], v[186:189], v[20:23]
	v_mfma_f32_16x16x32_bf16 v[4:7], v[170:173], v[194:197], v[4:7]
	v_mfma_f32_16x16x32_bf16 v[12:15], v[178:181], v[186:189], v[12:15]
	v_mfma_f32_16x16x32_bf16 v[0:3], v[178:181], v[194:197], v[0:3]
	s_setprio 0
	s_add_i32 s43, s43, 2
	s_addk_i32 s41, 0x100
	s_addk_i32 s42, 0x100
	s_cmp_gt_u32 s43, 29
	s_barrier
	s_cbranch_scc0 .LBB0_1639
	s_waitcnt lgkmcnt(0)
	s_getreg_b32 s10, hwreg(HW_REG_HW_ID, 0, 6)
	s_and_b32 s10, s10, 63
	s_lshl_b32 s10, s10, 2
	s_add_i32 s10, s10, 0
	s_add_i32 s10, s10, 0x20010
	v_mov_b32_e32 v96, s10
	ds_read_b32 v96, v96
	s_mul_i32 s10, s34, 0x120
	s_lshl_b32 s11, s37, 2
	v_mbcnt_lo_u32_b32 v136, -1, 0
	v_mbcnt_hi_u32_b32 v136, -1, v136
	s_add_i32 s11, s11, s10
	s_waitcnt lgkmcnt(0)
	v_readfirstlane_b32 s34, v96
	v_and_b32_e32 v137, 15, v136
	s_mov_b32 s10, 0x21000
	v_lshl_or_b32 v96, s34, 6, v136
	v_ashrrev_i32_e32 v134, 8, v96
	v_add_u32_e32 v134, s11, v134
	v_ashrrev_i32_e32 v135, 31, v134
	v_lshrrev_b32_e32 v96, 1, v96
	v_lshlrev_b64 v[134:135], 8, v[134:135]
	v_and_b32_e32 v96, 0x60, v96
	v_or3_b32 v134, v134, v96, v137
	v_lshlrev_b64 v[134:135], 8, v[134:135]
	v_lshl_add_u64 v[134:135], s[12:13], 0, v[134:135]
	v_and_b32_e32 v96, 48, v136
	v_lshl_add_u64 v[134:135], v[134:135], 0, v[96:97]
	global_store_dwordx4 v[134:135], v[126:129], off
	global_store_dwordx4 v[134:135], v[122:125], off offset:64
	global_store_dwordx4 v[134:135], v[118:121], off offset:128
	global_store_dwordx4 v[134:135], v[110:113], off offset:192
	s_mov_b32 s34, s14
	s_mov_b32 s37, s15
	v_add_co_u32_e32 v110, vcc, s75, v134
	s_mov_b32 s42, s17
	s_nop 0
	v_addc_co_u32_e32 v111, vcc, 0, v135, vcc
	v_add_co_u32_e32 v112, vcc, s10, v134
	s_mov_b64 s[10:11], 0x1000
	s_nop 0
	v_addc_co_u32_e32 v113, vcc, 0, v135, vcc
	global_store_dwordx4 v[112:113], v[88:91], off offset:-4096
	global_store_dwordx4 v[110:111], v[80:83], off offset:64
	global_store_dwordx4 v[110:111], v[68:71], off offset:128
	global_store_dwordx4 v[110:111], v[52:55], off offset:192
	s_mov_b32 s41, s16
	s_nop 0
	v_add_co_u32_e32 v54, vcc, s63, v134
	v_lshl_add_u64 v[52:53], v[134:135], 0, s[10:11]
	s_nop 0
	v_addc_co_u32_e32 v55, vcc, 0, v135, vcc
	s_mov_b64 s[10:11], 0x8000
	global_store_dwordx4 v[54:55], v[114:117], off
	global_store_dwordx4 v[52:53], v[106:109], off offset:64
	global_store_dwordx4 v[52:53], v[102:105], off offset:128
	global_store_dwordx4 v[52:53], v[98:101], off offset:192
	global_store_dwordx4 v[112:113], v[72:75], off
	global_store_dwordx4 v[112:113], v[56:59], off offset:64
	global_store_dwordx4 v[112:113], v[44:47], off offset:128
	global_store_dwordx4 v[112:113], v[36:39], off offset:192
	s_nop 1
	v_lshl_add_u64 v[36:37], v[134:135], 0, s[10:11]
	s_mov_b32 s10, 0x8000
	v_add_co_u32_e32 v38, vcc, s10, v134
	s_mov_b32 s10, 0x28000
	s_nop 0
	v_addc_co_u32_e32 v39, vcc, 0, v135, vcc
	global_store_dwordx4 v[38:39], v[92:95], off
	global_store_dwordx4 v[36:37], v[84:87], off offset:64
	global_store_dwordx4 v[36:37], v[76:79], off offset:128
	global_store_dwordx4 v[36:37], v[60:63], off offset:192
	v_add_co_u32_e32 v36, vcc, s10, v134
	s_mov_b64 s[10:11], 0x9000
	s_nop 0
	v_addc_co_u32_e32 v37, vcc, 0, v135, vcc
	global_store_dwordx4 v[36:37], v[28:31], off
	global_store_dwordx4 v[36:37], v[24:27], off offset:64
	global_store_dwordx4 v[36:37], v[20:23], off offset:128
	global_store_dwordx4 v[36:37], v[12:15], off offset:192
	s_nop 1
	v_add_co_u32_e32 v14, vcc, 0x9000, v134
	v_lshl_add_u64 v[12:13], v[134:135], 0, s[10:11]
	s_nop 0
	v_addc_co_u32_e32 v15, vcc, 0, v135, vcc
	global_store_dwordx4 v[14:15], v[64:67], off
	global_store_dwordx4 v[12:13], v[48:51], off offset:64
	global_store_dwordx4 v[12:13], v[40:43], off offset:128
	global_store_dwordx4 v[12:13], v[32:35], off offset:192
	v_add_co_u32_e32 v12, vcc, 0x29000, v134
	s_nop 1
	v_addc_co_u32_e32 v13, vcc, 0, v135, vcc
	s_and_b64 vcc, exec, s[4:5]
	global_store_dwordx4 v[12:13], v[16:19], off
	global_store_dwordx4 v[12:13], v[8:11], off offset:64
	global_store_dwordx4 v[12:13], v[4:7], off offset:128
	global_store_dwordx4 v[12:13], v[0:3], off offset:192
	s_cbranch_vccz .LBB0_1633
	s_branch .LBB0_1642
